# converter copies: LDS read chain de-serialised (32 reads issued then one wait); conversions rebalanced across the three GEMM tails; P0 skipped for layers 1-3
# baseline (speedup 1.0000x reference)
; #define LAS __attribute__((address_space(3)))
; __global__ void __launch_bounds__(NWAVES * 64, 2) mk_fwd(Args args) {
;     ...
;             PH_LOCALS
;             LAS float* scr = (LAS float*)(lds + RING_OFF + wave * 16640);   static_assert(8 * 16640 <= LDSCTL_OFF, "converter scratch below the LDS control words");
;             constexpr int I_UP = (D / 64) * (NUP / 64), I_DN = (DFF / 64) * (D / 64), I_IN = (D / 64) * (DINP / 64), I_GLU = 16 * 16, I_L = 4 * 16, I_V1 = 16 * 4, I_V2 = 4 * 16,
;                           I_BS5 = 16 * 32, I_BAT = 8 * 32, I_BRW = 16 * 32, I_OUT = 32 * 32;
;             constexpr int NITEMS = 2 * I_UP + 2 * I_DN + I_IN + I_GLU + 3 * I_L + I_V1 + I_V2 + I_BS5 + I_BAT + I_BRW + I_OUT;
;             const int lv = l > 0 ? l - 1 : 0;
;     ...
;             for (int it = gw; it < NITEMS; it += NGW) {
;                 ConvItem ca; CONV_DESC(ca, it);
.Lmy_p0_second:
	v_readlane_b32 s0, v254, 8
	v_readlane_b32 s4, v254, 10
	v_readlane_b32 s1, v254, 9
	v_mbcnt_lo_u32_b32 v11, -1, 0
	v_mbcnt_hi_u32_b32 v11, -1, v11
	s_load_dword s6, s[0:1], 0x0
	s_mov_b32 s3, s84
	s_waitcnt lgkmcnt(0)
	s_movk_i32 s6, 256
	s_lshl_b32 s3, s3, 3
	v_readlane_b32 s0, v254, 0
	s_add_i32 s3, s3, s4
	s_add_i32 s3, s3, 0x6280
	v_readlane_b32 s1, v254, 1
	s_cmpk_gt_i32 s3, 27071
	s_cbranch_scc1 .Lcvp0b_ret
	s_load_dwordx2 s[8:9], s[0:1], 0x138
	v_readlane_b32 s14, v254, 38
	s_mulk_i32 s4, 0x4100
	s_add_i32 s7, s4, 0
	v_sub_u32_e64 v0, s14, 1 clamp
	s_lshl_b32 s33, s6, 3
	v_readfirstlane_b32 s4, v0
	s_lshl_b32 s96, s4, 16
	s_waitcnt lgkmcnt(0)
	s_add_u32 s4, s8, 0x22800000
	s_addc_u32 s5, s9, 0
	v_writelane_b32 v254, s4, 39
	s_mov_b32 s15, s97
	v_and_b32_e32 v0, 7, v11
	v_writelane_b32 v254, s5, 40
	s_add_u32 s4, s8, 0x22780000
	s_addc_u32 s5, s9, 0
	v_writelane_b32 v254, s4, 41
	v_ashrrev_i32_e32 v13, 3, v11
	v_lshlrev_b32_e32 v10, 3, v0
	v_writelane_b32 v254, s5, 42
	s_lshl_b32 s4, s14, 18
	s_add_u32 s10, s8, 0x22700000
	s_addc_u32 s11, s9, 0
	v_writelane_b32 v254, s10, 43
	s_mov_b32 s5, s97
	v_mul_u32_u24_e32 v0, 0x820, v0
	v_writelane_b32 v254, s11, 44
	s_mul_i32 s10, s14, 0x18000
	s_mov_b32 s11, s97
	v_writelane_b32 v254, s10, 45
	v_lshlrev_b32_e32 v1, 2, v13
	v_lshl_add_u32 v12, v11, 2, s7
	v_writelane_b32 v254, s11, 46
	s_add_u32 s10, s8, 0x22680000
	s_addc_u32 s11, s9, 0
	v_writelane_b32 v254, s10, 47
	v_add3_u32 v14, s7, v0, v1
	s_mov_b32 s41, s97
	v_writelane_b32 v254, s11, 48
	s_add_u32 s10, s8, 0x22600000
	s_addc_u32 s11, s9, 0
	v_writelane_b32 v254, s10, 49
	s_nop 1
	v_writelane_b32 v254, s11, 50
	s_lshl_b32 s10, s14, 20
	s_mov_b32 s11, s97
	v_writelane_b32 v254, s10, 51
	s_nop 1
	v_writelane_b32 v254, s11, 52
	s_add_u32 s10, s8, 0x22400000
	s_addc_u32 s11, s9, 0
	v_writelane_b32 v254, s10, 53
	s_nop 1
	v_writelane_b32 v254, s11, 54
	s_lshl_b32 s10, s14, 21
	s_mov_b32 s11, s97
	v_writelane_b32 v254, s10, 55
	s_nop 1
	v_writelane_b32 v254, s11, 56
	s_add_u32 s10, s8, 0x22e80000
	s_addc_u32 s11, s9, 0
	v_writelane_b32 v254, s10, 57
	s_nop 1
	v_writelane_b32 v254, s11, 58
	s_add_u32 s10, s8, 0x27b80000
	s_addc_u32 s11, s9, 0
	v_writelane_b32 v254, s10, 59
	s_nop 1
	v_writelane_b32 v254, s11, 60
	s_add_u32 s10, s8, 0x22880000
	s_addc_u32 s11, s9, 0
	v_writelane_b32 v254, s10, 61
	s_nop 1
	v_writelane_b32 v254, s11, 62
	s_lshl_b32 s10, s14, 22
	s_add_u32 s12, s8, 0x23280000
	s_addc_u32 s13, s9, 0
	v_writelane_b32 v254, s12, 63
	s_mov_b32 s11, s97
	s_nop 0
	v_writelane_b32 v255, s13, 0
	s_mul_i32 s12, s14, 0xac0000
	s_mov_b32 s13, s97
	v_writelane_b32 v255, s12, 1
	s_nop 1
	v_writelane_b32 v255, s13, 2
	s_add_u32 s12, s8, 0x26580000
	s_addc_u32 s13, s9, 0
	v_writelane_b32 v255, s12, 3
	s_nop 1
	v_writelane_b32 v255, s13, 4
	s_add_u32 s12, s8, 0x1d200000
	s_addc_u32 s13, s9, 0
	s_lshl_b32 s40, s14, 11
	v_writelane_b32 v255, s12, 5
	s_add_u32 s16, s8, 0x1e800000
	s_addc_u32 s17, s9, 0
	v_writelane_b32 v255, s13, 6
	v_writelane_b32 v255, s16, 7
	s_mul_i32 s12, s14, 0x1de0000
	s_mul_i32 s14, s14, 0x1580000
	v_writelane_b32 v255, s17, 8
	v_writelane_b32 v255, s14, 9
	s_mov_b32 s13, s97
	s_nop 0
	v_writelane_b32 v255, s15, 10
	s_add_u32 s14, s8, 0x23a80000
	s_addc_u32 s15, s9, 0
	v_writelane_b32 v255, s14, 11
	s_add_u32 s8, s8, 0x1a700000
	s_addc_u32 s9, s9, 0
	v_writelane_b32 v255, s15, 12
	v_writelane_b32 v255, s8, 13
	s_lshl_b64 s[4:5], s[4:5], 2
	s_lshl_b32 s7, s3, 4
	v_writelane_b32 v255, s9, 14
	v_writelane_b32 v255, s4, 15
	s_add_i32 s72, s7, 0xc00
	s_lshl_b32 s7, s3, 1
	v_writelane_b32 v255, s5, 16
	s_lshl_b64 s[4:5], s[10:11], 2
	v_writelane_b32 v255, s4, 17
	s_lshl_b32 s66, s3, 6
	s_lshl_b32 s67, s6, 9
	v_writelane_b32 v255, s5, 18
	s_lshl_b64 s[4:5], s[12:13], 2
	v_writelane_b32 v255, s4, 19
	s_lshl_b32 s68, s3, 5
	s_lshl_b32 s69, s6, 8
	v_writelane_b32 v255, s5, 20
	v_writelane_b32 v255, s80, 21
	s_lshl_b32 s70, s3, 2
	s_lshl_b32 s71, s6, 5
	v_writelane_b32 v255, s81, 22
	v_writelane_b32 v255, s82, 23
	s_lshl_b32 s73, s6, 7
	s_add_i32 s74, s7, 0x13500
	s_lshl_b32 s75, s6, 4
	v_writelane_b32 v255, s83, 24
	s_branch .Lcvp0b_31

; #define LAS __attribute__((address_space(3)))
; __device__ __forceinline__ void conv_load(const ConvItem& ci, int lane, float (&v)[64]) {
;     ...
;     for (int i = 0; i < 64; ++i) { const int k = ci.k0 + i, kk = k < kmax ? k : kmax; v[i] = __builtin_nontemporal_load(base + (size_t)kk * ci.ldw); }
; #pragma unroll
;     for (int i = 0; i < 64; ++i) v[i] = (okc && (ci.k0 + i) < ci.Ksrc) ? v[i] : 0.f;
; }
; __device__ __forceinline__ void conv_store(const ConvItem& ci, LAS float* scr, int lane, const float (&v)[64]) {
;     const int c = lane & 7;
;     f32x4 s0 = {1.f, 1.f, 1.f, 1.f}, s1 = s0;
;     if (ci.ks) { const int kb = ci.k0 + 8 * c < ci.Ksrc - 8 ? ci.k0 + 8 * c : ci.Ksrc - 8; s0 = *(const f32x4*)(ci.ks + kb); s1 = *(const f32x4*)(ci.ks + kb + 4); }
; #pragma unroll
;     for (int i = 0; i < 64; ++i) scr[i * 65 + lane] = v[i];
.Lcvp0b_30:
	s_cmp_lt_i32 s58, s76
	s_cselect_b64 s[4:5], -1, 0
	s_and_b64 s[4:5], vcc, s[4:5]
	s_cmp_lt_i32 s64, s76
	s_waitcnt vmcnt(62)
	v_cndmask_b32_e64 v21, 0, v21, s[4:5]
	s_cselect_b64 s[4:5], -1, 0
	s_and_b64 s[4:5], vcc, s[4:5]
	s_cmp_lt_i32 s65, s76
	v_cndmask_b32_e64 v20, 0, v20, s[4:5]
	s_cselect_b64 s[4:5], -1, 0
	s_and_b64 s[4:5], vcc, s[4:5]
	s_cmp_lt_i32 s78, s76
	s_waitcnt vmcnt(61)
	v_cndmask_b32_e64 v19, 0, v19, s[4:5]
	s_cselect_b64 s[4:5], -1, 0
	s_and_b64 s[4:5], vcc, s[4:5]
	s_cmp_lt_i32 s79, s76
	s_waitcnt vmcnt(60)
	v_cndmask_b32_e64 v18, 0, v18, s[4:5]
	s_cselect_b64 s[4:5], -1, 0
	s_and_b64 s[4:5], vcc, s[4:5]
	s_cmp_lt_i32 s80, s76
	s_waitcnt vmcnt(59)
	v_cndmask_b32_e64 v17, 0, v17, s[4:5]
	s_cselect_b64 s[4:5], -1, 0
	s_and_b64 s[4:5], vcc, s[4:5]
	s_cmp_lt_i32 s81, s76
	s_waitcnt vmcnt(58)
	v_cndmask_b32_e64 v16, 0, v16, s[4:5]
	s_cselect_b64 s[4:5], -1, 0
	s_and_b64 s[4:5], vcc, s[4:5]
	s_cmp_lt_i32 s82, s76
	s_waitcnt vmcnt(57)
	v_cndmask_b32_e64 v15, 0, v15, s[4:5]
	s_cselect_b64 s[4:5], -1, 0
	s_and_b64 s[4:5], vcc, s[4:5]
	s_cmp_lt_i32 s83, s76
	s_waitcnt vmcnt(56)
	v_cndmask_b32_e64 v8, 0, v8, s[4:5]
	s_cselect_b64 s[4:5], -1, 0
	s_and_b64 s[4:5], vcc, s[4:5]
	s_cmp_lt_i32 s85, s76
	s_waitcnt vmcnt(55)
	v_cndmask_b32_e64 v29, 0, v29, s[4:5]
	s_cselect_b64 s[4:5], -1, 0
	s_and_b64 s[4:5], vcc, s[4:5]
	s_cmp_lt_i32 s86, s76
	s_waitcnt vmcnt(54)
	v_cndmask_b32_e64 v28, 0, v28, s[4:5]
	s_cselect_b64 s[4:5], -1, 0
	s_and_b64 s[4:5], vcc, s[4:5]
	s_cmp_lt_i32 s87, s76
	s_waitcnt vmcnt(53)
	v_cndmask_b32_e64 v27, 0, v27, s[4:5]
	s_cselect_b64 s[4:5], -1, 0
	s_and_b64 s[4:5], vcc, s[4:5]
	s_cmp_lt_i32 s88, s76
	s_waitcnt vmcnt(52)
	v_cndmask_b32_e64 v26, 0, v26, s[4:5]
	s_cselect_b64 s[4:5], -1, 0
	s_and_b64 s[4:5], vcc, s[4:5]
	s_cmp_lt_i32 s89, s76
	s_waitcnt vmcnt(51)
	v_cndmask_b32_e64 v25, 0, v25, s[4:5]
	s_cselect_b64 s[4:5], -1, 0
	s_and_b64 s[4:5], vcc, s[4:5]
	s_cmp_lt_i32 s90, s76
	s_waitcnt vmcnt(50)
	v_cndmask_b32_e64 v24, 0, v24, s[4:5]
	s_cselect_b64 s[4:5], -1, 0
	s_and_b64 s[4:5], vcc, s[4:5]
	s_cmp_lt_i32 s92, s76
	s_waitcnt vmcnt(49)
	v_cndmask_b32_e64 v23, 0, v23, s[4:5]
	s_cselect_b64 s[4:5], -1, 0
	s_and_b64 s[4:5], vcc, s[4:5]
	s_cmp_lt_i32 s93, s76
	s_waitcnt vmcnt(48)
	v_cndmask_b32_e64 v22, 0, v22, s[4:5]
	s_cselect_b64 s[4:5], -1, 0
	s_and_b64 s[4:5], vcc, s[4:5]
	s_cmp_lt_i32 s94, s76
	s_waitcnt vmcnt(47)
	v_cndmask_b32_e64 v37, 0, v37, s[4:5]
	s_cselect_b64 s[4:5], -1, 0
	s_and_b64 s[4:5], vcc, s[4:5]
	s_cmp_lt_i32 s95, s76
	s_waitcnt vmcnt(46)
	v_cndmask_b32_e64 v36, 0, v36, s[4:5]
	s_cselect_b64 s[4:5], -1, 0
	s_and_b64 s[4:5], vcc, s[4:5]
	s_cmp_lt_i32 s50, s76
	s_waitcnt vmcnt(45)
	v_cndmask_b32_e64 v35, 0, v35, s[4:5]
	s_cselect_b64 s[4:5], -1, 0
	s_and_b64 s[4:5], vcc, s[4:5]
	s_cmp_lt_i32 s51, s76
	s_waitcnt vmcnt(44)
	v_cndmask_b32_e64 v34, 0, v34, s[4:5]
	s_cselect_b64 s[4:5], -1, 0
	s_and_b64 s[4:5], vcc, s[4:5]
	s_cmp_lt_i32 s52, s76
	s_waitcnt vmcnt(43)
	v_cndmask_b32_e64 v33, 0, v33, s[4:5]
	s_cselect_b64 s[4:5], -1, 0
	s_and_b64 s[4:5], vcc, s[4:5]
	s_cmp_lt_i32 s53, s76
	s_waitcnt vmcnt(42)
	v_cndmask_b32_e64 v32, 0, v32, s[4:5]
	s_cselect_b64 s[4:5], -1, 0
	s_and_b64 s[4:5], vcc, s[4:5]
	s_cmp_lt_i32 s6, s76
	s_waitcnt vmcnt(41)
	v_cndmask_b32_e64 v31, 0, v31, s[4:5]
	s_cselect_b64 s[4:5], -1, 0
	s_and_b64 s[4:5], vcc, s[4:5]
	s_cmp_lt_i32 s7, s76
	s_waitcnt vmcnt(40)
	v_cndmask_b32_e64 v30, 0, v30, s[4:5]
	s_cselect_b64 s[4:5], -1, 0
	s_and_b64 s[4:5], vcc, s[4:5]
	s_cmp_lt_i32 s8, s76
	s_waitcnt vmcnt(39)
	v_cndmask_b32_e64 v45, 0, v45, s[4:5]
	s_cselect_b64 s[4:5], -1, 0
	s_and_b64 s[4:5], vcc, s[4:5]
	s_cmp_lt_i32 s9, s76
	s_waitcnt vmcnt(38)
	v_cndmask_b32_e64 v44, 0, v44, s[4:5]
	s_cselect_b64 s[4:5], -1, 0
	s_and_b64 s[4:5], vcc, s[4:5]
	s_cmp_lt_i32 s10, s76
	s_waitcnt vmcnt(37)
	v_cndmask_b32_e64 v43, 0, v43, s[4:5]
	s_cselect_b64 s[4:5], -1, 0
	s_and_b64 s[4:5], vcc, s[4:5]
	s_cmp_lt_i32 s11, s76
	s_waitcnt vmcnt(36)
	v_cndmask_b32_e64 v42, 0, v42, s[4:5]
	s_cselect_b64 s[4:5], -1, 0
	s_and_b64 s[4:5], vcc, s[4:5]
	s_cmp_lt_i32 s14, s76
	s_waitcnt vmcnt(35)
	v_cndmask_b32_e64 v41, 0, v41, s[4:5]
	s_cselect_b64 s[4:5], -1, 0
	s_and_b64 s[4:5], vcc, s[4:5]
	s_cmp_lt_i32 s15, s76
	s_waitcnt vmcnt(34)
	v_cndmask_b32_e64 v40, 0, v40, s[4:5]
	s_cselect_b64 s[4:5], -1, 0
	s_and_b64 s[4:5], vcc, s[4:5]
	s_cmp_lt_i32 s16, s76
	s_waitcnt vmcnt(33)
	v_cndmask_b32_e64 v39, 0, v39, s[4:5]
	s_cselect_b64 s[4:5], -1, 0
	s_and_b64 s[4:5], vcc, s[4:5]
	s_cmp_lt_i32 s17, s76
	s_waitcnt vmcnt(32)
	v_cndmask_b32_e64 v38, 0, v38, s[4:5]
	s_cselect_b64 s[4:5], -1, 0
	s_and_b64 s[4:5], vcc, s[4:5]
	s_cmp_lt_i32 s12, s76
	s_waitcnt vmcnt(31)
	v_cndmask_b32_e64 v53, 0, v53, s[4:5]
	s_cselect_b64 s[4:5], -1, 0
	s_and_b64 s[4:5], vcc, s[4:5]
	s_cmp_lt_i32 s13, s76
	s_waitcnt vmcnt(30)
	v_cndmask_b32_e64 v52, 0, v52, s[4:5]
	s_cselect_b64 s[4:5], -1, 0
	s_and_b64 s[4:5], vcc, s[4:5]
	s_cmp_lt_i32 s20, s76
	s_waitcnt vmcnt(29)
	v_cndmask_b32_e64 v51, 0, v51, s[4:5]
	s_cselect_b64 s[4:5], -1, 0
	s_and_b64 s[4:5], vcc, s[4:5]
	s_cmp_lt_i32 s21, s76
	s_waitcnt vmcnt(28)
	v_cndmask_b32_e64 v50, 0, v50, s[4:5]
	s_cselect_b64 s[4:5], -1, 0
	s_and_b64 s[4:5], vcc, s[4:5]
	s_cmp_lt_i32 s24, s76
	s_waitcnt vmcnt(27)
	v_cndmask_b32_e64 v49, 0, v49, s[4:5]
	s_cselect_b64 s[4:5], -1, 0
	s_and_b64 s[4:5], vcc, s[4:5]
	s_cmp_lt_i32 s25, s76
	s_waitcnt vmcnt(26)
	v_cndmask_b32_e64 v48, 0, v48, s[4:5]
	s_cselect_b64 s[4:5], -1, 0
	s_and_b64 s[4:5], vcc, s[4:5]
	s_cmp_lt_i32 s26, s76
	s_waitcnt vmcnt(25)
	v_cndmask_b32_e64 v47, 0, v47, s[4:5]
	s_cselect_b64 s[4:5], -1, 0
	s_and_b64 s[4:5], vcc, s[4:5]
	s_cmp_lt_i32 s27, s76
	s_waitcnt vmcnt(24)
; #define LAS __attribute__((address_space(3)))
; #define LDS_WAIT() asm volatile("s_waitcnt lgkmcnt(0)" ::: "memory")
; __device__ __forceinline__ void conv_load(const ConvItem& ci, int lane, float (&v)[64]) {
;     ...
;     for (int i = 0; i < 64; ++i) v[i] = (okc && (ci.k0 + i) < ci.Ksrc) ? v[i] : 0.f;
; }
; __device__ __forceinline__ void conv_store(const ConvItem& ci, LAS float* scr, int lane, const float (&v)[64]) {
;     const int c = lane & 7;
;     f32x4 s0 = {1.f, 1.f, 1.f, 1.f}, s1 = s0;
;     if (ci.ks) { const int kb = ci.k0 + 8 * c < ci.Ksrc - 8 ? ci.k0 + 8 * c : ci.Ksrc - 8; s0 = *(const f32x4*)(ci.ks + kb); s1 = *(const f32x4*)(ci.ks + kb + 4); }
; #pragma unroll
;     for (int i = 0; i < 64; ++i) scr[i * 65 + lane] = v[i];
;     LDS_WAIT(); asm volatile("" ::: "memory");
	v_cndmask_b32_e64 v46, 0, v46, s[4:5]
	s_cselect_b64 s[4:5], -1, 0
	s_and_b64 s[4:5], vcc, s[4:5]
	s_cmp_lt_i32 s18, s76
	s_waitcnt vmcnt(23)
	v_cndmask_b32_e64 v61, 0, v61, s[4:5]
	s_cselect_b64 s[4:5], -1, 0
	s_and_b64 s[4:5], vcc, s[4:5]
	s_cmp_lt_i32 s19, s76
	s_waitcnt vmcnt(22)
	v_cndmask_b32_e64 v60, 0, v60, s[4:5]
	s_cselect_b64 s[4:5], -1, 0
	s_and_b64 s[4:5], vcc, s[4:5]
	s_cmp_lt_i32 s28, s76
	s_waitcnt vmcnt(21)
	v_cndmask_b32_e64 v59, 0, v59, s[4:5]
	s_cselect_b64 s[4:5], -1, 0
	s_and_b64 s[4:5], vcc, s[4:5]
	s_cmp_lt_i32 s29, s76
	s_waitcnt vmcnt(20)
	v_cndmask_b32_e64 v58, 0, v58, s[4:5]
	s_cselect_b64 s[4:5], -1, 0
	s_and_b64 s[4:5], vcc, s[4:5]
	s_cmp_lt_i32 s22, s76
	s_waitcnt vmcnt(19)
	v_cndmask_b32_e64 v57, 0, v57, s[4:5]
	s_cselect_b64 s[4:5], -1, 0
	s_and_b64 s[4:5], vcc, s[4:5]
	s_cmp_lt_i32 s23, s76
	s_waitcnt vmcnt(18)
	v_cndmask_b32_e64 v56, 0, v56, s[4:5]
	s_cselect_b64 s[4:5], -1, 0
	s_and_b64 s[4:5], vcc, s[4:5]
	s_cmp_lt_i32 s30, s76
	s_waitcnt vmcnt(17)
	v_cndmask_b32_e64 v55, 0, v55, s[4:5]
	s_cselect_b64 s[4:5], -1, 0
	s_and_b64 s[4:5], vcc, s[4:5]
	s_cmp_lt_i32 s31, s76
	s_waitcnt vmcnt(16)
	v_cndmask_b32_e64 v54, 0, v54, s[4:5]
	s_cselect_b64 s[4:5], -1, 0
	s_and_b64 s[4:5], vcc, s[4:5]
	s_cmp_lt_i32 s36, s76
	s_waitcnt vmcnt(15)
	v_cndmask_b32_e64 v70, 0, v70, s[4:5]
	s_cselect_b64 s[4:5], -1, 0
	s_and_b64 s[4:5], vcc, s[4:5]
	s_cmp_lt_i32 s37, s76
	s_waitcnt vmcnt(14)
	v_cndmask_b32_e64 v69, 0, v69, s[4:5]
	s_cselect_b64 s[4:5], -1, 0
	s_and_b64 s[4:5], vcc, s[4:5]
	s_cmp_lt_i32 s38, s76
	s_waitcnt vmcnt(13)
	v_cndmask_b32_e64 v68, 0, v68, s[4:5]
	s_cselect_b64 s[4:5], -1, 0
	s_and_b64 s[4:5], vcc, s[4:5]
	s_cmp_lt_i32 s39, s76
	s_waitcnt vmcnt(12)
	v_cndmask_b32_e64 v67, 0, v67, s[4:5]
	s_cselect_b64 s[4:5], -1, 0
	s_and_b64 s[4:5], vcc, s[4:5]
	s_cmp_lt_i32 s34, s76
	s_waitcnt vmcnt(11)
	v_cndmask_b32_e64 v66, 0, v66, s[4:5]
	s_cselect_b64 s[4:5], -1, 0
	s_and_b64 s[4:5], vcc, s[4:5]
	s_cmp_lt_i32 s35, s76
	s_waitcnt vmcnt(10)
	v_cndmask_b32_e64 v64, 0, v64, s[4:5]
	s_cselect_b64 s[4:5], -1, 0
	s_and_b64 s[4:5], vcc, s[4:5]
	s_cmp_lt_i32 s42, s76
	s_waitcnt vmcnt(9)
	v_cndmask_b32_e64 v63, 0, v63, s[4:5]
	s_cselect_b64 s[4:5], -1, 0
	s_and_b64 s[4:5], vcc, s[4:5]
	s_cmp_lt_i32 s43, s76
	s_waitcnt vmcnt(8)
	v_cndmask_b32_e64 v62, 0, v62, s[4:5]
	s_cselect_b64 s[4:5], -1, 0
	s_and_b64 s[4:5], vcc, s[4:5]
	s_cmp_lt_i32 s54, s76
	s_waitcnt vmcnt(7)
	v_cndmask_b32_e64 v65, 0, v65, s[4:5]
	s_cselect_b64 s[4:5], -1, 0
	s_and_b64 s[4:5], vcc, s[4:5]
	s_cmp_lt_i32 s55, s76
	s_waitcnt vmcnt(6)
	v_cndmask_b32_e64 v74, 0, v74, s[4:5]
	s_cselect_b64 s[4:5], -1, 0
	s_and_b64 s[4:5], vcc, s[4:5]
	s_cmp_lt_i32 s46, s76
	ds_write2_b32 v12, v21, v20 offset1:65
	ds_write2_b32 v12, v19, v18 offset0:130 offset1:195
	v_add_u32_e32 v18, 0x400, v12
	s_waitcnt vmcnt(5)
	v_cndmask_b32_e64 v73, 0, v73, s[4:5]
	s_cselect_b64 s[4:5], -1, 0
	ds_write2_b32 v18, v17, v16 offset0:4 offset1:69
	ds_write2_b32 v18, v15, v8 offset0:134 offset1:199
	v_add_u32_e32 v8, 0x800, v12
	s_and_b64 s[4:5], vcc, s[4:5]
	ds_write2_b32 v8, v29, v28 offset0:8 offset1:73
	ds_write2_b32 v8, v27, v26 offset0:138 offset1:203
	v_add_u32_e32 v8, 0xc00, v12
	s_cmp_lt_i32 s47, s76
	ds_write2_b32 v8, v25, v24 offset0:12 offset1:77
	ds_write2_b32 v8, v23, v22 offset0:142 offset1:207
	v_add_u32_e32 v8, 0x1000, v12
	s_waitcnt vmcnt(4)
	v_cndmask_b32_e64 v72, 0, v72, s[4:5]
	s_cselect_b64 s[4:5], -1, 0
	ds_write2_b32 v8, v37, v36 offset0:16 offset1:81
	ds_write2_b32 v8, v35, v34 offset0:146 offset1:211
	v_add_u32_e32 v8, 0x1400, v12
	s_and_b64 s[4:5], vcc, s[4:5]
	ds_write2_b32 v8, v33, v32 offset0:20 offset1:85
	ds_write2_b32 v8, v31, v30 offset0:150 offset1:215
	v_add_u32_e32 v8, 0x1800, v12
	s_cmp_lt_i32 s48, s76
	ds_write2_b32 v8, v45, v44 offset0:24 offset1:89
	ds_write2_b32 v8, v43, v42 offset0:154 offset1:219
	v_add_u32_e32 v8, 0x1c00, v12
	s_waitcnt vmcnt(3)
	v_cndmask_b32_e64 v71, 0, v71, s[4:5]
	s_cselect_b64 s[4:5], -1, 0
	ds_write2_b32 v8, v41, v40 offset0:28 offset1:93
	ds_write2_b32 v8, v39, v38 offset0:158 offset1:223
	v_add_u32_e32 v8, 0x2000, v12
	s_and_b64 s[4:5], vcc, s[4:5]
	ds_write2_b32 v8, v53, v52 offset0:32 offset1:97
	ds_write2_b32 v8, v51, v50 offset0:162 offset1:227
	v_add_u32_e32 v8, 0x2400, v12
	s_cmp_lt_i32 s49, s76
	ds_write2_b32 v8, v49, v48 offset0:36 offset1:101
	ds_write2_b32 v8, v47, v46 offset0:166 offset1:231
	v_add_u32_e32 v8, 0x2800, v12
	s_waitcnt vmcnt(2)
	v_cndmask_b32_e64 v77, 0, v77, s[4:5]
	s_cselect_b64 s[4:5], -1, 0
	ds_write2_b32 v8, v61, v60 offset0:40 offset1:105
	ds_write2_b32 v8, v59, v58 offset0:170 offset1:235
	v_add_u32_e32 v8, 0x2c00, v12
	s_and_b64 s[4:5], vcc, s[4:5]
	ds_write2_b32 v8, v57, v56 offset0:44 offset1:109
	ds_write2_b32 v8, v55, v54 offset0:174 offset1:239
	v_add_u32_e32 v8, 0x3000, v12
	s_cmp_lt_i32 s44, s76
	ds_write2_b32 v8, v70, v69 offset0:48 offset1:113
	ds_write2_b32 v8, v68, v67 offset0:178 offset1:243
	v_add_u32_e32 v8, 0x3400, v12
	s_waitcnt vmcnt(1)
	v_cndmask_b32_e64 v76, 0, v76, s[4:5]
	s_cselect_b64 s[4:5], -1, 0
	ds_write2_b32 v8, v66, v64 offset0:52 offset1:117
	ds_write2_b32 v8, v63, v62 offset0:182 offset1:247
	v_add_u32_e32 v8, 0x3800, v12
	s_and_b64 vcc, vcc, s[4:5]
	ds_write2_b32 v8, v65, v74 offset0:56 offset1:121
	ds_write2_b32 v8, v73, v72 offset0:186 offset1:251
	v_add_u32_e32 v8, 0x3c00, v12
	s_waitcnt vmcnt(0)
	v_cndmask_b32_e32 v75, 0, v75, vcc
	ds_write2_b32 v8, v71, v77 offset0:60 offset1:125
	ds_write2_b32 v8, v76, v75 offset0:190 offset1:255
	s_waitcnt lgkmcnt(0)
; __device__ __forceinline__ unsigned cvt_pk_bf16(float lo, float hi) { unsigned r; asm volatile("v_cvt_pk_bf16_f32 %0, %1, %2" : "=v"(r) : "v"(lo), "v"(hi)); return r; }
; #define LAS __attribute__((address_space(3)))
; __device__ __forceinline__ void conv_store(const ConvItem& ci, LAS float* scr, int lane, const float (&v)[64]) {
;     ...
;     for (int j = 0; j < 8; ++j) { const int n = (lane >> 3) + 8 * j; const LAS float* s = scr + (8 * c) * 65 + n;
;         v4u o; o.x = cvt_pk_bf16(s[0 * 65] * s0[0], s[1 * 65] * s0[1]); o.y = cvt_pk_bf16(s[2 * 65] * s0[2], s[3 * 65] * s0[3]); o.z = cvt_pk_bf16(s[4 * 65] * s1[0], s[5 * 65] * s1[1]); o.w = cvt_pk_bf16(s[6 * 65] * s1[2], s[7 * 65] * s1[3]);
;         *(v4u*)(ci.dst + (size_t)(ci.drow0 + n) * ci.ldd + ci.k0 + 8 * c) = o; }
	v_add_u32_e32 v192, 0x400, v14
	ds_read2_b32 v[128:129], v14 offset1:65
	ds_read2_b32 v[130:131], v14 offset0:130 offset1:195
	ds_read2_b32 v[132:133], v192 offset0:4 offset1:69
	ds_read2_b32 v[134:135], v192 offset0:134 offset1:199
	ds_read2_b32 v[136:137], v14 offset0:8 offset1:73
	ds_read2_b32 v[138:139], v14 offset0:138 offset1:203
	ds_read2_b32 v[140:141], v192 offset0:12 offset1:77
	ds_read2_b32 v[142:143], v192 offset0:142 offset1:207
	ds_read2_b32 v[144:145], v14 offset0:16 offset1:81
	ds_read2_b32 v[146:147], v14 offset0:146 offset1:211
	ds_read2_b32 v[148:149], v192 offset0:20 offset1:85
	ds_read2_b32 v[150:151], v192 offset0:150 offset1:215
	ds_read2_b32 v[152:153], v14 offset0:24 offset1:89
	ds_read2_b32 v[154:155], v14 offset0:154 offset1:219
	ds_read2_b32 v[156:157], v192 offset0:28 offset1:93
	ds_read2_b32 v[158:159], v192 offset0:158 offset1:223
	ds_read2_b32 v[160:161], v14 offset0:32 offset1:97
	ds_read2_b32 v[162:163], v14 offset0:162 offset1:227
	ds_read2_b32 v[164:165], v192 offset0:36 offset1:101
	ds_read2_b32 v[166:167], v192 offset0:166 offset1:231
	ds_read2_b32 v[168:169], v14 offset0:40 offset1:105
	ds_read2_b32 v[170:171], v14 offset0:170 offset1:235
	ds_read2_b32 v[172:173], v192 offset0:44 offset1:109
	ds_read2_b32 v[174:175], v192 offset0:174 offset1:239
	ds_read2_b32 v[176:177], v14 offset0:48 offset1:113
	ds_read2_b32 v[178:179], v14 offset0:178 offset1:243
	ds_read2_b32 v[180:181], v192 offset0:52 offset1:117
	ds_read2_b32 v[182:183], v192 offset0:182 offset1:247
	ds_read2_b32 v[184:185], v14 offset0:56 offset1:121
	ds_read2_b32 v[186:187], v14 offset0:186 offset1:251
	ds_read2_b32 v[188:189], v192 offset0:60 offset1:125
	ds_read2_b32 v[190:191], v192 offset0:190 offset1:255
	s_waitcnt lgkmcnt(0)
	v_add_u32_e32 v24, s59, v13
	v_mul_lo_u32 v22, s57, v24
	s_ashr_i32 s59, s58, 31
	v_readlane_b32 s76, v254, 31
	s_waitcnt lgkmcnt(0)
	v_mul_f32_e32 v8, v4, v128
	v_mul_f32_e32 v15, v5, v129
	v_cvt_pk_bf16_f32 v16, v8, v15
	s_add_i32 s3, s3, s33
	s_add_i32 s66, s66, s67
	s_add_i32 s68, s68, s69
	s_add_i32 s70, s70, s71
	s_waitcnt lgkmcnt(0)
	v_mul_f32_e32 v15, v7, v131
	v_mul_f32_e32 v8, v6, v130
	v_cvt_pk_bf16_f32 v17, v8, v15
	v_add_u32_e32 v15, 0x400, v14
	s_add_i32 s72, s72, s73
	s_add_i32 s74, s74, s75
	v_readlane_b32 s78, v254, 33
	v_readlane_b32 s79, v254, 34
	s_waitcnt lgkmcnt(0)
	v_mul_f32_e32 v8, v0, v132
	v_mul_f32_e32 v18, v1, v133
	v_cvt_pk_bf16_f32 v18, v8, v18
	v_readlane_b32 s80, v255, 21
	v_readlane_b32 s77, v254, 32
	s_movk_i32 s78, 0x1580
	v_readlane_b32 s82, v255, 23
	s_waitcnt lgkmcnt(0)
	v_mul_f32_e32 v8, v2, v134
	v_mul_f32_e32 v19, v3, v135
	v_cvt_pk_bf16_f32 v19, v8, v19
	v_ashrrev_i32_e32 v8, 31, v24
	v_mul_lo_u32 v8, s56, v8
	v_mad_u64_u32 v[20:21], s[4:5], s56, v24, 0
	v_add3_u32 v21, v21, v8, v22
	v_lshl_add_u64 v[20:21], v[20:21], 1, s[60:61]
	s_lshl_b64 s[4:5], s[58:59], 1
	v_lshl_add_u64 v[20:21], v[20:21], 0, s[4:5]
	v_lshlrev_b32_e32 v8, 1, v10
	v_lshl_add_u64 v[20:21], v[20:21], 0, v[8:9]
	global_store_dwordx4 v[20:21], v[16:19], off
	s_cmpk_lt_i32 s3, 27072
	v_readlane_b32 s83, v255, 24
	s_waitcnt lgkmcnt(0)
	v_mul_f32_e32 v16, v4, v136
	v_mul_f32_e32 v17, v5, v137
	v_cvt_pk_bf16_f32 v16, v16, v17
	s_mov_b32 s79, 0x3f22f983
	s_mov_b32 s85, 0xbfc90fda
	s_brev_b32 s86, 1
	s_movk_i32 s87, 0x1f8
	s_waitcnt lgkmcnt(0)
	v_mul_f32_e32 v17, v6, v138
	v_mul_f32_e32 v18, v7, v139
	v_cvt_pk_bf16_f32 v17, v17, v18
	s_mov_b64 s[88:89], 0x80
	s_mov_b64 s[92:93], 0x4000
	s_mov_b64 s[94:95], 0x4800
	v_readlane_b32 s81, v255, 22
	s_waitcnt lgkmcnt(0)
	v_mul_f32_e32 v18, v0, v140
	v_mul_f32_e32 v19, v1, v141
	v_cvt_pk_bf16_f32 v18, v18, v19
	s_waitcnt lgkmcnt(0)
	v_mul_f32_e32 v19, v2, v142
	v_mul_f32_e32 v20, v3, v143
	v_cvt_pk_bf16_f32 v19, v19, v20
	v_add_u32_e32 v20, 8, v24
	v_ashrrev_i32_e32 v21, 31, v20
	v_mul_lo_u32 v22, s56, v21
	v_mul_lo_u32 v23, s57, v20
	v_mad_u64_u32 v[20:21], s[6:7], s56, v20, 0
	v_add3_u32 v21, v21, v22, v23
	v_lshl_add_u64 v[20:21], v[20:21], 1, s[60:61]
	v_lshl_add_u64 v[20:21], v[20:21], 0, s[4:5]
	v_lshl_add_u64 v[20:21], v[20:21], 0, v[8:9]
	global_store_dwordx4 v[20:21], v[16:19], off
	s_waitcnt lgkmcnt(0)
	s_nop 0
	v_mul_f32_e32 v16, v4, v144
	v_mul_f32_e32 v17, v5, v145
	v_cvt_pk_bf16_f32 v16, v16, v17
	s_waitcnt lgkmcnt(0)
	v_mul_f32_e32 v17, v6, v146
	v_mul_f32_e32 v18, v7, v147
	v_cvt_pk_bf16_f32 v17, v17, v18
	s_waitcnt lgkmcnt(0)
	v_mul_f32_e32 v18, v0, v148
	v_mul_f32_e32 v19, v1, v149
	v_cvt_pk_bf16_f32 v18, v18, v19
	s_waitcnt lgkmcnt(0)
; __device__ __forceinline__ unsigned cvt_pk_bf16(float lo, float hi) { unsigned r; asm volatile("v_cvt_pk_bf16_f32 %0, %1, %2" : "=v"(r) : "v"(lo), "v"(hi)); return r; }
; #define LAS __attribute__((address_space(3)))
; #define LDS_WAIT() asm volatile("s_waitcnt lgkmcnt(0)" ::: "memory")
; __device__ __forceinline__ void conv_store(const ConvItem& ci, LAS float* scr, int lane, const float (&v)[64]) {
;     ...
;     for (int j = 0; j < 8; ++j) { const int n = (lane >> 3) + 8 * j; const LAS float* s = scr + (8 * c) * 65 + n;
;         v4u o; o.x = cvt_pk_bf16(s[0 * 65] * s0[0], s[1 * 65] * s0[1]); o.y = cvt_pk_bf16(s[2 * 65] * s0[2], s[3 * 65] * s0[3]); o.z = cvt_pk_bf16(s[4 * 65] * s1[0], s[5 * 65] * s1[1]); o.w = cvt_pk_bf16(s[6 * 65] * s1[2], s[7 * 65] * s1[3]);
;         *(v4u*)(ci.dst + (size_t)(ci.drow0 + n) * ci.ldd + ci.k0 + 8 * c) = o; }
;     LDS_WAIT(); asm volatile("" ::: "memory");
	v_mul_f32_e32 v19, v2, v150
	v_mul_f32_e32 v20, v3, v151
	v_cvt_pk_bf16_f32 v19, v19, v20
	v_add_u32_e32 v20, 16, v24
	v_ashrrev_i32_e32 v21, 31, v20
	v_mul_lo_u32 v22, s56, v21
	v_mul_lo_u32 v23, s57, v20
	v_mad_u64_u32 v[20:21], s[6:7], s56, v20, 0
	v_add3_u32 v21, v21, v22, v23
	v_lshl_add_u64 v[20:21], v[20:21], 1, s[60:61]
	v_lshl_add_u64 v[20:21], v[20:21], 0, s[4:5]
	v_lshl_add_u64 v[20:21], v[20:21], 0, v[8:9]
	global_store_dwordx4 v[20:21], v[16:19], off
	s_waitcnt lgkmcnt(0)
	s_nop 0
	v_mul_f32_e32 v16, v4, v152
	v_mul_f32_e32 v17, v5, v153
	v_cvt_pk_bf16_f32 v16, v16, v17
	s_waitcnt lgkmcnt(0)
	v_mul_f32_e32 v17, v6, v154
	v_mul_f32_e32 v18, v7, v155
	v_cvt_pk_bf16_f32 v17, v17, v18
	s_waitcnt lgkmcnt(0)
	v_mul_f32_e32 v18, v0, v156
	v_mul_f32_e32 v19, v1, v157
	v_cvt_pk_bf16_f32 v18, v18, v19
	s_waitcnt lgkmcnt(0)
	v_mul_f32_e32 v19, v2, v158
	v_mul_f32_e32 v20, v3, v159
	v_cvt_pk_bf16_f32 v19, v19, v20
	v_add_u32_e32 v20, 24, v24
	v_ashrrev_i32_e32 v21, 31, v20
	v_mul_lo_u32 v22, s56, v21
	v_mul_lo_u32 v23, s57, v20
	v_mad_u64_u32 v[20:21], s[6:7], s56, v20, 0
	v_add3_u32 v21, v21, v22, v23
	v_lshl_add_u64 v[20:21], v[20:21], 1, s[60:61]
	v_lshl_add_u64 v[20:21], v[20:21], 0, s[4:5]
	v_lshl_add_u64 v[20:21], v[20:21], 0, v[8:9]
	global_store_dwordx4 v[20:21], v[16:19], off
	s_waitcnt lgkmcnt(0)
	s_nop 0
	v_mul_f32_e32 v16, v4, v160
	v_mul_f32_e32 v17, v5, v161
	v_cvt_pk_bf16_f32 v16, v16, v17
	s_waitcnt lgkmcnt(0)
	v_mul_f32_e32 v17, v6, v162
	v_mul_f32_e32 v18, v7, v163
	v_cvt_pk_bf16_f32 v17, v17, v18
	s_waitcnt lgkmcnt(0)
	v_mul_f32_e32 v18, v0, v164
	v_mul_f32_e32 v19, v1, v165
	v_cvt_pk_bf16_f32 v18, v18, v19
	s_waitcnt lgkmcnt(0)
	v_mul_f32_e32 v19, v2, v166
	v_mul_f32_e32 v20, v3, v167
	v_cvt_pk_bf16_f32 v19, v19, v20
	v_add_u32_e32 v20, 32, v24
	v_ashrrev_i32_e32 v21, 31, v20
	v_mul_lo_u32 v22, s56, v21
	v_mul_lo_u32 v23, s57, v20
	v_mad_u64_u32 v[20:21], s[6:7], s56, v20, 0
	v_add3_u32 v21, v21, v22, v23
	v_lshl_add_u64 v[20:21], v[20:21], 1, s[60:61]
	v_lshl_add_u64 v[20:21], v[20:21], 0, s[4:5]
	v_lshl_add_u64 v[20:21], v[20:21], 0, v[8:9]
	global_store_dwordx4 v[20:21], v[16:19], off
	s_waitcnt lgkmcnt(0)
	s_nop 0
	v_mul_f32_e32 v16, v4, v168
	v_mul_f32_e32 v17, v5, v169
	v_cvt_pk_bf16_f32 v16, v16, v17
	s_waitcnt lgkmcnt(0)
	v_mul_f32_e32 v17, v6, v170
	v_mul_f32_e32 v18, v7, v171
	v_cvt_pk_bf16_f32 v17, v17, v18
	s_waitcnt lgkmcnt(0)
	v_mul_f32_e32 v18, v0, v172
	v_mul_f32_e32 v19, v1, v173
	v_cvt_pk_bf16_f32 v18, v18, v19
	s_waitcnt lgkmcnt(0)
	v_mul_f32_e32 v19, v2, v174
	v_mul_f32_e32 v20, v3, v175
	v_cvt_pk_bf16_f32 v19, v19, v20
	v_add_u32_e32 v20, 40, v24
	v_ashrrev_i32_e32 v21, 31, v20
	v_mul_lo_u32 v22, s56, v21
	v_mul_lo_u32 v23, s57, v20
	v_mad_u64_u32 v[20:21], s[6:7], s56, v20, 0
	v_add3_u32 v21, v21, v22, v23
	v_lshl_add_u64 v[20:21], v[20:21], 1, s[60:61]
	v_lshl_add_u64 v[20:21], v[20:21], 0, s[4:5]
	v_lshl_add_u64 v[20:21], v[20:21], 0, v[8:9]
	global_store_dwordx4 v[20:21], v[16:19], off
	s_waitcnt lgkmcnt(0)
	s_nop 0
	v_mul_f32_e32 v16, v4, v176
	v_mul_f32_e32 v17, v5, v177
	v_cvt_pk_bf16_f32 v16, v16, v17
	s_waitcnt lgkmcnt(0)
	v_mul_f32_e32 v17, v6, v178
	v_mul_f32_e32 v18, v7, v179
	v_cvt_pk_bf16_f32 v17, v17, v18
	s_waitcnt lgkmcnt(0)
	v_mul_f32_e32 v18, v0, v180
	v_mul_f32_e32 v19, v1, v181
	v_cvt_pk_bf16_f32 v18, v18, v19
	s_waitcnt lgkmcnt(0)
	v_mul_f32_e32 v19, v2, v182
	v_mul_f32_e32 v20, v3, v183
	v_cvt_pk_bf16_f32 v19, v19, v20
	v_add_u32_e32 v20, 48, v24
	v_ashrrev_i32_e32 v21, 31, v20
	v_mul_lo_u32 v22, s56, v21
	v_mul_lo_u32 v23, s57, v20
	v_mad_u64_u32 v[20:21], s[6:7], s56, v20, 0
	v_add3_u32 v21, v21, v22, v23
	v_lshl_add_u64 v[20:21], v[20:21], 1, s[60:61]
	v_lshl_add_u64 v[20:21], v[20:21], 0, s[4:5]
	v_lshl_add_u64 v[20:21], v[20:21], 0, v[8:9]
	global_store_dwordx4 v[20:21], v[16:19], off
	s_waitcnt lgkmcnt(0)
	v_mul_f32_e32 v4, v4, v184
	v_mul_f32_e32 v5, v5, v185
	v_cvt_pk_bf16_f32 v4, v4, v5
	s_waitcnt lgkmcnt(0)
	v_mul_f32_e32 v5, v6, v186
	v_mul_f32_e32 v6, v7, v187
	v_cvt_pk_bf16_f32 v5, v5, v6
	s_waitcnt lgkmcnt(0)
	v_mul_f32_e32 v0, v0, v188
	v_mul_f32_e32 v1, v1, v189
	v_cvt_pk_bf16_f32 v6, v0, v1
	s_waitcnt lgkmcnt(0)
	v_mul_f32_e32 v0, v2, v190
	v_mul_f32_e32 v1, v3, v191
	v_cvt_pk_bf16_f32 v7, v0, v1
	v_add_u32_e32 v0, 56, v24
	v_ashrrev_i32_e32 v1, 31, v0
	v_mul_lo_u32 v2, s56, v1
	v_mul_lo_u32 v3, s57, v0
	v_mad_u64_u32 v[0:1], s[6:7], s56, v0, 0
	v_add3_u32 v1, v1, v2, v3
	v_lshl_add_u64 v[0:1], v[0:1], 1, s[60:61]
	v_lshl_add_u64 v[0:1], v[0:1], 0, s[4:5]
	v_lshl_add_u64 v[0:1], v[0:1], 0, v[8:9]
	global_store_dwordx4 v[0:1], v[4:7], off
	s_waitcnt lgkmcnt(0)
	s_cbranch_scc0 .Lcvp0b_ret

; __device__ __forceinline__ void conv_load(const ConvItem& ci, int lane, float (&v)[64]) {
;     ...
;     for (int i = 0; i < 64; ++i) { const int k = ci.k0 + i, kk = k < kmax ? k : kmax; v[i] = __builtin_nontemporal_load(base + (size_t)kk * ci.ldw); }
; #pragma unroll
;     for (int i = 0; i < 64; ++i) v[i] = (okc && (ci.k0 + i) < ci.Ksrc) ? v[i] : 0.f;
.Lcvp0c_30:
	s_cmp_lt_i32 s58, s76
	s_cselect_b64 s[4:5], -1, 0
	s_and_b64 s[4:5], vcc, s[4:5]
	s_cmp_lt_i32 s64, s76
	s_waitcnt vmcnt(62)
	v_cndmask_b32_e64 v21, 0, v21, s[4:5]
	s_cselect_b64 s[4:5], -1, 0
	s_and_b64 s[4:5], vcc, s[4:5]
	s_cmp_lt_i32 s65, s76
	v_cndmask_b32_e64 v20, 0, v20, s[4:5]
	s_cselect_b64 s[4:5], -1, 0
	s_and_b64 s[4:5], vcc, s[4:5]
	s_cmp_lt_i32 s78, s76
	s_waitcnt vmcnt(61)
	v_cndmask_b32_e64 v19, 0, v19, s[4:5]
	s_cselect_b64 s[4:5], -1, 0
	s_and_b64 s[4:5], vcc, s[4:5]
	s_cmp_lt_i32 s79, s76
	s_waitcnt vmcnt(60)
	v_cndmask_b32_e64 v18, 0, v18, s[4:5]
	s_cselect_b64 s[4:5], -1, 0
	s_and_b64 s[4:5], vcc, s[4:5]
	s_cmp_lt_i32 s80, s76
	s_waitcnt vmcnt(59)
	v_cndmask_b32_e64 v17, 0, v17, s[4:5]
	s_cselect_b64 s[4:5], -1, 0
	s_and_b64 s[4:5], vcc, s[4:5]
	s_cmp_lt_i32 s81, s76
	s_waitcnt vmcnt(58)
	v_cndmask_b32_e64 v16, 0, v16, s[4:5]
	s_cselect_b64 s[4:5], -1, 0
	s_and_b64 s[4:5], vcc, s[4:5]
	s_cmp_lt_i32 s82, s76
	s_waitcnt vmcnt(57)
	v_cndmask_b32_e64 v15, 0, v15, s[4:5]
	s_cselect_b64 s[4:5], -1, 0
	s_and_b64 s[4:5], vcc, s[4:5]
	s_cmp_lt_i32 s83, s76
	s_waitcnt vmcnt(56)
	v_cndmask_b32_e64 v8, 0, v8, s[4:5]
	s_cselect_b64 s[4:5], -1, 0
	s_and_b64 s[4:5], vcc, s[4:5]
	s_cmp_lt_i32 s85, s76
	s_waitcnt vmcnt(55)
	v_cndmask_b32_e64 v29, 0, v29, s[4:5]
	s_cselect_b64 s[4:5], -1, 0
	s_and_b64 s[4:5], vcc, s[4:5]
	s_cmp_lt_i32 s86, s76
	s_waitcnt vmcnt(54)
	v_cndmask_b32_e64 v28, 0, v28, s[4:5]
	s_cselect_b64 s[4:5], -1, 0
	s_and_b64 s[4:5], vcc, s[4:5]
	s_cmp_lt_i32 s87, s76
	s_waitcnt vmcnt(53)
	v_cndmask_b32_e64 v27, 0, v27, s[4:5]
	s_cselect_b64 s[4:5], -1, 0
	s_and_b64 s[4:5], vcc, s[4:5]
	s_cmp_lt_i32 s88, s76
	s_waitcnt vmcnt(52)
	v_cndmask_b32_e64 v26, 0, v26, s[4:5]
	s_cselect_b64 s[4:5], -1, 0
	s_and_b64 s[4:5], vcc, s[4:5]
	s_cmp_lt_i32 s89, s76
	s_waitcnt vmcnt(51)
	v_cndmask_b32_e64 v25, 0, v25, s[4:5]
	s_cselect_b64 s[4:5], -1, 0
	s_and_b64 s[4:5], vcc, s[4:5]
	s_cmp_lt_i32 s90, s76
	s_waitcnt vmcnt(50)
	v_cndmask_b32_e64 v24, 0, v24, s[4:5]
	s_cselect_b64 s[4:5], -1, 0
	s_and_b64 s[4:5], vcc, s[4:5]
	s_cmp_lt_i32 s92, s76
	s_waitcnt vmcnt(49)
	v_cndmask_b32_e64 v23, 0, v23, s[4:5]
	s_cselect_b64 s[4:5], -1, 0
	s_and_b64 s[4:5], vcc, s[4:5]
	s_cmp_lt_i32 s93, s76
	s_waitcnt vmcnt(48)
	v_cndmask_b32_e64 v22, 0, v22, s[4:5]
	s_cselect_b64 s[4:5], -1, 0
	s_and_b64 s[4:5], vcc, s[4:5]
	s_cmp_lt_i32 s94, s76
	s_waitcnt vmcnt(47)
	v_cndmask_b32_e64 v37, 0, v37, s[4:5]
	s_cselect_b64 s[4:5], -1, 0
	s_and_b64 s[4:5], vcc, s[4:5]
	s_cmp_lt_i32 s95, s76
	s_waitcnt vmcnt(46)
	v_cndmask_b32_e64 v36, 0, v36, s[4:5]
	s_cselect_b64 s[4:5], -1, 0
	s_and_b64 s[4:5], vcc, s[4:5]
	s_cmp_lt_i32 s50, s76
	s_waitcnt vmcnt(45)
	v_cndmask_b32_e64 v35, 0, v35, s[4:5]
	s_cselect_b64 s[4:5], -1, 0
	s_and_b64 s[4:5], vcc, s[4:5]
	s_cmp_lt_i32 s51, s76
	s_waitcnt vmcnt(44)
	v_cndmask_b32_e64 v34, 0, v34, s[4:5]
	s_cselect_b64 s[4:5], -1, 0
	s_and_b64 s[4:5], vcc, s[4:5]
	s_cmp_lt_i32 s52, s76
	s_waitcnt vmcnt(43)
	v_cndmask_b32_e64 v33, 0, v33, s[4:5]
	s_cselect_b64 s[4:5], -1, 0
	s_and_b64 s[4:5], vcc, s[4:5]
	s_cmp_lt_i32 s53, s76
	s_waitcnt vmcnt(42)
	v_cndmask_b32_e64 v32, 0, v32, s[4:5]
	s_cselect_b64 s[4:5], -1, 0
	s_and_b64 s[4:5], vcc, s[4:5]
	s_cmp_lt_i32 s6, s76
	s_waitcnt vmcnt(41)
	v_cndmask_b32_e64 v31, 0, v31, s[4:5]
	s_cselect_b64 s[4:5], -1, 0
	s_and_b64 s[4:5], vcc, s[4:5]
	s_cmp_lt_i32 s7, s76
	s_waitcnt vmcnt(40)
	v_cndmask_b32_e64 v30, 0, v30, s[4:5]
	s_cselect_b64 s[4:5], -1, 0
	s_and_b64 s[4:5], vcc, s[4:5]
	s_cmp_lt_i32 s8, s76
	s_waitcnt vmcnt(39)
	v_cndmask_b32_e64 v45, 0, v45, s[4:5]
	s_cselect_b64 s[4:5], -1, 0
	s_and_b64 s[4:5], vcc, s[4:5]
	s_cmp_lt_i32 s9, s76
	s_waitcnt vmcnt(38)
	v_cndmask_b32_e64 v44, 0, v44, s[4:5]
	s_cselect_b64 s[4:5], -1, 0
	s_and_b64 s[4:5], vcc, s[4:5]
	s_cmp_lt_i32 s10, s76
	s_waitcnt vmcnt(37)
	v_cndmask_b32_e64 v43, 0, v43, s[4:5]
	s_cselect_b64 s[4:5], -1, 0
	s_and_b64 s[4:5], vcc, s[4:5]
	s_cmp_lt_i32 s11, s76
	s_waitcnt vmcnt(36)
	v_cndmask_b32_e64 v42, 0, v42, s[4:5]
	s_cselect_b64 s[4:5], -1, 0
	s_and_b64 s[4:5], vcc, s[4:5]
	s_cmp_lt_i32 s14, s76
	s_waitcnt vmcnt(35)
	v_cndmask_b32_e64 v41, 0, v41, s[4:5]
	s_cselect_b64 s[4:5], -1, 0
	s_and_b64 s[4:5], vcc, s[4:5]
	s_cmp_lt_i32 s15, s76
	s_waitcnt vmcnt(34)
	v_cndmask_b32_e64 v40, 0, v40, s[4:5]
	s_cselect_b64 s[4:5], -1, 0
	s_and_b64 s[4:5], vcc, s[4:5]
	s_cmp_lt_i32 s16, s76
	s_waitcnt vmcnt(33)
	v_cndmask_b32_e64 v39, 0, v39, s[4:5]
	s_cselect_b64 s[4:5], -1, 0
	s_and_b64 s[4:5], vcc, s[4:5]
	s_cmp_lt_i32 s17, s76
	s_waitcnt vmcnt(32)
	v_cndmask_b32_e64 v38, 0, v38, s[4:5]
	s_cselect_b64 s[4:5], -1, 0
	s_and_b64 s[4:5], vcc, s[4:5]
	s_cmp_lt_i32 s12, s76
	s_waitcnt vmcnt(31)
	v_cndmask_b32_e64 v53, 0, v53, s[4:5]
	s_cselect_b64 s[4:5], -1, 0
	s_and_b64 s[4:5], vcc, s[4:5]
	s_cmp_lt_i32 s13, s76
	s_waitcnt vmcnt(30)
	v_cndmask_b32_e64 v52, 0, v52, s[4:5]
	s_cselect_b64 s[4:5], -1, 0
	s_and_b64 s[4:5], vcc, s[4:5]
	s_cmp_lt_i32 s20, s76
	s_waitcnt vmcnt(29)
	v_cndmask_b32_e64 v51, 0, v51, s[4:5]
	s_cselect_b64 s[4:5], -1, 0
	s_and_b64 s[4:5], vcc, s[4:5]
	s_cmp_lt_i32 s21, s76
	s_waitcnt vmcnt(28)
	v_cndmask_b32_e64 v50, 0, v50, s[4:5]
	s_cselect_b64 s[4:5], -1, 0
	s_and_b64 s[4:5], vcc, s[4:5]
	s_cmp_lt_i32 s24, s76
	s_waitcnt vmcnt(27)
	v_cndmask_b32_e64 v49, 0, v49, s[4:5]
	s_cselect_b64 s[4:5], -1, 0
	s_and_b64 s[4:5], vcc, s[4:5]
	s_cmp_lt_i32 s25, s76
	s_waitcnt vmcnt(26)
	v_cndmask_b32_e64 v48, 0, v48, s[4:5]
	s_cselect_b64 s[4:5], -1, 0
	s_and_b64 s[4:5], vcc, s[4:5]
	s_cmp_lt_i32 s26, s76
	s_waitcnt vmcnt(25)
	v_cndmask_b32_e64 v47, 0, v47, s[4:5]
	s_cselect_b64 s[4:5], -1, 0
	s_and_b64 s[4:5], vcc, s[4:5]
	s_cmp_lt_i32 s27, s76
	s_waitcnt vmcnt(24)
; #define LAS __attribute__((address_space(3)))
; #define LDS_WAIT() asm volatile("s_waitcnt lgkmcnt(0)" ::: "memory")
; __device__ __forceinline__ void conv_load(const ConvItem& ci, int lane, float (&v)[64]) {
;     ...
;     for (int i = 0; i < 64; ++i) v[i] = (okc && (ci.k0 + i) < ci.Ksrc) ? v[i] : 0.f;
; }
; __device__ __forceinline__ void conv_store(const ConvItem& ci, LAS float* scr, int lane, const float (&v)[64]) {
;     const int c = lane & 7;
;     f32x4 s0 = {1.f, 1.f, 1.f, 1.f}, s1 = s0;
;     if (ci.ks) { const int kb = ci.k0 + 8 * c < ci.Ksrc - 8 ? ci.k0 + 8 * c : ci.Ksrc - 8; s0 = *(const f32x4*)(ci.ks + kb); s1 = *(const f32x4*)(ci.ks + kb + 4); }
; #pragma unroll
;     for (int i = 0; i < 64; ++i) scr[i * 65 + lane] = v[i];
;     LDS_WAIT(); asm volatile("" ::: "memory");
	v_cndmask_b32_e64 v46, 0, v46, s[4:5]
	s_cselect_b64 s[4:5], -1, 0
	s_and_b64 s[4:5], vcc, s[4:5]
	s_cmp_lt_i32 s18, s76
	s_waitcnt vmcnt(23)
	v_cndmask_b32_e64 v61, 0, v61, s[4:5]
	s_cselect_b64 s[4:5], -1, 0
	s_and_b64 s[4:5], vcc, s[4:5]
	s_cmp_lt_i32 s19, s76
	s_waitcnt vmcnt(22)
	v_cndmask_b32_e64 v60, 0, v60, s[4:5]
	s_cselect_b64 s[4:5], -1, 0
	s_and_b64 s[4:5], vcc, s[4:5]
	s_cmp_lt_i32 s28, s76
	s_waitcnt vmcnt(21)
	v_cndmask_b32_e64 v59, 0, v59, s[4:5]
	s_cselect_b64 s[4:5], -1, 0
	s_and_b64 s[4:5], vcc, s[4:5]
	s_cmp_lt_i32 s29, s76
	s_waitcnt vmcnt(20)
	v_cndmask_b32_e64 v58, 0, v58, s[4:5]
	s_cselect_b64 s[4:5], -1, 0
	s_and_b64 s[4:5], vcc, s[4:5]
	s_cmp_lt_i32 s22, s76
	s_waitcnt vmcnt(19)
	v_cndmask_b32_e64 v57, 0, v57, s[4:5]
	s_cselect_b64 s[4:5], -1, 0
	s_and_b64 s[4:5], vcc, s[4:5]
	s_cmp_lt_i32 s23, s76
	s_waitcnt vmcnt(18)
	v_cndmask_b32_e64 v56, 0, v56, s[4:5]
	s_cselect_b64 s[4:5], -1, 0
	s_and_b64 s[4:5], vcc, s[4:5]
	s_cmp_lt_i32 s30, s76
	s_waitcnt vmcnt(17)
	v_cndmask_b32_e64 v55, 0, v55, s[4:5]
	s_cselect_b64 s[4:5], -1, 0
	s_and_b64 s[4:5], vcc, s[4:5]
	s_cmp_lt_i32 s31, s76
	s_waitcnt vmcnt(16)
	v_cndmask_b32_e64 v54, 0, v54, s[4:5]
	s_cselect_b64 s[4:5], -1, 0
	s_and_b64 s[4:5], vcc, s[4:5]
	s_cmp_lt_i32 s36, s76
	s_waitcnt vmcnt(15)
	v_cndmask_b32_e64 v70, 0, v70, s[4:5]
	s_cselect_b64 s[4:5], -1, 0
	s_and_b64 s[4:5], vcc, s[4:5]
	s_cmp_lt_i32 s37, s76
	s_waitcnt vmcnt(14)
	v_cndmask_b32_e64 v69, 0, v69, s[4:5]
	s_cselect_b64 s[4:5], -1, 0
	s_and_b64 s[4:5], vcc, s[4:5]
	s_cmp_lt_i32 s38, s76
	s_waitcnt vmcnt(13)
	v_cndmask_b32_e64 v68, 0, v68, s[4:5]
	s_cselect_b64 s[4:5], -1, 0
	s_and_b64 s[4:5], vcc, s[4:5]
	s_cmp_lt_i32 s39, s76
	s_waitcnt vmcnt(12)
	v_cndmask_b32_e64 v67, 0, v67, s[4:5]
	s_cselect_b64 s[4:5], -1, 0
	s_and_b64 s[4:5], vcc, s[4:5]
	s_cmp_lt_i32 s34, s76
	s_waitcnt vmcnt(11)
	v_cndmask_b32_e64 v66, 0, v66, s[4:5]
	s_cselect_b64 s[4:5], -1, 0
	s_and_b64 s[4:5], vcc, s[4:5]
	s_cmp_lt_i32 s35, s76
	s_waitcnt vmcnt(10)
	v_cndmask_b32_e64 v64, 0, v64, s[4:5]
	s_cselect_b64 s[4:5], -1, 0
	s_and_b64 s[4:5], vcc, s[4:5]
	s_cmp_lt_i32 s42, s76
	s_waitcnt vmcnt(9)
	v_cndmask_b32_e64 v63, 0, v63, s[4:5]
	s_cselect_b64 s[4:5], -1, 0
	s_and_b64 s[4:5], vcc, s[4:5]
	s_cmp_lt_i32 s43, s76
	s_waitcnt vmcnt(8)
	v_cndmask_b32_e64 v62, 0, v62, s[4:5]
	s_cselect_b64 s[4:5], -1, 0
	s_and_b64 s[4:5], vcc, s[4:5]
	s_cmp_lt_i32 s54, s76
	s_waitcnt vmcnt(7)
	v_cndmask_b32_e64 v65, 0, v65, s[4:5]
	s_cselect_b64 s[4:5], -1, 0
	s_and_b64 s[4:5], vcc, s[4:5]
	s_cmp_lt_i32 s55, s76
	s_waitcnt vmcnt(6)
	v_cndmask_b32_e64 v74, 0, v74, s[4:5]
	s_cselect_b64 s[4:5], -1, 0
	s_and_b64 s[4:5], vcc, s[4:5]
	s_cmp_lt_i32 s46, s76
	ds_write2_b32 v12, v21, v20 offset1:65
	ds_write2_b32 v12, v19, v18 offset0:130 offset1:195
	v_add_u32_e32 v18, 0x400, v12
	s_waitcnt vmcnt(5)
	v_cndmask_b32_e64 v73, 0, v73, s[4:5]
	s_cselect_b64 s[4:5], -1, 0
	ds_write2_b32 v18, v17, v16 offset0:4 offset1:69
	ds_write2_b32 v18, v15, v8 offset0:134 offset1:199
	v_add_u32_e32 v8, 0x800, v12
	s_and_b64 s[4:5], vcc, s[4:5]
	ds_write2_b32 v8, v29, v28 offset0:8 offset1:73
	ds_write2_b32 v8, v27, v26 offset0:138 offset1:203
	v_add_u32_e32 v8, 0xc00, v12
	s_cmp_lt_i32 s47, s76
	ds_write2_b32 v8, v25, v24 offset0:12 offset1:77
	ds_write2_b32 v8, v23, v22 offset0:142 offset1:207
	v_add_u32_e32 v8, 0x1000, v12
	s_waitcnt vmcnt(4)
	v_cndmask_b32_e64 v72, 0, v72, s[4:5]
	s_cselect_b64 s[4:5], -1, 0
	ds_write2_b32 v8, v37, v36 offset0:16 offset1:81
	ds_write2_b32 v8, v35, v34 offset0:146 offset1:211
	v_add_u32_e32 v8, 0x1400, v12
	s_and_b64 s[4:5], vcc, s[4:5]
	ds_write2_b32 v8, v33, v32 offset0:20 offset1:85
	ds_write2_b32 v8, v31, v30 offset0:150 offset1:215
	v_add_u32_e32 v8, 0x1800, v12
	s_cmp_lt_i32 s48, s76
	ds_write2_b32 v8, v45, v44 offset0:24 offset1:89
	ds_write2_b32 v8, v43, v42 offset0:154 offset1:219
	v_add_u32_e32 v8, 0x1c00, v12
	s_waitcnt vmcnt(3)
	v_cndmask_b32_e64 v71, 0, v71, s[4:5]
	s_cselect_b64 s[4:5], -1, 0
	ds_write2_b32 v8, v41, v40 offset0:28 offset1:93
	ds_write2_b32 v8, v39, v38 offset0:158 offset1:223
	v_add_u32_e32 v8, 0x2000, v12
	s_and_b64 s[4:5], vcc, s[4:5]
	ds_write2_b32 v8, v53, v52 offset0:32 offset1:97
	ds_write2_b32 v8, v51, v50 offset0:162 offset1:227
	v_add_u32_e32 v8, 0x2400, v12
	s_cmp_lt_i32 s49, s76
	ds_write2_b32 v8, v49, v48 offset0:36 offset1:101
	ds_write2_b32 v8, v47, v46 offset0:166 offset1:231
	v_add_u32_e32 v8, 0x2800, v12
	s_waitcnt vmcnt(2)
	v_cndmask_b32_e64 v77, 0, v77, s[4:5]
	s_cselect_b64 s[4:5], -1, 0
	ds_write2_b32 v8, v61, v60 offset0:40 offset1:105
	ds_write2_b32 v8, v59, v58 offset0:170 offset1:235
	v_add_u32_e32 v8, 0x2c00, v12
	s_and_b64 s[4:5], vcc, s[4:5]
	ds_write2_b32 v8, v57, v56 offset0:44 offset1:109
	ds_write2_b32 v8, v55, v54 offset0:174 offset1:239
	v_add_u32_e32 v8, 0x3000, v12
	s_cmp_lt_i32 s44, s76
	ds_write2_b32 v8, v70, v69 offset0:48 offset1:113
	ds_write2_b32 v8, v68, v67 offset0:178 offset1:243
	v_add_u32_e32 v8, 0x3400, v12
	s_waitcnt vmcnt(1)
	v_cndmask_b32_e64 v76, 0, v76, s[4:5]
	s_cselect_b64 s[4:5], -1, 0
	ds_write2_b32 v8, v66, v64 offset0:52 offset1:117
	ds_write2_b32 v8, v63, v62 offset0:182 offset1:247
	v_add_u32_e32 v8, 0x3800, v12
	s_and_b64 vcc, vcc, s[4:5]
	ds_write2_b32 v8, v65, v74 offset0:56 offset1:121
	ds_write2_b32 v8, v73, v72 offset0:186 offset1:251
	v_add_u32_e32 v8, 0x3c00, v12
	s_waitcnt vmcnt(0)
	v_cndmask_b32_e32 v75, 0, v75, vcc
	ds_write2_b32 v8, v71, v77 offset0:60 offset1:125
	ds_write2_b32 v8, v76, v75 offset0:190 offset1:255
	s_waitcnt lgkmcnt(0)
; __device__ __forceinline__ unsigned cvt_pk_bf16(float lo, float hi) { unsigned r; asm volatile("v_cvt_pk_bf16_f32 %0, %1, %2" : "=v"(r) : "v"(lo), "v"(hi)); return r; }
; #define LAS __attribute__((address_space(3)))
; __device__ __forceinline__ void conv_store(const ConvItem& ci, LAS float* scr, int lane, const float (&v)[64]) {
;     ...
;     for (int j = 0; j < 8; ++j) { const int n = (lane >> 3) + 8 * j; const LAS float* s = scr + (8 * c) * 65 + n;
;         v4u o; o.x = cvt_pk_bf16(s[0 * 65] * s0[0], s[1 * 65] * s0[1]); o.y = cvt_pk_bf16(s[2 * 65] * s0[2], s[3 * 65] * s0[3]); o.z = cvt_pk_bf16(s[4 * 65] * s1[0], s[5 * 65] * s1[1]); o.w = cvt_pk_bf16(s[6 * 65] * s1[2], s[7 * 65] * s1[3]);
;         *(v4u*)(ci.dst + (size_t)(ci.drow0 + n) * ci.ldd + ci.k0 + 8 * c) = o; }
	v_add_u32_e32 v192, 0x400, v14
	ds_read2_b32 v[128:129], v14 offset1:65
	ds_read2_b32 v[130:131], v14 offset0:130 offset1:195
	ds_read2_b32 v[132:133], v192 offset0:4 offset1:69
	ds_read2_b32 v[134:135], v192 offset0:134 offset1:199
	ds_read2_b32 v[136:137], v14 offset0:8 offset1:73
	ds_read2_b32 v[138:139], v14 offset0:138 offset1:203
	ds_read2_b32 v[140:141], v192 offset0:12 offset1:77
	ds_read2_b32 v[142:143], v192 offset0:142 offset1:207
	ds_read2_b32 v[144:145], v14 offset0:16 offset1:81
	ds_read2_b32 v[146:147], v14 offset0:146 offset1:211
	ds_read2_b32 v[148:149], v192 offset0:20 offset1:85
	ds_read2_b32 v[150:151], v192 offset0:150 offset1:215
	ds_read2_b32 v[152:153], v14 offset0:24 offset1:89
	ds_read2_b32 v[154:155], v14 offset0:154 offset1:219
	ds_read2_b32 v[156:157], v192 offset0:28 offset1:93
	ds_read2_b32 v[158:159], v192 offset0:158 offset1:223
	ds_read2_b32 v[160:161], v14 offset0:32 offset1:97
	ds_read2_b32 v[162:163], v14 offset0:162 offset1:227
	ds_read2_b32 v[164:165], v192 offset0:36 offset1:101
	ds_read2_b32 v[166:167], v192 offset0:166 offset1:231
	ds_read2_b32 v[168:169], v14 offset0:40 offset1:105
	ds_read2_b32 v[170:171], v14 offset0:170 offset1:235
	ds_read2_b32 v[172:173], v192 offset0:44 offset1:109
	ds_read2_b32 v[174:175], v192 offset0:174 offset1:239
	ds_read2_b32 v[176:177], v14 offset0:48 offset1:113
	ds_read2_b32 v[178:179], v14 offset0:178 offset1:243
	ds_read2_b32 v[180:181], v192 offset0:52 offset1:117
	ds_read2_b32 v[182:183], v192 offset0:182 offset1:247
	ds_read2_b32 v[184:185], v14 offset0:56 offset1:121
	ds_read2_b32 v[186:187], v14 offset0:186 offset1:251
	ds_read2_b32 v[188:189], v192 offset0:60 offset1:125
	ds_read2_b32 v[190:191], v192 offset0:190 offset1:255
	s_waitcnt lgkmcnt(0)
	v_add_u32_e32 v24, s59, v13
	v_mul_lo_u32 v22, s57, v24
	s_ashr_i32 s59, s58, 31
	v_readlane_b32 s76, v254, 31
	s_waitcnt lgkmcnt(0)
	v_mul_f32_e32 v8, v4, v128
	v_mul_f32_e32 v15, v5, v129
	v_cvt_pk_bf16_f32 v16, v8, v15
	s_add_i32 s3, s3, s33
	s_add_i32 s66, s66, s67
	s_add_i32 s68, s68, s69
	s_add_i32 s70, s70, s71
	s_waitcnt lgkmcnt(0)
	v_mul_f32_e32 v15, v7, v131
	v_mul_f32_e32 v8, v6, v130
	v_cvt_pk_bf16_f32 v17, v8, v15
	v_add_u32_e32 v15, 0x400, v14
	s_add_i32 s72, s72, s73
	s_add_i32 s74, s74, s75
	v_readlane_b32 s78, v254, 33
	v_readlane_b32 s79, v254, 34
	s_waitcnt lgkmcnt(0)
	v_mul_f32_e32 v8, v0, v132
	v_mul_f32_e32 v18, v1, v133
	v_cvt_pk_bf16_f32 v18, v8, v18
	v_readlane_b32 s80, v255, 21
	v_readlane_b32 s77, v254, 32
	s_movk_i32 s78, 0x1580
	v_readlane_b32 s82, v255, 23
	s_waitcnt lgkmcnt(0)
	v_mul_f32_e32 v8, v2, v134
	v_mul_f32_e32 v19, v3, v135
	v_cvt_pk_bf16_f32 v19, v8, v19
	v_ashrrev_i32_e32 v8, 31, v24
	v_mul_lo_u32 v8, s56, v8
	v_mad_u64_u32 v[20:21], s[4:5], s56, v24, 0
	v_add3_u32 v21, v21, v8, v22
	v_lshl_add_u64 v[20:21], v[20:21], 1, s[60:61]
	s_lshl_b64 s[4:5], s[58:59], 1
	v_lshl_add_u64 v[20:21], v[20:21], 0, s[4:5]
	v_lshlrev_b32_e32 v8, 1, v10
	v_lshl_add_u64 v[20:21], v[20:21], 0, v[8:9]
	global_store_dwordx4 v[20:21], v[16:19], off
	s_cmpk_lt_i32 s3, 21440
	v_readlane_b32 s83, v255, 24
	s_waitcnt lgkmcnt(0)
	v_mul_f32_e32 v16, v4, v136
	v_mul_f32_e32 v17, v5, v137
	v_cvt_pk_bf16_f32 v16, v16, v17
	s_mov_b32 s79, 0x3f22f983
	s_mov_b32 s85, 0xbfc90fda
	s_brev_b32 s86, 1
	s_movk_i32 s87, 0x1f8
	s_waitcnt lgkmcnt(0)
	v_mul_f32_e32 v17, v6, v138
	v_mul_f32_e32 v18, v7, v139
	v_cvt_pk_bf16_f32 v17, v17, v18
	s_mov_b64 s[88:89], 0x80
	s_mov_b64 s[92:93], 0x4000
	s_mov_b64 s[94:95], 0x4800
	v_readlane_b32 s81, v255, 22
	s_waitcnt lgkmcnt(0)
	v_mul_f32_e32 v18, v0, v140
	v_mul_f32_e32 v19, v1, v141
	v_cvt_pk_bf16_f32 v18, v18, v19
	s_waitcnt lgkmcnt(0)
	v_mul_f32_e32 v19, v2, v142
	v_mul_f32_e32 v20, v3, v143
	v_cvt_pk_bf16_f32 v19, v19, v20
	v_add_u32_e32 v20, 8, v24
	v_ashrrev_i32_e32 v21, 31, v20
	v_mul_lo_u32 v22, s56, v21
	v_mul_lo_u32 v23, s57, v20
	v_mad_u64_u32 v[20:21], s[6:7], s56, v20, 0
	v_add3_u32 v21, v21, v22, v23
	v_lshl_add_u64 v[20:21], v[20:21], 1, s[60:61]
	v_lshl_add_u64 v[20:21], v[20:21], 0, s[4:5]
	v_lshl_add_u64 v[20:21], v[20:21], 0, v[8:9]
	global_store_dwordx4 v[20:21], v[16:19], off
	s_waitcnt lgkmcnt(0)
	s_nop 0
	v_mul_f32_e32 v16, v4, v144
	v_mul_f32_e32 v17, v5, v145
	v_cvt_pk_bf16_f32 v16, v16, v17
	s_waitcnt lgkmcnt(0)
	v_mul_f32_e32 v17, v6, v146
	v_mul_f32_e32 v18, v7, v147
	v_cvt_pk_bf16_f32 v17, v17, v18
	s_waitcnt lgkmcnt(0)
	v_mul_f32_e32 v18, v0, v148
	v_mul_f32_e32 v19, v1, v149
	v_cvt_pk_bf16_f32 v18, v18, v19
	s_waitcnt lgkmcnt(0)
; __device__ __forceinline__ unsigned cvt_pk_bf16(float lo, float hi) { unsigned r; asm volatile("v_cvt_pk_bf16_f32 %0, %1, %2" : "=v"(r) : "v"(lo), "v"(hi)); return r; }
; #define LAS __attribute__((address_space(3)))
; #define LDS_WAIT() asm volatile("s_waitcnt lgkmcnt(0)" ::: "memory")
; __device__ __forceinline__ void conv_store(const ConvItem& ci, LAS float* scr, int lane, const float (&v)[64]) {
;     ...
;     for (int j = 0; j < 8; ++j) { const int n = (lane >> 3) + 8 * j; const LAS float* s = scr + (8 * c) * 65 + n;
;         v4u o; o.x = cvt_pk_bf16(s[0 * 65] * s0[0], s[1 * 65] * s0[1]); o.y = cvt_pk_bf16(s[2 * 65] * s0[2], s[3 * 65] * s0[3]); o.z = cvt_pk_bf16(s[4 * 65] * s1[0], s[5 * 65] * s1[1]); o.w = cvt_pk_bf16(s[6 * 65] * s1[2], s[7 * 65] * s1[3]);
;         *(v4u*)(ci.dst + (size_t)(ci.drow0 + n) * ci.ldd + ci.k0 + 8 * c) = o; }
;     LDS_WAIT(); asm volatile("" ::: "memory");
	v_mul_f32_e32 v19, v2, v150
	v_mul_f32_e32 v20, v3, v151
	v_cvt_pk_bf16_f32 v19, v19, v20
	v_add_u32_e32 v20, 16, v24
	v_ashrrev_i32_e32 v21, 31, v20
	v_mul_lo_u32 v22, s56, v21
	v_mul_lo_u32 v23, s57, v20
	v_mad_u64_u32 v[20:21], s[6:7], s56, v20, 0
	v_add3_u32 v21, v21, v22, v23
	v_lshl_add_u64 v[20:21], v[20:21], 1, s[60:61]
	v_lshl_add_u64 v[20:21], v[20:21], 0, s[4:5]
	v_lshl_add_u64 v[20:21], v[20:21], 0, v[8:9]
	global_store_dwordx4 v[20:21], v[16:19], off
	s_waitcnt lgkmcnt(0)
	s_nop 0
	v_mul_f32_e32 v16, v4, v152
	v_mul_f32_e32 v17, v5, v153
	v_cvt_pk_bf16_f32 v16, v16, v17
	s_waitcnt lgkmcnt(0)
	v_mul_f32_e32 v17, v6, v154
	v_mul_f32_e32 v18, v7, v155
	v_cvt_pk_bf16_f32 v17, v17, v18
	s_waitcnt lgkmcnt(0)
	v_mul_f32_e32 v18, v0, v156
	v_mul_f32_e32 v19, v1, v157
	v_cvt_pk_bf16_f32 v18, v18, v19
	s_waitcnt lgkmcnt(0)
	v_mul_f32_e32 v19, v2, v158
	v_mul_f32_e32 v20, v3, v159
	v_cvt_pk_bf16_f32 v19, v19, v20
	v_add_u32_e32 v20, 24, v24
	v_ashrrev_i32_e32 v21, 31, v20
	v_mul_lo_u32 v22, s56, v21
	v_mul_lo_u32 v23, s57, v20
	v_mad_u64_u32 v[20:21], s[6:7], s56, v20, 0
	v_add3_u32 v21, v21, v22, v23
	v_lshl_add_u64 v[20:21], v[20:21], 1, s[60:61]
	v_lshl_add_u64 v[20:21], v[20:21], 0, s[4:5]
	v_lshl_add_u64 v[20:21], v[20:21], 0, v[8:9]
	global_store_dwordx4 v[20:21], v[16:19], off
	s_waitcnt lgkmcnt(0)
	s_nop 0
	v_mul_f32_e32 v16, v4, v160
	v_mul_f32_e32 v17, v5, v161
	v_cvt_pk_bf16_f32 v16, v16, v17
	s_waitcnt lgkmcnt(0)
	v_mul_f32_e32 v17, v6, v162
	v_mul_f32_e32 v18, v7, v163
	v_cvt_pk_bf16_f32 v17, v17, v18
	s_waitcnt lgkmcnt(0)
	v_mul_f32_e32 v18, v0, v164
	v_mul_f32_e32 v19, v1, v165
	v_cvt_pk_bf16_f32 v18, v18, v19
	s_waitcnt lgkmcnt(0)
	v_mul_f32_e32 v19, v2, v166
	v_mul_f32_e32 v20, v3, v167
	v_cvt_pk_bf16_f32 v19, v19, v20
	v_add_u32_e32 v20, 32, v24
	v_ashrrev_i32_e32 v21, 31, v20
	v_mul_lo_u32 v22, s56, v21
	v_mul_lo_u32 v23, s57, v20
	v_mad_u64_u32 v[20:21], s[6:7], s56, v20, 0
	v_add3_u32 v21, v21, v22, v23
	v_lshl_add_u64 v[20:21], v[20:21], 1, s[60:61]
	v_lshl_add_u64 v[20:21], v[20:21], 0, s[4:5]
	v_lshl_add_u64 v[20:21], v[20:21], 0, v[8:9]
	global_store_dwordx4 v[20:21], v[16:19], off
	s_waitcnt lgkmcnt(0)
	s_nop 0
	v_mul_f32_e32 v16, v4, v168
	v_mul_f32_e32 v17, v5, v169
	v_cvt_pk_bf16_f32 v16, v16, v17
	s_waitcnt lgkmcnt(0)
	v_mul_f32_e32 v17, v6, v170
	v_mul_f32_e32 v18, v7, v171
	v_cvt_pk_bf16_f32 v17, v17, v18
	s_waitcnt lgkmcnt(0)
	v_mul_f32_e32 v18, v0, v172
	v_mul_f32_e32 v19, v1, v173
	v_cvt_pk_bf16_f32 v18, v18, v19
	s_waitcnt lgkmcnt(0)
	v_mul_f32_e32 v19, v2, v174
	v_mul_f32_e32 v20, v3, v175
	v_cvt_pk_bf16_f32 v19, v19, v20
	v_add_u32_e32 v20, 40, v24
	v_ashrrev_i32_e32 v21, 31, v20
	v_mul_lo_u32 v22, s56, v21
	v_mul_lo_u32 v23, s57, v20
	v_mad_u64_u32 v[20:21], s[6:7], s56, v20, 0
	v_add3_u32 v21, v21, v22, v23
	v_lshl_add_u64 v[20:21], v[20:21], 1, s[60:61]
	v_lshl_add_u64 v[20:21], v[20:21], 0, s[4:5]
	v_lshl_add_u64 v[20:21], v[20:21], 0, v[8:9]
	global_store_dwordx4 v[20:21], v[16:19], off
	s_waitcnt lgkmcnt(0)
	s_nop 0
	v_mul_f32_e32 v16, v4, v176
	v_mul_f32_e32 v17, v5, v177
	v_cvt_pk_bf16_f32 v16, v16, v17
	s_waitcnt lgkmcnt(0)
	v_mul_f32_e32 v17, v6, v178
	v_mul_f32_e32 v18, v7, v179
	v_cvt_pk_bf16_f32 v17, v17, v18
	s_waitcnt lgkmcnt(0)
	v_mul_f32_e32 v18, v0, v180
	v_mul_f32_e32 v19, v1, v181
	v_cvt_pk_bf16_f32 v18, v18, v19
	s_waitcnt lgkmcnt(0)
	v_mul_f32_e32 v19, v2, v182
	v_mul_f32_e32 v20, v3, v183
	v_cvt_pk_bf16_f32 v19, v19, v20
	v_add_u32_e32 v20, 48, v24
	v_ashrrev_i32_e32 v21, 31, v20
	v_mul_lo_u32 v22, s56, v21
	v_mul_lo_u32 v23, s57, v20
	v_mad_u64_u32 v[20:21], s[6:7], s56, v20, 0
	v_add3_u32 v21, v21, v22, v23
	v_lshl_add_u64 v[20:21], v[20:21], 1, s[60:61]
	v_lshl_add_u64 v[20:21], v[20:21], 0, s[4:5]
	v_lshl_add_u64 v[20:21], v[20:21], 0, v[8:9]
	global_store_dwordx4 v[20:21], v[16:19], off
	s_waitcnt lgkmcnt(0)
	v_mul_f32_e32 v4, v4, v184
	v_mul_f32_e32 v5, v5, v185
	v_cvt_pk_bf16_f32 v4, v4, v5
	s_waitcnt lgkmcnt(0)
	v_mul_f32_e32 v5, v6, v186
	v_mul_f32_e32 v6, v7, v187
	v_cvt_pk_bf16_f32 v5, v5, v6
	s_waitcnt lgkmcnt(0)
	v_mul_f32_e32 v0, v0, v188
	v_mul_f32_e32 v1, v1, v189
	v_cvt_pk_bf16_f32 v6, v0, v1
	s_waitcnt lgkmcnt(0)
	v_mul_f32_e32 v0, v2, v190
	v_mul_f32_e32 v1, v3, v191
	v_cvt_pk_bf16_f32 v7, v0, v1
	v_add_u32_e32 v0, 56, v24
	v_ashrrev_i32_e32 v1, 31, v0
	v_mul_lo_u32 v2, s56, v1
	v_mul_lo_u32 v3, s57, v0
	v_mad_u64_u32 v[0:1], s[6:7], s56, v0, 0
	v_add3_u32 v1, v1, v2, v3
	v_lshl_add_u64 v[0:1], v[0:1], 1, s[60:61]
	v_lshl_add_u64 v[0:1], v[0:1], 0, s[4:5]
	v_lshl_add_u64 v[0:1], v[0:1], 0, v[8:9]
	global_store_dwordx4 v[0:1], v[4:7], off
	s_waitcnt lgkmcnt(0)
	s_cbranch_scc0 .Lcvp0c_ret

; __device__ __forceinline__ void conv_load(const ConvItem& ci, int lane, float (&v)[64]) {
;     ...
;     for (int i = 0; i < 64; ++i) { const int k = ci.k0 + i, kk = k < kmax ? k : kmax; v[i] = __builtin_nontemporal_load(base + (size_t)kk * ci.ldw); }
; #pragma unroll
;     for (int i = 0; i < 64; ++i) v[i] = (okc && (ci.k0 + i) < ci.Ksrc) ? v[i] : 0.f;
.Lcvp10_30:
	s_cmp_lt_i32 s58, s76
	s_cselect_b64 s[4:5], -1, 0
	s_and_b64 s[4:5], vcc, s[4:5]
	s_cmp_lt_i32 s64, s76
	s_waitcnt vmcnt(62)
	v_cndmask_b32_e64 v21, 0, v21, s[4:5]
	s_cselect_b64 s[4:5], -1, 0
	s_and_b64 s[4:5], vcc, s[4:5]
	s_cmp_lt_i32 s65, s76
	v_cndmask_b32_e64 v20, 0, v20, s[4:5]
	s_cselect_b64 s[4:5], -1, 0
	s_and_b64 s[4:5], vcc, s[4:5]
	s_cmp_lt_i32 s78, s76
	s_waitcnt vmcnt(61)
	v_cndmask_b32_e64 v19, 0, v19, s[4:5]
	s_cselect_b64 s[4:5], -1, 0
	s_and_b64 s[4:5], vcc, s[4:5]
	s_cmp_lt_i32 s79, s76
	s_waitcnt vmcnt(60)
	v_cndmask_b32_e64 v18, 0, v18, s[4:5]
	s_cselect_b64 s[4:5], -1, 0
	s_and_b64 s[4:5], vcc, s[4:5]
	s_cmp_lt_i32 s80, s76
	s_waitcnt vmcnt(59)
	v_cndmask_b32_e64 v17, 0, v17, s[4:5]
	s_cselect_b64 s[4:5], -1, 0
	s_and_b64 s[4:5], vcc, s[4:5]
	s_cmp_lt_i32 s81, s76
	s_waitcnt vmcnt(58)
	v_cndmask_b32_e64 v16, 0, v16, s[4:5]
	s_cselect_b64 s[4:5], -1, 0
	s_and_b64 s[4:5], vcc, s[4:5]
	s_cmp_lt_i32 s82, s76
	s_waitcnt vmcnt(57)
	v_cndmask_b32_e64 v15, 0, v15, s[4:5]
	s_cselect_b64 s[4:5], -1, 0
	s_and_b64 s[4:5], vcc, s[4:5]
	s_cmp_lt_i32 s83, s76
	s_waitcnt vmcnt(56)
	v_cndmask_b32_e64 v8, 0, v8, s[4:5]
	s_cselect_b64 s[4:5], -1, 0
	s_and_b64 s[4:5], vcc, s[4:5]
	s_cmp_lt_i32 s85, s76
	s_waitcnt vmcnt(55)
	v_cndmask_b32_e64 v29, 0, v29, s[4:5]
	s_cselect_b64 s[4:5], -1, 0
	s_and_b64 s[4:5], vcc, s[4:5]
	s_cmp_lt_i32 s86, s76
	s_waitcnt vmcnt(54)
	v_cndmask_b32_e64 v28, 0, v28, s[4:5]
	s_cselect_b64 s[4:5], -1, 0
	s_and_b64 s[4:5], vcc, s[4:5]
	s_cmp_lt_i32 s87, s76
	s_waitcnt vmcnt(53)
	v_cndmask_b32_e64 v27, 0, v27, s[4:5]
	s_cselect_b64 s[4:5], -1, 0
	s_and_b64 s[4:5], vcc, s[4:5]
	s_cmp_lt_i32 s88, s76
	s_waitcnt vmcnt(52)
	v_cndmask_b32_e64 v26, 0, v26, s[4:5]
	s_cselect_b64 s[4:5], -1, 0
	s_and_b64 s[4:5], vcc, s[4:5]
	s_cmp_lt_i32 s89, s76
	s_waitcnt vmcnt(51)
	v_cndmask_b32_e64 v25, 0, v25, s[4:5]
	s_cselect_b64 s[4:5], -1, 0
	s_and_b64 s[4:5], vcc, s[4:5]
	s_cmp_lt_i32 s90, s76
	s_waitcnt vmcnt(50)
	v_cndmask_b32_e64 v24, 0, v24, s[4:5]
	s_cselect_b64 s[4:5], -1, 0
	s_and_b64 s[4:5], vcc, s[4:5]
	s_cmp_lt_i32 s92, s76
	s_waitcnt vmcnt(49)
	v_cndmask_b32_e64 v23, 0, v23, s[4:5]
	s_cselect_b64 s[4:5], -1, 0
	s_and_b64 s[4:5], vcc, s[4:5]
	s_cmp_lt_i32 s93, s76
	s_waitcnt vmcnt(48)
	v_cndmask_b32_e64 v22, 0, v22, s[4:5]
	s_cselect_b64 s[4:5], -1, 0
	s_and_b64 s[4:5], vcc, s[4:5]
	s_cmp_lt_i32 s94, s76
	s_waitcnt vmcnt(47)
	v_cndmask_b32_e64 v37, 0, v37, s[4:5]
	s_cselect_b64 s[4:5], -1, 0
	s_and_b64 s[4:5], vcc, s[4:5]
	s_cmp_lt_i32 s95, s76
	s_waitcnt vmcnt(46)
	v_cndmask_b32_e64 v36, 0, v36, s[4:5]
	s_cselect_b64 s[4:5], -1, 0
	s_and_b64 s[4:5], vcc, s[4:5]
	s_cmp_lt_i32 s50, s76
	s_waitcnt vmcnt(45)
	v_cndmask_b32_e64 v35, 0, v35, s[4:5]
	s_cselect_b64 s[4:5], -1, 0
	s_and_b64 s[4:5], vcc, s[4:5]
	s_cmp_lt_i32 s51, s76
	s_waitcnt vmcnt(44)
	v_cndmask_b32_e64 v34, 0, v34, s[4:5]
	s_cselect_b64 s[4:5], -1, 0
	s_and_b64 s[4:5], vcc, s[4:5]
	s_cmp_lt_i32 s52, s76
	s_waitcnt vmcnt(43)
	v_cndmask_b32_e64 v33, 0, v33, s[4:5]
	s_cselect_b64 s[4:5], -1, 0
	s_and_b64 s[4:5], vcc, s[4:5]
	s_cmp_lt_i32 s53, s76
	s_waitcnt vmcnt(42)
	v_cndmask_b32_e64 v32, 0, v32, s[4:5]
	s_cselect_b64 s[4:5], -1, 0
	s_and_b64 s[4:5], vcc, s[4:5]
	s_cmp_lt_i32 s6, s76
	s_waitcnt vmcnt(41)
	v_cndmask_b32_e64 v31, 0, v31, s[4:5]
	s_cselect_b64 s[4:5], -1, 0
	s_and_b64 s[4:5], vcc, s[4:5]
	s_cmp_lt_i32 s7, s76
	s_waitcnt vmcnt(40)
	v_cndmask_b32_e64 v30, 0, v30, s[4:5]
	s_cselect_b64 s[4:5], -1, 0
	s_and_b64 s[4:5], vcc, s[4:5]
	s_cmp_lt_i32 s8, s76
	s_waitcnt vmcnt(39)
	v_cndmask_b32_e64 v45, 0, v45, s[4:5]
	s_cselect_b64 s[4:5], -1, 0
	s_and_b64 s[4:5], vcc, s[4:5]
	s_cmp_lt_i32 s9, s76
	s_waitcnt vmcnt(38)
	v_cndmask_b32_e64 v44, 0, v44, s[4:5]
	s_cselect_b64 s[4:5], -1, 0
	s_and_b64 s[4:5], vcc, s[4:5]
	s_cmp_lt_i32 s10, s76
	s_waitcnt vmcnt(37)
	v_cndmask_b32_e64 v43, 0, v43, s[4:5]
	s_cselect_b64 s[4:5], -1, 0
	s_and_b64 s[4:5], vcc, s[4:5]
	s_cmp_lt_i32 s11, s76
	s_waitcnt vmcnt(36)
	v_cndmask_b32_e64 v42, 0, v42, s[4:5]
	s_cselect_b64 s[4:5], -1, 0
	s_and_b64 s[4:5], vcc, s[4:5]
	s_cmp_lt_i32 s14, s76
	s_waitcnt vmcnt(35)
	v_cndmask_b32_e64 v41, 0, v41, s[4:5]
	s_cselect_b64 s[4:5], -1, 0
	s_and_b64 s[4:5], vcc, s[4:5]
	s_cmp_lt_i32 s15, s76
	s_waitcnt vmcnt(34)
	v_cndmask_b32_e64 v40, 0, v40, s[4:5]
	s_cselect_b64 s[4:5], -1, 0
	s_and_b64 s[4:5], vcc, s[4:5]
	s_cmp_lt_i32 s16, s76
	s_waitcnt vmcnt(33)
	v_cndmask_b32_e64 v39, 0, v39, s[4:5]
	s_cselect_b64 s[4:5], -1, 0
	s_and_b64 s[4:5], vcc, s[4:5]
	s_cmp_lt_i32 s17, s76
	s_waitcnt vmcnt(32)
	v_cndmask_b32_e64 v38, 0, v38, s[4:5]
	s_cselect_b64 s[4:5], -1, 0
	s_and_b64 s[4:5], vcc, s[4:5]
	s_cmp_lt_i32 s12, s76
	s_waitcnt vmcnt(31)
	v_cndmask_b32_e64 v53, 0, v53, s[4:5]
	s_cselect_b64 s[4:5], -1, 0
	s_and_b64 s[4:5], vcc, s[4:5]
	s_cmp_lt_i32 s13, s76
	s_waitcnt vmcnt(30)
	v_cndmask_b32_e64 v52, 0, v52, s[4:5]
	s_cselect_b64 s[4:5], -1, 0
	s_and_b64 s[4:5], vcc, s[4:5]
	s_cmp_lt_i32 s20, s76
	s_waitcnt vmcnt(29)
	v_cndmask_b32_e64 v51, 0, v51, s[4:5]
	s_cselect_b64 s[4:5], -1, 0
	s_and_b64 s[4:5], vcc, s[4:5]
	s_cmp_lt_i32 s21, s76
	s_waitcnt vmcnt(28)
	v_cndmask_b32_e64 v50, 0, v50, s[4:5]
	s_cselect_b64 s[4:5], -1, 0
	s_and_b64 s[4:5], vcc, s[4:5]
	s_cmp_lt_i32 s24, s76
	s_waitcnt vmcnt(27)
	v_cndmask_b32_e64 v49, 0, v49, s[4:5]
	s_cselect_b64 s[4:5], -1, 0
	s_and_b64 s[4:5], vcc, s[4:5]
	s_cmp_lt_i32 s25, s76
	s_waitcnt vmcnt(26)
	v_cndmask_b32_e64 v48, 0, v48, s[4:5]
	s_cselect_b64 s[4:5], -1, 0
	s_and_b64 s[4:5], vcc, s[4:5]
	s_cmp_lt_i32 s26, s76
	s_waitcnt vmcnt(25)
	v_cndmask_b32_e64 v47, 0, v47, s[4:5]
	s_cselect_b64 s[4:5], -1, 0
	s_and_b64 s[4:5], vcc, s[4:5]
	s_cmp_lt_i32 s27, s76
	s_waitcnt vmcnt(24)
; #define LAS __attribute__((address_space(3)))
; #define LDS_WAIT() asm volatile("s_waitcnt lgkmcnt(0)" ::: "memory")
; __device__ __forceinline__ void conv_load(const ConvItem& ci, int lane, float (&v)[64]) {
;     ...
;     for (int i = 0; i < 64; ++i) v[i] = (okc && (ci.k0 + i) < ci.Ksrc) ? v[i] : 0.f;
; }
; __device__ __forceinline__ void conv_store(const ConvItem& ci, LAS float* scr, int lane, const float (&v)[64]) {
;     const int c = lane & 7;
;     f32x4 s0 = {1.f, 1.f, 1.f, 1.f}, s1 = s0;
;     if (ci.ks) { const int kb = ci.k0 + 8 * c < ci.Ksrc - 8 ? ci.k0 + 8 * c : ci.Ksrc - 8; s0 = *(const f32x4*)(ci.ks + kb); s1 = *(const f32x4*)(ci.ks + kb + 4); }
; #pragma unroll
;     for (int i = 0; i < 64; ++i) scr[i * 65 + lane] = v[i];
;     LDS_WAIT(); asm volatile("" ::: "memory");
	v_cndmask_b32_e64 v46, 0, v46, s[4:5]
	s_cselect_b64 s[4:5], -1, 0
	s_and_b64 s[4:5], vcc, s[4:5]
	s_cmp_lt_i32 s18, s76
	s_waitcnt vmcnt(23)
	v_cndmask_b32_e64 v61, 0, v61, s[4:5]
	s_cselect_b64 s[4:5], -1, 0
	s_and_b64 s[4:5], vcc, s[4:5]
	s_cmp_lt_i32 s19, s76
	s_waitcnt vmcnt(22)
	v_cndmask_b32_e64 v60, 0, v60, s[4:5]
	s_cselect_b64 s[4:5], -1, 0
	s_and_b64 s[4:5], vcc, s[4:5]
	s_cmp_lt_i32 s28, s76
	s_waitcnt vmcnt(21)
	v_cndmask_b32_e64 v59, 0, v59, s[4:5]
	s_cselect_b64 s[4:5], -1, 0
	s_and_b64 s[4:5], vcc, s[4:5]
	s_cmp_lt_i32 s29, s76
	s_waitcnt vmcnt(20)
	v_cndmask_b32_e64 v58, 0, v58, s[4:5]
	s_cselect_b64 s[4:5], -1, 0
	s_and_b64 s[4:5], vcc, s[4:5]
	s_cmp_lt_i32 s22, s76
	s_waitcnt vmcnt(19)
	v_cndmask_b32_e64 v57, 0, v57, s[4:5]
	s_cselect_b64 s[4:5], -1, 0
	s_and_b64 s[4:5], vcc, s[4:5]
	s_cmp_lt_i32 s23, s76
	s_waitcnt vmcnt(18)
	v_cndmask_b32_e64 v56, 0, v56, s[4:5]
	s_cselect_b64 s[4:5], -1, 0
	s_and_b64 s[4:5], vcc, s[4:5]
	s_cmp_lt_i32 s30, s76
	s_waitcnt vmcnt(17)
	v_cndmask_b32_e64 v55, 0, v55, s[4:5]
	s_cselect_b64 s[4:5], -1, 0
	s_and_b64 s[4:5], vcc, s[4:5]
	s_cmp_lt_i32 s31, s76
	s_waitcnt vmcnt(16)
	v_cndmask_b32_e64 v54, 0, v54, s[4:5]
	s_cselect_b64 s[4:5], -1, 0
	s_and_b64 s[4:5], vcc, s[4:5]
	s_cmp_lt_i32 s36, s76
	s_waitcnt vmcnt(15)
	v_cndmask_b32_e64 v70, 0, v70, s[4:5]
	s_cselect_b64 s[4:5], -1, 0
	s_and_b64 s[4:5], vcc, s[4:5]
	s_cmp_lt_i32 s37, s76
	s_waitcnt vmcnt(14)
	v_cndmask_b32_e64 v69, 0, v69, s[4:5]
	s_cselect_b64 s[4:5], -1, 0
	s_and_b64 s[4:5], vcc, s[4:5]
	s_cmp_lt_i32 s38, s76
	s_waitcnt vmcnt(13)
	v_cndmask_b32_e64 v68, 0, v68, s[4:5]
	s_cselect_b64 s[4:5], -1, 0
	s_and_b64 s[4:5], vcc, s[4:5]
	s_cmp_lt_i32 s39, s76
	s_waitcnt vmcnt(12)
	v_cndmask_b32_e64 v67, 0, v67, s[4:5]
	s_cselect_b64 s[4:5], -1, 0
	s_and_b64 s[4:5], vcc, s[4:5]
	s_cmp_lt_i32 s34, s76
	s_waitcnt vmcnt(11)
	v_cndmask_b32_e64 v66, 0, v66, s[4:5]
	s_cselect_b64 s[4:5], -1, 0
	s_and_b64 s[4:5], vcc, s[4:5]
	s_cmp_lt_i32 s35, s76
	s_waitcnt vmcnt(10)
	v_cndmask_b32_e64 v64, 0, v64, s[4:5]
	s_cselect_b64 s[4:5], -1, 0
	s_and_b64 s[4:5], vcc, s[4:5]
	s_cmp_lt_i32 s42, s76
	s_waitcnt vmcnt(9)
	v_cndmask_b32_e64 v63, 0, v63, s[4:5]
	s_cselect_b64 s[4:5], -1, 0
	s_and_b64 s[4:5], vcc, s[4:5]
	s_cmp_lt_i32 s43, s76
	s_waitcnt vmcnt(8)
	v_cndmask_b32_e64 v62, 0, v62, s[4:5]
	s_cselect_b64 s[4:5], -1, 0
	s_and_b64 s[4:5], vcc, s[4:5]
	s_cmp_lt_i32 s54, s76
	s_waitcnt vmcnt(7)
	v_cndmask_b32_e64 v65, 0, v65, s[4:5]
	s_cselect_b64 s[4:5], -1, 0
	s_and_b64 s[4:5], vcc, s[4:5]
	s_cmp_lt_i32 s55, s76
	s_waitcnt vmcnt(6)
	v_cndmask_b32_e64 v74, 0, v74, s[4:5]
	s_cselect_b64 s[4:5], -1, 0
	s_and_b64 s[4:5], vcc, s[4:5]
	s_cmp_lt_i32 s46, s76
	ds_write2_b32 v12, v21, v20 offset1:65
	ds_write2_b32 v12, v19, v18 offset0:130 offset1:195
	v_add_u32_e32 v18, 0x400, v12
	s_waitcnt vmcnt(5)
	v_cndmask_b32_e64 v73, 0, v73, s[4:5]
	s_cselect_b64 s[4:5], -1, 0
	ds_write2_b32 v18, v17, v16 offset0:4 offset1:69
	ds_write2_b32 v18, v15, v8 offset0:134 offset1:199
	v_add_u32_e32 v8, 0x800, v12
	s_and_b64 s[4:5], vcc, s[4:5]
	ds_write2_b32 v8, v29, v28 offset0:8 offset1:73
	ds_write2_b32 v8, v27, v26 offset0:138 offset1:203
	v_add_u32_e32 v8, 0xc00, v12
	s_cmp_lt_i32 s47, s76
	ds_write2_b32 v8, v25, v24 offset0:12 offset1:77
	ds_write2_b32 v8, v23, v22 offset0:142 offset1:207
	v_add_u32_e32 v8, 0x1000, v12
	s_waitcnt vmcnt(4)
	v_cndmask_b32_e64 v72, 0, v72, s[4:5]
	s_cselect_b64 s[4:5], -1, 0
	ds_write2_b32 v8, v37, v36 offset0:16 offset1:81
	ds_write2_b32 v8, v35, v34 offset0:146 offset1:211
	v_add_u32_e32 v8, 0x1400, v12
	s_and_b64 s[4:5], vcc, s[4:5]
	ds_write2_b32 v8, v33, v32 offset0:20 offset1:85
	ds_write2_b32 v8, v31, v30 offset0:150 offset1:215
	v_add_u32_e32 v8, 0x1800, v12
	s_cmp_lt_i32 s48, s76
	ds_write2_b32 v8, v45, v44 offset0:24 offset1:89
	ds_write2_b32 v8, v43, v42 offset0:154 offset1:219
	v_add_u32_e32 v8, 0x1c00, v12
	s_waitcnt vmcnt(3)
	v_cndmask_b32_e64 v71, 0, v71, s[4:5]
	s_cselect_b64 s[4:5], -1, 0
	ds_write2_b32 v8, v41, v40 offset0:28 offset1:93
	ds_write2_b32 v8, v39, v38 offset0:158 offset1:223
	v_add_u32_e32 v8, 0x2000, v12
	s_and_b64 s[4:5], vcc, s[4:5]
	ds_write2_b32 v8, v53, v52 offset0:32 offset1:97
	ds_write2_b32 v8, v51, v50 offset0:162 offset1:227
	v_add_u32_e32 v8, 0x2400, v12
	s_cmp_lt_i32 s49, s76
	ds_write2_b32 v8, v49, v48 offset0:36 offset1:101
	ds_write2_b32 v8, v47, v46 offset0:166 offset1:231
	v_add_u32_e32 v8, 0x2800, v12
	s_waitcnt vmcnt(2)
	v_cndmask_b32_e64 v77, 0, v77, s[4:5]
	s_cselect_b64 s[4:5], -1, 0
	ds_write2_b32 v8, v61, v60 offset0:40 offset1:105
	ds_write2_b32 v8, v59, v58 offset0:170 offset1:235
	v_add_u32_e32 v8, 0x2c00, v12
	s_and_b64 s[4:5], vcc, s[4:5]
	ds_write2_b32 v8, v57, v56 offset0:44 offset1:109
	ds_write2_b32 v8, v55, v54 offset0:174 offset1:239
	v_add_u32_e32 v8, 0x3000, v12
	s_cmp_lt_i32 s44, s76
	ds_write2_b32 v8, v70, v69 offset0:48 offset1:113
	ds_write2_b32 v8, v68, v67 offset0:178 offset1:243
	v_add_u32_e32 v8, 0x3400, v12
	s_waitcnt vmcnt(1)
	v_cndmask_b32_e64 v76, 0, v76, s[4:5]
	s_cselect_b64 s[4:5], -1, 0
	ds_write2_b32 v8, v66, v64 offset0:52 offset1:117
	ds_write2_b32 v8, v63, v62 offset0:182 offset1:247
	v_add_u32_e32 v8, 0x3800, v12
	s_and_b64 vcc, vcc, s[4:5]
	ds_write2_b32 v8, v65, v74 offset0:56 offset1:121
	ds_write2_b32 v8, v73, v72 offset0:186 offset1:251
	v_add_u32_e32 v8, 0x3c00, v12
	s_waitcnt vmcnt(0)
	v_cndmask_b32_e32 v75, 0, v75, vcc
	ds_write2_b32 v8, v71, v77 offset0:60 offset1:125
	ds_write2_b32 v8, v76, v75 offset0:190 offset1:255
	s_waitcnt lgkmcnt(0)
; __device__ __forceinline__ unsigned cvt_pk_bf16(float lo, float hi) { unsigned r; asm volatile("v_cvt_pk_bf16_f32 %0, %1, %2" : "=v"(r) : "v"(lo), "v"(hi)); return r; }
; #define LAS __attribute__((address_space(3)))
; __device__ __forceinline__ void conv_store(const ConvItem& ci, LAS float* scr, int lane, const float (&v)[64]) {
;     ...
;     for (int j = 0; j < 8; ++j) { const int n = (lane >> 3) + 8 * j; const LAS float* s = scr + (8 * c) * 65 + n;
;         v4u o; o.x = cvt_pk_bf16(s[0 * 65] * s0[0], s[1 * 65] * s0[1]); o.y = cvt_pk_bf16(s[2 * 65] * s0[2], s[3 * 65] * s0[3]); o.z = cvt_pk_bf16(s[4 * 65] * s1[0], s[5 * 65] * s1[1]); o.w = cvt_pk_bf16(s[6 * 65] * s1[2], s[7 * 65] * s1[3]);
;         *(v4u*)(ci.dst + (size_t)(ci.drow0 + n) * ci.ldd + ci.k0 + 8 * c) = o; }
	v_add_u32_e32 v192, 0x400, v14
	ds_read2_b32 v[128:129], v14 offset1:65
	ds_read2_b32 v[130:131], v14 offset0:130 offset1:195
	ds_read2_b32 v[132:133], v192 offset0:4 offset1:69
	ds_read2_b32 v[134:135], v192 offset0:134 offset1:199
	ds_read2_b32 v[136:137], v14 offset0:8 offset1:73
	ds_read2_b32 v[138:139], v14 offset0:138 offset1:203
	ds_read2_b32 v[140:141], v192 offset0:12 offset1:77
	ds_read2_b32 v[142:143], v192 offset0:142 offset1:207
	ds_read2_b32 v[144:145], v14 offset0:16 offset1:81
	ds_read2_b32 v[146:147], v14 offset0:146 offset1:211
	ds_read2_b32 v[148:149], v192 offset0:20 offset1:85
	ds_read2_b32 v[150:151], v192 offset0:150 offset1:215
	ds_read2_b32 v[152:153], v14 offset0:24 offset1:89
	ds_read2_b32 v[154:155], v14 offset0:154 offset1:219
	ds_read2_b32 v[156:157], v192 offset0:28 offset1:93
	ds_read2_b32 v[158:159], v192 offset0:158 offset1:223
	ds_read2_b32 v[160:161], v14 offset0:32 offset1:97
	ds_read2_b32 v[162:163], v14 offset0:162 offset1:227
	ds_read2_b32 v[164:165], v192 offset0:36 offset1:101
	ds_read2_b32 v[166:167], v192 offset0:166 offset1:231
	ds_read2_b32 v[168:169], v14 offset0:40 offset1:105
	ds_read2_b32 v[170:171], v14 offset0:170 offset1:235
	ds_read2_b32 v[172:173], v192 offset0:44 offset1:109
	ds_read2_b32 v[174:175], v192 offset0:174 offset1:239
	ds_read2_b32 v[176:177], v14 offset0:48 offset1:113
	ds_read2_b32 v[178:179], v14 offset0:178 offset1:243
	ds_read2_b32 v[180:181], v192 offset0:52 offset1:117
	ds_read2_b32 v[182:183], v192 offset0:182 offset1:247
	ds_read2_b32 v[184:185], v14 offset0:56 offset1:121
	ds_read2_b32 v[186:187], v14 offset0:186 offset1:251
	ds_read2_b32 v[188:189], v192 offset0:60 offset1:125
	ds_read2_b32 v[190:191], v192 offset0:190 offset1:255
	s_waitcnt lgkmcnt(0)
	v_add_u32_e32 v24, s59, v13
	v_mul_lo_u32 v22, s57, v24
	s_ashr_i32 s59, s58, 31
	v_readlane_b32 s76, v254, 31
	s_waitcnt lgkmcnt(0)
	v_mul_f32_e32 v8, v4, v128
	v_mul_f32_e32 v15, v5, v129
	v_cvt_pk_bf16_f32 v16, v8, v15
	s_add_i32 s3, s3, s33
	s_add_i32 s66, s66, s67
	s_add_i32 s68, s68, s69
	s_add_i32 s70, s70, s71
	s_waitcnt lgkmcnt(0)
	v_mul_f32_e32 v15, v7, v131
	v_mul_f32_e32 v8, v6, v130
	v_cvt_pk_bf16_f32 v17, v8, v15
	v_add_u32_e32 v15, 0x400, v14
	s_add_i32 s72, s72, s73
	s_add_i32 s74, s74, s75
	v_readlane_b32 s78, v254, 33
	v_readlane_b32 s79, v254, 34
	s_waitcnt lgkmcnt(0)
	v_mul_f32_e32 v8, v0, v132
	v_mul_f32_e32 v18, v1, v133
	v_cvt_pk_bf16_f32 v18, v8, v18
	v_readlane_b32 s80, v255, 21
	v_readlane_b32 s77, v254, 32
	s_movk_i32 s78, 0x1580
	v_readlane_b32 s82, v255, 23
	s_waitcnt lgkmcnt(0)
	v_mul_f32_e32 v8, v2, v134
	v_mul_f32_e32 v19, v3, v135
	v_cvt_pk_bf16_f32 v19, v8, v19
	v_ashrrev_i32_e32 v8, 31, v24
	v_mul_lo_u32 v8, s56, v8
	v_mad_u64_u32 v[20:21], s[4:5], s56, v24, 0
	v_add3_u32 v21, v21, v8, v22
	v_lshl_add_u64 v[20:21], v[20:21], 1, s[60:61]
	s_lshl_b64 s[4:5], s[58:59], 1
	v_lshl_add_u64 v[20:21], v[20:21], 0, s[4:5]
	v_lshlrev_b32_e32 v8, 1, v10
	v_lshl_add_u64 v[20:21], v[20:21], 0, v[8:9]
	global_store_dwordx4 v[20:21], v[16:19], off
	s_cmpk_lt_i32 s3, 11008
	v_readlane_b32 s83, v255, 24
	s_waitcnt lgkmcnt(0)
	v_mul_f32_e32 v16, v4, v136
	v_mul_f32_e32 v17, v5, v137
	v_cvt_pk_bf16_f32 v16, v16, v17
	s_mov_b32 s79, 0x3f22f983
	s_mov_b32 s85, 0xbfc90fda
	s_brev_b32 s86, 1
	s_movk_i32 s87, 0x1f8
	s_waitcnt lgkmcnt(0)
	v_mul_f32_e32 v17, v6, v138
	v_mul_f32_e32 v18, v7, v139
	v_cvt_pk_bf16_f32 v17, v17, v18
	s_mov_b64 s[88:89], 0x80
	s_mov_b64 s[92:93], 0x4000
	s_mov_b64 s[94:95], 0x4800
	v_readlane_b32 s81, v255, 22
	s_waitcnt lgkmcnt(0)
	v_mul_f32_e32 v18, v0, v140
	v_mul_f32_e32 v19, v1, v141
	v_cvt_pk_bf16_f32 v18, v18, v19
	s_waitcnt lgkmcnt(0)
	v_mul_f32_e32 v19, v2, v142
	v_mul_f32_e32 v20, v3, v143
	v_cvt_pk_bf16_f32 v19, v19, v20
	v_add_u32_e32 v20, 8, v24
	v_ashrrev_i32_e32 v21, 31, v20
	v_mul_lo_u32 v22, s56, v21
	v_mul_lo_u32 v23, s57, v20
	v_mad_u64_u32 v[20:21], s[6:7], s56, v20, 0
	v_add3_u32 v21, v21, v22, v23
	v_lshl_add_u64 v[20:21], v[20:21], 1, s[60:61]
	v_lshl_add_u64 v[20:21], v[20:21], 0, s[4:5]
	v_lshl_add_u64 v[20:21], v[20:21], 0, v[8:9]
	global_store_dwordx4 v[20:21], v[16:19], off
	s_waitcnt lgkmcnt(0)
	s_nop 0
	v_mul_f32_e32 v16, v4, v144
	v_mul_f32_e32 v17, v5, v145
	v_cvt_pk_bf16_f32 v16, v16, v17
	s_waitcnt lgkmcnt(0)
	v_mul_f32_e32 v17, v6, v146
	v_mul_f32_e32 v18, v7, v147
	v_cvt_pk_bf16_f32 v17, v17, v18
	s_waitcnt lgkmcnt(0)
	v_mul_f32_e32 v18, v0, v148
	v_mul_f32_e32 v19, v1, v149
	v_cvt_pk_bf16_f32 v18, v18, v19
	s_waitcnt lgkmcnt(0)
; __device__ __forceinline__ unsigned cvt_pk_bf16(float lo, float hi) { unsigned r; asm volatile("v_cvt_pk_bf16_f32 %0, %1, %2" : "=v"(r) : "v"(lo), "v"(hi)); return r; }
; #define LAS __attribute__((address_space(3)))
; #define LDS_WAIT() asm volatile("s_waitcnt lgkmcnt(0)" ::: "memory")
; __device__ __forceinline__ void conv_store(const ConvItem& ci, LAS float* scr, int lane, const float (&v)[64]) {
;     ...
;     for (int j = 0; j < 8; ++j) { const int n = (lane >> 3) + 8 * j; const LAS float* s = scr + (8 * c) * 65 + n;
;         v4u o; o.x = cvt_pk_bf16(s[0 * 65] * s0[0], s[1 * 65] * s0[1]); o.y = cvt_pk_bf16(s[2 * 65] * s0[2], s[3 * 65] * s0[3]); o.z = cvt_pk_bf16(s[4 * 65] * s1[0], s[5 * 65] * s1[1]); o.w = cvt_pk_bf16(s[6 * 65] * s1[2], s[7 * 65] * s1[3]);
;         *(v4u*)(ci.dst + (size_t)(ci.drow0 + n) * ci.ldd + ci.k0 + 8 * c) = o; }
;     LDS_WAIT(); asm volatile("" ::: "memory");
	v_mul_f32_e32 v19, v2, v150
	v_mul_f32_e32 v20, v3, v151
	v_cvt_pk_bf16_f32 v19, v19, v20
	v_add_u32_e32 v20, 16, v24
	v_ashrrev_i32_e32 v21, 31, v20
	v_mul_lo_u32 v22, s56, v21
	v_mul_lo_u32 v23, s57, v20
	v_mad_u64_u32 v[20:21], s[6:7], s56, v20, 0
	v_add3_u32 v21, v21, v22, v23
	v_lshl_add_u64 v[20:21], v[20:21], 1, s[60:61]
	v_lshl_add_u64 v[20:21], v[20:21], 0, s[4:5]
	v_lshl_add_u64 v[20:21], v[20:21], 0, v[8:9]
	global_store_dwordx4 v[20:21], v[16:19], off
	s_waitcnt lgkmcnt(0)
	s_nop 0
	v_mul_f32_e32 v16, v4, v152
	v_mul_f32_e32 v17, v5, v153
	v_cvt_pk_bf16_f32 v16, v16, v17
	s_waitcnt lgkmcnt(0)
	v_mul_f32_e32 v17, v6, v154
	v_mul_f32_e32 v18, v7, v155
	v_cvt_pk_bf16_f32 v17, v17, v18
	s_waitcnt lgkmcnt(0)
	v_mul_f32_e32 v18, v0, v156
	v_mul_f32_e32 v19, v1, v157
	v_cvt_pk_bf16_f32 v18, v18, v19
	s_waitcnt lgkmcnt(0)
	v_mul_f32_e32 v19, v2, v158
	v_mul_f32_e32 v20, v3, v159
	v_cvt_pk_bf16_f32 v19, v19, v20
	v_add_u32_e32 v20, 24, v24
	v_ashrrev_i32_e32 v21, 31, v20
	v_mul_lo_u32 v22, s56, v21
	v_mul_lo_u32 v23, s57, v20
	v_mad_u64_u32 v[20:21], s[6:7], s56, v20, 0
	v_add3_u32 v21, v21, v22, v23
	v_lshl_add_u64 v[20:21], v[20:21], 1, s[60:61]
	v_lshl_add_u64 v[20:21], v[20:21], 0, s[4:5]
	v_lshl_add_u64 v[20:21], v[20:21], 0, v[8:9]
	global_store_dwordx4 v[20:21], v[16:19], off
	s_waitcnt lgkmcnt(0)
	s_nop 0
	v_mul_f32_e32 v16, v4, v160
	v_mul_f32_e32 v17, v5, v161
	v_cvt_pk_bf16_f32 v16, v16, v17
	s_waitcnt lgkmcnt(0)
	v_mul_f32_e32 v17, v6, v162
	v_mul_f32_e32 v18, v7, v163
	v_cvt_pk_bf16_f32 v17, v17, v18
	s_waitcnt lgkmcnt(0)
	v_mul_f32_e32 v18, v0, v164
	v_mul_f32_e32 v19, v1, v165
	v_cvt_pk_bf16_f32 v18, v18, v19
	s_waitcnt lgkmcnt(0)
	v_mul_f32_e32 v19, v2, v166
	v_mul_f32_e32 v20, v3, v167
	v_cvt_pk_bf16_f32 v19, v19, v20
	v_add_u32_e32 v20, 32, v24
	v_ashrrev_i32_e32 v21, 31, v20
	v_mul_lo_u32 v22, s56, v21
	v_mul_lo_u32 v23, s57, v20
	v_mad_u64_u32 v[20:21], s[6:7], s56, v20, 0
	v_add3_u32 v21, v21, v22, v23
	v_lshl_add_u64 v[20:21], v[20:21], 1, s[60:61]
	v_lshl_add_u64 v[20:21], v[20:21], 0, s[4:5]
	v_lshl_add_u64 v[20:21], v[20:21], 0, v[8:9]
	global_store_dwordx4 v[20:21], v[16:19], off
	s_waitcnt lgkmcnt(0)
	s_nop 0
	v_mul_f32_e32 v16, v4, v168
	v_mul_f32_e32 v17, v5, v169
	v_cvt_pk_bf16_f32 v16, v16, v17
	s_waitcnt lgkmcnt(0)
	v_mul_f32_e32 v17, v6, v170
	v_mul_f32_e32 v18, v7, v171
	v_cvt_pk_bf16_f32 v17, v17, v18
	s_waitcnt lgkmcnt(0)
	v_mul_f32_e32 v18, v0, v172
	v_mul_f32_e32 v19, v1, v173
	v_cvt_pk_bf16_f32 v18, v18, v19
	s_waitcnt lgkmcnt(0)
	v_mul_f32_e32 v19, v2, v174
	v_mul_f32_e32 v20, v3, v175
	v_cvt_pk_bf16_f32 v19, v19, v20
	v_add_u32_e32 v20, 40, v24
	v_ashrrev_i32_e32 v21, 31, v20
	v_mul_lo_u32 v22, s56, v21
	v_mul_lo_u32 v23, s57, v20
	v_mad_u64_u32 v[20:21], s[6:7], s56, v20, 0
	v_add3_u32 v21, v21, v22, v23
	v_lshl_add_u64 v[20:21], v[20:21], 1, s[60:61]
	v_lshl_add_u64 v[20:21], v[20:21], 0, s[4:5]
	v_lshl_add_u64 v[20:21], v[20:21], 0, v[8:9]
	global_store_dwordx4 v[20:21], v[16:19], off
	s_waitcnt lgkmcnt(0)
	s_nop 0
	v_mul_f32_e32 v16, v4, v176
	v_mul_f32_e32 v17, v5, v177
	v_cvt_pk_bf16_f32 v16, v16, v17
	s_waitcnt lgkmcnt(0)
	v_mul_f32_e32 v17, v6, v178
	v_mul_f32_e32 v18, v7, v179
	v_cvt_pk_bf16_f32 v17, v17, v18
	s_waitcnt lgkmcnt(0)
	v_mul_f32_e32 v18, v0, v180
	v_mul_f32_e32 v19, v1, v181
	v_cvt_pk_bf16_f32 v18, v18, v19
	s_waitcnt lgkmcnt(0)
	v_mul_f32_e32 v19, v2, v182
	v_mul_f32_e32 v20, v3, v183
	v_cvt_pk_bf16_f32 v19, v19, v20
	v_add_u32_e32 v20, 48, v24
	v_ashrrev_i32_e32 v21, 31, v20
	v_mul_lo_u32 v22, s56, v21
	v_mul_lo_u32 v23, s57, v20
	v_mad_u64_u32 v[20:21], s[6:7], s56, v20, 0
	v_add3_u32 v21, v21, v22, v23
	v_lshl_add_u64 v[20:21], v[20:21], 1, s[60:61]
	v_lshl_add_u64 v[20:21], v[20:21], 0, s[4:5]
	v_lshl_add_u64 v[20:21], v[20:21], 0, v[8:9]
	global_store_dwordx4 v[20:21], v[16:19], off
	s_waitcnt lgkmcnt(0)
	v_mul_f32_e32 v4, v4, v184
	v_mul_f32_e32 v5, v5, v185
	v_cvt_pk_bf16_f32 v4, v4, v5
	s_waitcnt lgkmcnt(0)
	v_mul_f32_e32 v5, v6, v186
	v_mul_f32_e32 v6, v7, v187
	v_cvt_pk_bf16_f32 v5, v5, v6
	s_waitcnt lgkmcnt(0)
	v_mul_f32_e32 v0, v0, v188
	v_mul_f32_e32 v1, v1, v189
	v_cvt_pk_bf16_f32 v6, v0, v1
	s_waitcnt lgkmcnt(0)
	v_mul_f32_e32 v0, v2, v190
	v_mul_f32_e32 v1, v3, v191
	v_cvt_pk_bf16_f32 v7, v0, v1
	v_add_u32_e32 v0, 56, v24
	v_ashrrev_i32_e32 v1, 31, v0
	v_mul_lo_u32 v2, s56, v1
	v_mul_lo_u32 v3, s57, v0
	v_mad_u64_u32 v[0:1], s[6:7], s56, v0, 0
	v_add3_u32 v1, v1, v2, v3
	v_lshl_add_u64 v[0:1], v[0:1], 1, s[60:61]
	v_lshl_add_u64 v[0:1], v[0:1], 0, s[4:5]
	v_lshl_add_u64 v[0:1], v[0:1], 0, v[8:9]
	global_store_dwordx4 v[0:1], v[4:7], off
	s_waitcnt lgkmcnt(0)
	s_cbranch_scc0 .Lcvp10_ret

; __global__ void __launch_bounds__(NWAVES * 64, 2) mk_fwd(Args args) {
;     ...
;             constexpr int I_UP = (D / 64) * (NUP / 64), I_DN = (DFF / 64) * (D / 64), I_IN = (D / 64) * (DINP / 64), I_GLU = 16 * 16, I_L = 4 * 16, I_V1 = 16 * 4, I_V2 = 4 * 16,
;                           I_BS5 = 16 * 32, I_BAT = 8 * 32, I_BRW = 16 * 32, I_OUT = 32 * 32;
;             constexpr int NITEMS = 2 * I_UP + 2 * I_DN + I_IN + I_GLU + 3 * I_L + I_V1 + I_V2 + I_BS5 + I_BAT + I_BRW + I_OUT;
;             const int lv = l > 0 ? l - 1 : 0;
;     ...
;             for (int it = gw; it < NITEMS; it += NGW) {
.Lcvp10_ret:
.Lcvrs_p10:
	v_readlane_b32 s0, v254, 8
	v_readlane_b32 s4, v254, 10
	v_readlane_b32 s1, v254, 9
	v_mbcnt_lo_u32_b32 v11, -1, 0
	v_mbcnt_hi_u32_b32 v11, -1, v11
	s_load_dword s6, s[0:1], 0x0
	s_mov_b32 s3, s84
	s_waitcnt lgkmcnt(0)
	s_movk_i32 s6, 160
	s_lshl_b32 s3, s3, 3
	v_readlane_b32 s0, v254, 0
	s_add_i32 s3, s3, s4
	s_add_i32 s3, s3, 0x50c0
	v_readlane_b32 s1, v254, 1
	s_cmpk_gt_i32 s3, 25215
	s_cbranch_scc1 .Lcvp11_ret
	s_load_dwordx2 s[8:9], s[0:1], 0x138
	v_readlane_b32 s14, v254, 38
	s_mulk_i32 s4, 0x4100
	s_add_i32 s7, s4, 0
	v_sub_u32_e64 v0, s14, 1 clamp
	s_lshl_b32 s33, s6, 3
	v_readfirstlane_b32 s4, v0
	s_lshl_b32 s96, s4, 16
	s_waitcnt lgkmcnt(0)
	s_add_u32 s4, s8, 0x22800000
	s_addc_u32 s5, s9, 0
	v_writelane_b32 v254, s4, 39
	s_mov_b32 s15, s97
	v_and_b32_e32 v0, 7, v11
	v_writelane_b32 v254, s5, 40
	s_add_u32 s4, s8, 0x22780000
	s_addc_u32 s5, s9, 0
	v_writelane_b32 v254, s4, 41
	v_ashrrev_i32_e32 v13, 3, v11
	v_lshlrev_b32_e32 v10, 3, v0
	v_writelane_b32 v254, s5, 42
	s_lshl_b32 s4, s14, 18
	s_add_u32 s10, s8, 0x22700000
	s_addc_u32 s11, s9, 0
	v_writelane_b32 v254, s10, 43
	s_mov_b32 s5, s97
	v_mul_u32_u24_e32 v0, 0x820, v0
	v_writelane_b32 v254, s11, 44
	s_mul_i32 s10, s14, 0x18000
	s_mov_b32 s11, s97
	v_writelane_b32 v254, s10, 45
	v_lshlrev_b32_e32 v1, 2, v13
	v_lshl_add_u32 v12, v11, 2, s7
	v_writelane_b32 v254, s11, 46
	s_add_u32 s10, s8, 0x22680000
	s_addc_u32 s11, s9, 0
	v_writelane_b32 v254, s10, 47
	v_add3_u32 v14, s7, v0, v1
	s_mov_b32 s41, s97
	v_writelane_b32 v254, s11, 48
	s_add_u32 s10, s8, 0x22600000
	s_addc_u32 s11, s9, 0
	v_writelane_b32 v254, s10, 49
	s_nop 1
	v_writelane_b32 v254, s11, 50
	s_lshl_b32 s10, s14, 20
	s_mov_b32 s11, s97
	v_writelane_b32 v254, s10, 51
	s_nop 1
	v_writelane_b32 v254, s11, 52
	s_add_u32 s10, s8, 0x22400000
	s_addc_u32 s11, s9, 0
	v_writelane_b32 v254, s10, 53
	s_nop 1
	v_writelane_b32 v254, s11, 54
	s_lshl_b32 s10, s14, 21
	s_mov_b32 s11, s97
	v_writelane_b32 v254, s10, 55
	s_nop 1
	v_writelane_b32 v254, s11, 56
	s_add_u32 s10, s8, 0x22e80000
	s_addc_u32 s11, s9, 0
	v_writelane_b32 v254, s10, 57
	s_nop 1
	v_writelane_b32 v254, s11, 58
	s_add_u32 s10, s8, 0x27b80000
	s_addc_u32 s11, s9, 0
	v_writelane_b32 v254, s10, 59
	s_nop 1
	v_writelane_b32 v254, s11, 60
	s_add_u32 s10, s8, 0x22880000
	s_addc_u32 s11, s9, 0
	v_writelane_b32 v254, s10, 61
	s_nop 1
	v_writelane_b32 v254, s11, 62
	s_lshl_b32 s10, s14, 22
	s_add_u32 s12, s8, 0x23280000
	s_addc_u32 s13, s9, 0
	v_writelane_b32 v254, s12, 63
	s_mov_b32 s11, s97
	s_nop 0
	v_writelane_b32 v255, s13, 0
	s_mul_i32 s12, s14, 0xac0000
	s_mov_b32 s13, s97
	v_writelane_b32 v255, s12, 1
	s_nop 1
	v_writelane_b32 v255, s13, 2
	s_add_u32 s12, s8, 0x26580000
	s_addc_u32 s13, s9, 0
	v_writelane_b32 v255, s12, 3
	s_nop 1
	v_writelane_b32 v255, s13, 4
	s_add_u32 s12, s8, 0x1d200000
	s_addc_u32 s13, s9, 0
	s_lshl_b32 s40, s14, 11
	v_writelane_b32 v255, s12, 5
	s_add_u32 s16, s8, 0x1e800000
	s_addc_u32 s17, s9, 0
	v_writelane_b32 v255, s13, 6
	v_writelane_b32 v255, s16, 7
	s_mul_i32 s12, s14, 0x1de0000
	s_mul_i32 s14, s14, 0x1580000
	v_writelane_b32 v255, s17, 8
	v_writelane_b32 v255, s14, 9
	s_mov_b32 s13, s97
	s_nop 0
	v_writelane_b32 v255, s15, 10
	s_add_u32 s14, s8, 0x23a80000
	s_addc_u32 s15, s9, 0
	v_writelane_b32 v255, s14, 11
	s_add_u32 s8, s8, 0x1a700000
	s_addc_u32 s9, s9, 0
	v_writelane_b32 v255, s15, 12
	v_writelane_b32 v255, s8, 13
	s_lshl_b64 s[4:5], s[4:5], 2
	s_lshl_b32 s7, s3, 4
	v_writelane_b32 v255, s9, 14
	v_writelane_b32 v255, s4, 15
	s_add_i32 s72, s7, 0xc00
	s_lshl_b32 s7, s3, 1
	v_writelane_b32 v255, s5, 16
	s_lshl_b64 s[4:5], s[10:11], 2
	v_writelane_b32 v255, s4, 17
	s_lshl_b32 s66, s3, 6
	s_lshl_b32 s67, s6, 9
	v_writelane_b32 v255, s5, 18
	s_lshl_b64 s[4:5], s[12:13], 2
	v_writelane_b32 v255, s4, 19
	s_lshl_b32 s68, s3, 5
	s_lshl_b32 s69, s6, 8
	v_writelane_b32 v255, s5, 20
	v_writelane_b32 v255, s80, 21
	s_lshl_b32 s70, s3, 2
	s_lshl_b32 s71, s6, 5
	v_writelane_b32 v255, s81, 22
	v_writelane_b32 v255, s82, 23
	s_lshl_b32 s73, s6, 7
	s_add_i32 s74, s7, 0x13500
	s_lshl_b32 s75, s6, 4
	v_writelane_b32 v255, s83, 24
	s_branch .Lcvp11_31

; __device__ __forceinline__ void conv_load(const ConvItem& ci, int lane, float (&v)[64]) {
;     ...
;     for (int i = 0; i < 64; ++i) { const int k = ci.k0 + i, kk = k < kmax ? k : kmax; v[i] = __builtin_nontemporal_load(base + (size_t)kk * ci.ldw); }
; #pragma unroll
;     for (int i = 0; i < 64; ++i) v[i] = (okc && (ci.k0 + i) < ci.Ksrc) ? v[i] : 0.f;
.Lcvp11_30:
	s_cmp_lt_i32 s58, s76
	s_cselect_b64 s[4:5], -1, 0
	s_and_b64 s[4:5], vcc, s[4:5]
	s_cmp_lt_i32 s64, s76
	s_waitcnt vmcnt(62)
	v_cndmask_b32_e64 v21, 0, v21, s[4:5]
	s_cselect_b64 s[4:5], -1, 0
	s_and_b64 s[4:5], vcc, s[4:5]
	s_cmp_lt_i32 s65, s76
	v_cndmask_b32_e64 v20, 0, v20, s[4:5]
	s_cselect_b64 s[4:5], -1, 0
	s_and_b64 s[4:5], vcc, s[4:5]
	s_cmp_lt_i32 s78, s76
	s_waitcnt vmcnt(61)
	v_cndmask_b32_e64 v19, 0, v19, s[4:5]
	s_cselect_b64 s[4:5], -1, 0
	s_and_b64 s[4:5], vcc, s[4:5]
	s_cmp_lt_i32 s79, s76
	s_waitcnt vmcnt(60)
	v_cndmask_b32_e64 v18, 0, v18, s[4:5]
	s_cselect_b64 s[4:5], -1, 0
	s_and_b64 s[4:5], vcc, s[4:5]
	s_cmp_lt_i32 s80, s76
	s_waitcnt vmcnt(59)
	v_cndmask_b32_e64 v17, 0, v17, s[4:5]
	s_cselect_b64 s[4:5], -1, 0
	s_and_b64 s[4:5], vcc, s[4:5]
	s_cmp_lt_i32 s81, s76
	s_waitcnt vmcnt(58)
	v_cndmask_b32_e64 v16, 0, v16, s[4:5]
	s_cselect_b64 s[4:5], -1, 0
	s_and_b64 s[4:5], vcc, s[4:5]
	s_cmp_lt_i32 s82, s76
	s_waitcnt vmcnt(57)
	v_cndmask_b32_e64 v15, 0, v15, s[4:5]
	s_cselect_b64 s[4:5], -1, 0
	s_and_b64 s[4:5], vcc, s[4:5]
	s_cmp_lt_i32 s83, s76
	s_waitcnt vmcnt(56)
	v_cndmask_b32_e64 v8, 0, v8, s[4:5]
	s_cselect_b64 s[4:5], -1, 0
	s_and_b64 s[4:5], vcc, s[4:5]
	s_cmp_lt_i32 s85, s76
	s_waitcnt vmcnt(55)
	v_cndmask_b32_e64 v29, 0, v29, s[4:5]
	s_cselect_b64 s[4:5], -1, 0
	s_and_b64 s[4:5], vcc, s[4:5]
	s_cmp_lt_i32 s86, s76
	s_waitcnt vmcnt(54)
	v_cndmask_b32_e64 v28, 0, v28, s[4:5]
	s_cselect_b64 s[4:5], -1, 0
	s_and_b64 s[4:5], vcc, s[4:5]
	s_cmp_lt_i32 s87, s76
	s_waitcnt vmcnt(53)
	v_cndmask_b32_e64 v27, 0, v27, s[4:5]
	s_cselect_b64 s[4:5], -1, 0
	s_and_b64 s[4:5], vcc, s[4:5]
	s_cmp_lt_i32 s88, s76
	s_waitcnt vmcnt(52)
	v_cndmask_b32_e64 v26, 0, v26, s[4:5]
	s_cselect_b64 s[4:5], -1, 0
	s_and_b64 s[4:5], vcc, s[4:5]
	s_cmp_lt_i32 s89, s76
	s_waitcnt vmcnt(51)
	v_cndmask_b32_e64 v25, 0, v25, s[4:5]
	s_cselect_b64 s[4:5], -1, 0
	s_and_b64 s[4:5], vcc, s[4:5]
	s_cmp_lt_i32 s90, s76
	s_waitcnt vmcnt(50)
	v_cndmask_b32_e64 v24, 0, v24, s[4:5]
	s_cselect_b64 s[4:5], -1, 0
	s_and_b64 s[4:5], vcc, s[4:5]
	s_cmp_lt_i32 s92, s76
	s_waitcnt vmcnt(49)
	v_cndmask_b32_e64 v23, 0, v23, s[4:5]
	s_cselect_b64 s[4:5], -1, 0
	s_and_b64 s[4:5], vcc, s[4:5]
	s_cmp_lt_i32 s93, s76
	s_waitcnt vmcnt(48)
	v_cndmask_b32_e64 v22, 0, v22, s[4:5]
	s_cselect_b64 s[4:5], -1, 0
	s_and_b64 s[4:5], vcc, s[4:5]
	s_cmp_lt_i32 s94, s76
	s_waitcnt vmcnt(47)
	v_cndmask_b32_e64 v37, 0, v37, s[4:5]
	s_cselect_b64 s[4:5], -1, 0
	s_and_b64 s[4:5], vcc, s[4:5]
	s_cmp_lt_i32 s95, s76
	s_waitcnt vmcnt(46)
	v_cndmask_b32_e64 v36, 0, v36, s[4:5]
	s_cselect_b64 s[4:5], -1, 0
	s_and_b64 s[4:5], vcc, s[4:5]
	s_cmp_lt_i32 s50, s76
	s_waitcnt vmcnt(45)
	v_cndmask_b32_e64 v35, 0, v35, s[4:5]
	s_cselect_b64 s[4:5], -1, 0
	s_and_b64 s[4:5], vcc, s[4:5]
	s_cmp_lt_i32 s51, s76
	s_waitcnt vmcnt(44)
	v_cndmask_b32_e64 v34, 0, v34, s[4:5]
	s_cselect_b64 s[4:5], -1, 0
	s_and_b64 s[4:5], vcc, s[4:5]
	s_cmp_lt_i32 s52, s76
	s_waitcnt vmcnt(43)
	v_cndmask_b32_e64 v33, 0, v33, s[4:5]
	s_cselect_b64 s[4:5], -1, 0
	s_and_b64 s[4:5], vcc, s[4:5]
	s_cmp_lt_i32 s53, s76
	s_waitcnt vmcnt(42)
	v_cndmask_b32_e64 v32, 0, v32, s[4:5]
	s_cselect_b64 s[4:5], -1, 0
	s_and_b64 s[4:5], vcc, s[4:5]
	s_cmp_lt_i32 s6, s76
	s_waitcnt vmcnt(41)
	v_cndmask_b32_e64 v31, 0, v31, s[4:5]
	s_cselect_b64 s[4:5], -1, 0
	s_and_b64 s[4:5], vcc, s[4:5]
	s_cmp_lt_i32 s7, s76
	s_waitcnt vmcnt(40)
	v_cndmask_b32_e64 v30, 0, v30, s[4:5]
	s_cselect_b64 s[4:5], -1, 0
	s_and_b64 s[4:5], vcc, s[4:5]
	s_cmp_lt_i32 s8, s76
	s_waitcnt vmcnt(39)
	v_cndmask_b32_e64 v45, 0, v45, s[4:5]
	s_cselect_b64 s[4:5], -1, 0
	s_and_b64 s[4:5], vcc, s[4:5]
	s_cmp_lt_i32 s9, s76
	s_waitcnt vmcnt(38)
	v_cndmask_b32_e64 v44, 0, v44, s[4:5]
	s_cselect_b64 s[4:5], -1, 0
	s_and_b64 s[4:5], vcc, s[4:5]
	s_cmp_lt_i32 s10, s76
	s_waitcnt vmcnt(37)
	v_cndmask_b32_e64 v43, 0, v43, s[4:5]
	s_cselect_b64 s[4:5], -1, 0
	s_and_b64 s[4:5], vcc, s[4:5]
	s_cmp_lt_i32 s11, s76
	s_waitcnt vmcnt(36)
	v_cndmask_b32_e64 v42, 0, v42, s[4:5]
	s_cselect_b64 s[4:5], -1, 0
	s_and_b64 s[4:5], vcc, s[4:5]
	s_cmp_lt_i32 s14, s76
	s_waitcnt vmcnt(35)
	v_cndmask_b32_e64 v41, 0, v41, s[4:5]
	s_cselect_b64 s[4:5], -1, 0
	s_and_b64 s[4:5], vcc, s[4:5]
	s_cmp_lt_i32 s15, s76
	s_waitcnt vmcnt(34)
	v_cndmask_b32_e64 v40, 0, v40, s[4:5]
	s_cselect_b64 s[4:5], -1, 0
	s_and_b64 s[4:5], vcc, s[4:5]
	s_cmp_lt_i32 s16, s76
	s_waitcnt vmcnt(33)
	v_cndmask_b32_e64 v39, 0, v39, s[4:5]
	s_cselect_b64 s[4:5], -1, 0
	s_and_b64 s[4:5], vcc, s[4:5]
	s_cmp_lt_i32 s17, s76
	s_waitcnt vmcnt(32)
	v_cndmask_b32_e64 v38, 0, v38, s[4:5]
	s_cselect_b64 s[4:5], -1, 0
	s_and_b64 s[4:5], vcc, s[4:5]
	s_cmp_lt_i32 s12, s76
	s_waitcnt vmcnt(31)
	v_cndmask_b32_e64 v53, 0, v53, s[4:5]
	s_cselect_b64 s[4:5], -1, 0
	s_and_b64 s[4:5], vcc, s[4:5]
	s_cmp_lt_i32 s13, s76
	s_waitcnt vmcnt(30)
	v_cndmask_b32_e64 v52, 0, v52, s[4:5]
	s_cselect_b64 s[4:5], -1, 0
	s_and_b64 s[4:5], vcc, s[4:5]
	s_cmp_lt_i32 s20, s76
	s_waitcnt vmcnt(29)
	v_cndmask_b32_e64 v51, 0, v51, s[4:5]
	s_cselect_b64 s[4:5], -1, 0
	s_and_b64 s[4:5], vcc, s[4:5]
	s_cmp_lt_i32 s21, s76
	s_waitcnt vmcnt(28)
	v_cndmask_b32_e64 v50, 0, v50, s[4:5]
	s_cselect_b64 s[4:5], -1, 0
	s_and_b64 s[4:5], vcc, s[4:5]
	s_cmp_lt_i32 s24, s76
	s_waitcnt vmcnt(27)
	v_cndmask_b32_e64 v49, 0, v49, s[4:5]
	s_cselect_b64 s[4:5], -1, 0
	s_and_b64 s[4:5], vcc, s[4:5]
	s_cmp_lt_i32 s25, s76
	s_waitcnt vmcnt(26)
	v_cndmask_b32_e64 v48, 0, v48, s[4:5]
	s_cselect_b64 s[4:5], -1, 0
	s_and_b64 s[4:5], vcc, s[4:5]
	s_cmp_lt_i32 s26, s76
	s_waitcnt vmcnt(25)
	v_cndmask_b32_e64 v47, 0, v47, s[4:5]
	s_cselect_b64 s[4:5], -1, 0
	s_and_b64 s[4:5], vcc, s[4:5]
	s_cmp_lt_i32 s27, s76
	s_waitcnt vmcnt(24)
; #define LAS __attribute__((address_space(3)))
; #define LDS_WAIT() asm volatile("s_waitcnt lgkmcnt(0)" ::: "memory")
; __device__ __forceinline__ void conv_load(const ConvItem& ci, int lane, float (&v)[64]) {
;     ...
;     for (int i = 0; i < 64; ++i) v[i] = (okc && (ci.k0 + i) < ci.Ksrc) ? v[i] : 0.f;
; }
; __device__ __forceinline__ void conv_store(const ConvItem& ci, LAS float* scr, int lane, const float (&v)[64]) {
;     const int c = lane & 7;
;     f32x4 s0 = {1.f, 1.f, 1.f, 1.f}, s1 = s0;
;     if (ci.ks) { const int kb = ci.k0 + 8 * c < ci.Ksrc - 8 ? ci.k0 + 8 * c : ci.Ksrc - 8; s0 = *(const f32x4*)(ci.ks + kb); s1 = *(const f32x4*)(ci.ks + kb + 4); }
; #pragma unroll
;     for (int i = 0; i < 64; ++i) scr[i * 65 + lane] = v[i];
;     LDS_WAIT(); asm volatile("" ::: "memory");
	v_cndmask_b32_e64 v46, 0, v46, s[4:5]
	s_cselect_b64 s[4:5], -1, 0
	s_and_b64 s[4:5], vcc, s[4:5]
	s_cmp_lt_i32 s18, s76
	s_waitcnt vmcnt(23)
	v_cndmask_b32_e64 v61, 0, v61, s[4:5]
	s_cselect_b64 s[4:5], -1, 0
	s_and_b64 s[4:5], vcc, s[4:5]
	s_cmp_lt_i32 s19, s76
	s_waitcnt vmcnt(22)
	v_cndmask_b32_e64 v60, 0, v60, s[4:5]
	s_cselect_b64 s[4:5], -1, 0
	s_and_b64 s[4:5], vcc, s[4:5]
	s_cmp_lt_i32 s28, s76
	s_waitcnt vmcnt(21)
	v_cndmask_b32_e64 v59, 0, v59, s[4:5]
	s_cselect_b64 s[4:5], -1, 0
	s_and_b64 s[4:5], vcc, s[4:5]
	s_cmp_lt_i32 s29, s76
	s_waitcnt vmcnt(20)
	v_cndmask_b32_e64 v58, 0, v58, s[4:5]
	s_cselect_b64 s[4:5], -1, 0
	s_and_b64 s[4:5], vcc, s[4:5]
	s_cmp_lt_i32 s22, s76
	s_waitcnt vmcnt(19)
	v_cndmask_b32_e64 v57, 0, v57, s[4:5]
	s_cselect_b64 s[4:5], -1, 0
	s_and_b64 s[4:5], vcc, s[4:5]
	s_cmp_lt_i32 s23, s76
	s_waitcnt vmcnt(18)
	v_cndmask_b32_e64 v56, 0, v56, s[4:5]
	s_cselect_b64 s[4:5], -1, 0
	s_and_b64 s[4:5], vcc, s[4:5]
	s_cmp_lt_i32 s30, s76
	s_waitcnt vmcnt(17)
	v_cndmask_b32_e64 v55, 0, v55, s[4:5]
	s_cselect_b64 s[4:5], -1, 0
	s_and_b64 s[4:5], vcc, s[4:5]
	s_cmp_lt_i32 s31, s76
	s_waitcnt vmcnt(16)
	v_cndmask_b32_e64 v54, 0, v54, s[4:5]
	s_cselect_b64 s[4:5], -1, 0
	s_and_b64 s[4:5], vcc, s[4:5]
	s_cmp_lt_i32 s36, s76
	s_waitcnt vmcnt(15)
	v_cndmask_b32_e64 v70, 0, v70, s[4:5]
	s_cselect_b64 s[4:5], -1, 0
	s_and_b64 s[4:5], vcc, s[4:5]
	s_cmp_lt_i32 s37, s76
	s_waitcnt vmcnt(14)
	v_cndmask_b32_e64 v69, 0, v69, s[4:5]
	s_cselect_b64 s[4:5], -1, 0
	s_and_b64 s[4:5], vcc, s[4:5]
	s_cmp_lt_i32 s38, s76
	s_waitcnt vmcnt(13)
	v_cndmask_b32_e64 v68, 0, v68, s[4:5]
	s_cselect_b64 s[4:5], -1, 0
	s_and_b64 s[4:5], vcc, s[4:5]
	s_cmp_lt_i32 s39, s76
	s_waitcnt vmcnt(12)
	v_cndmask_b32_e64 v67, 0, v67, s[4:5]
	s_cselect_b64 s[4:5], -1, 0
	s_and_b64 s[4:5], vcc, s[4:5]
	s_cmp_lt_i32 s34, s76
	s_waitcnt vmcnt(11)
	v_cndmask_b32_e64 v66, 0, v66, s[4:5]
	s_cselect_b64 s[4:5], -1, 0
	s_and_b64 s[4:5], vcc, s[4:5]
	s_cmp_lt_i32 s35, s76
	s_waitcnt vmcnt(10)
	v_cndmask_b32_e64 v64, 0, v64, s[4:5]
	s_cselect_b64 s[4:5], -1, 0
	s_and_b64 s[4:5], vcc, s[4:5]
	s_cmp_lt_i32 s42, s76
	s_waitcnt vmcnt(9)
	v_cndmask_b32_e64 v63, 0, v63, s[4:5]
	s_cselect_b64 s[4:5], -1, 0
	s_and_b64 s[4:5], vcc, s[4:5]
	s_cmp_lt_i32 s43, s76
	s_waitcnt vmcnt(8)
	v_cndmask_b32_e64 v62, 0, v62, s[4:5]
	s_cselect_b64 s[4:5], -1, 0
	s_and_b64 s[4:5], vcc, s[4:5]
	s_cmp_lt_i32 s54, s76
	s_waitcnt vmcnt(7)
	v_cndmask_b32_e64 v65, 0, v65, s[4:5]
	s_cselect_b64 s[4:5], -1, 0
	s_and_b64 s[4:5], vcc, s[4:5]
	s_cmp_lt_i32 s55, s76
	s_waitcnt vmcnt(6)
	v_cndmask_b32_e64 v74, 0, v74, s[4:5]
	s_cselect_b64 s[4:5], -1, 0
	s_and_b64 s[4:5], vcc, s[4:5]
	s_cmp_lt_i32 s46, s76
	ds_write2_b32 v12, v21, v20 offset1:65
	ds_write2_b32 v12, v19, v18 offset0:130 offset1:195
	v_add_u32_e32 v18, 0x400, v12
	s_waitcnt vmcnt(5)
	v_cndmask_b32_e64 v73, 0, v73, s[4:5]
	s_cselect_b64 s[4:5], -1, 0
	ds_write2_b32 v18, v17, v16 offset0:4 offset1:69
	ds_write2_b32 v18, v15, v8 offset0:134 offset1:199
	v_add_u32_e32 v8, 0x800, v12
	s_and_b64 s[4:5], vcc, s[4:5]
	ds_write2_b32 v8, v29, v28 offset0:8 offset1:73
	ds_write2_b32 v8, v27, v26 offset0:138 offset1:203
	v_add_u32_e32 v8, 0xc00, v12
	s_cmp_lt_i32 s47, s76
	ds_write2_b32 v8, v25, v24 offset0:12 offset1:77
	ds_write2_b32 v8, v23, v22 offset0:142 offset1:207
	v_add_u32_e32 v8, 0x1000, v12
	s_waitcnt vmcnt(4)
	v_cndmask_b32_e64 v72, 0, v72, s[4:5]
	s_cselect_b64 s[4:5], -1, 0
	ds_write2_b32 v8, v37, v36 offset0:16 offset1:81
	ds_write2_b32 v8, v35, v34 offset0:146 offset1:211
	v_add_u32_e32 v8, 0x1400, v12
	s_and_b64 s[4:5], vcc, s[4:5]
	ds_write2_b32 v8, v33, v32 offset0:20 offset1:85
	ds_write2_b32 v8, v31, v30 offset0:150 offset1:215
	v_add_u32_e32 v8, 0x1800, v12
	s_cmp_lt_i32 s48, s76
	ds_write2_b32 v8, v45, v44 offset0:24 offset1:89
	ds_write2_b32 v8, v43, v42 offset0:154 offset1:219
	v_add_u32_e32 v8, 0x1c00, v12
	s_waitcnt vmcnt(3)
	v_cndmask_b32_e64 v71, 0, v71, s[4:5]
	s_cselect_b64 s[4:5], -1, 0
	ds_write2_b32 v8, v41, v40 offset0:28 offset1:93
	ds_write2_b32 v8, v39, v38 offset0:158 offset1:223
	v_add_u32_e32 v8, 0x2000, v12
	s_and_b64 s[4:5], vcc, s[4:5]
	ds_write2_b32 v8, v53, v52 offset0:32 offset1:97
	ds_write2_b32 v8, v51, v50 offset0:162 offset1:227
	v_add_u32_e32 v8, 0x2400, v12
	s_cmp_lt_i32 s49, s76
	ds_write2_b32 v8, v49, v48 offset0:36 offset1:101
	ds_write2_b32 v8, v47, v46 offset0:166 offset1:231
	v_add_u32_e32 v8, 0x2800, v12
	s_waitcnt vmcnt(2)
	v_cndmask_b32_e64 v77, 0, v77, s[4:5]
	s_cselect_b64 s[4:5], -1, 0
	ds_write2_b32 v8, v61, v60 offset0:40 offset1:105
	ds_write2_b32 v8, v59, v58 offset0:170 offset1:235
	v_add_u32_e32 v8, 0x2c00, v12
	s_and_b64 s[4:5], vcc, s[4:5]
	ds_write2_b32 v8, v57, v56 offset0:44 offset1:109
	ds_write2_b32 v8, v55, v54 offset0:174 offset1:239
	v_add_u32_e32 v8, 0x3000, v12
	s_cmp_lt_i32 s44, s76
	ds_write2_b32 v8, v70, v69 offset0:48 offset1:113
	ds_write2_b32 v8, v68, v67 offset0:178 offset1:243
	v_add_u32_e32 v8, 0x3400, v12
	s_waitcnt vmcnt(1)
	v_cndmask_b32_e64 v76, 0, v76, s[4:5]
	s_cselect_b64 s[4:5], -1, 0
	ds_write2_b32 v8, v66, v64 offset0:52 offset1:117
	ds_write2_b32 v8, v63, v62 offset0:182 offset1:247
	v_add_u32_e32 v8, 0x3800, v12
	s_and_b64 vcc, vcc, s[4:5]
	ds_write2_b32 v8, v65, v74 offset0:56 offset1:121
	ds_write2_b32 v8, v73, v72 offset0:186 offset1:251
	v_add_u32_e32 v8, 0x3c00, v12
	s_waitcnt vmcnt(0)
	v_cndmask_b32_e32 v75, 0, v75, vcc
	ds_write2_b32 v8, v71, v77 offset0:60 offset1:125
	ds_write2_b32 v8, v76, v75 offset0:190 offset1:255
	s_waitcnt lgkmcnt(0)
; __device__ __forceinline__ unsigned cvt_pk_bf16(float lo, float hi) { unsigned r; asm volatile("v_cvt_pk_bf16_f32 %0, %1, %2" : "=v"(r) : "v"(lo), "v"(hi)); return r; }
; #define LAS __attribute__((address_space(3)))
; __device__ __forceinline__ void conv_store(const ConvItem& ci, LAS float* scr, int lane, const float (&v)[64]) {
;     ...
;     for (int j = 0; j < 8; ++j) { const int n = (lane >> 3) + 8 * j; const LAS float* s = scr + (8 * c) * 65 + n;
;         v4u o; o.x = cvt_pk_bf16(s[0 * 65] * s0[0], s[1 * 65] * s0[1]); o.y = cvt_pk_bf16(s[2 * 65] * s0[2], s[3 * 65] * s0[3]); o.z = cvt_pk_bf16(s[4 * 65] * s1[0], s[5 * 65] * s1[1]); o.w = cvt_pk_bf16(s[6 * 65] * s1[2], s[7 * 65] * s1[3]);
;         *(v4u*)(ci.dst + (size_t)(ci.drow0 + n) * ci.ldd + ci.k0 + 8 * c) = o; }
	v_add_u32_e32 v192, 0x400, v14
	ds_read2_b32 v[128:129], v14 offset1:65
	ds_read2_b32 v[130:131], v14 offset0:130 offset1:195
	ds_read2_b32 v[132:133], v192 offset0:4 offset1:69
	ds_read2_b32 v[134:135], v192 offset0:134 offset1:199
	ds_read2_b32 v[136:137], v14 offset0:8 offset1:73
	ds_read2_b32 v[138:139], v14 offset0:138 offset1:203
	ds_read2_b32 v[140:141], v192 offset0:12 offset1:77
	ds_read2_b32 v[142:143], v192 offset0:142 offset1:207
	ds_read2_b32 v[144:145], v14 offset0:16 offset1:81
	ds_read2_b32 v[146:147], v14 offset0:146 offset1:211
	ds_read2_b32 v[148:149], v192 offset0:20 offset1:85
	ds_read2_b32 v[150:151], v192 offset0:150 offset1:215
	ds_read2_b32 v[152:153], v14 offset0:24 offset1:89
	ds_read2_b32 v[154:155], v14 offset0:154 offset1:219
	ds_read2_b32 v[156:157], v192 offset0:28 offset1:93
	ds_read2_b32 v[158:159], v192 offset0:158 offset1:223
	ds_read2_b32 v[160:161], v14 offset0:32 offset1:97
	ds_read2_b32 v[162:163], v14 offset0:162 offset1:227
	ds_read2_b32 v[164:165], v192 offset0:36 offset1:101
	ds_read2_b32 v[166:167], v192 offset0:166 offset1:231
	ds_read2_b32 v[168:169], v14 offset0:40 offset1:105
	ds_read2_b32 v[170:171], v14 offset0:170 offset1:235
	ds_read2_b32 v[172:173], v192 offset0:44 offset1:109
	ds_read2_b32 v[174:175], v192 offset0:174 offset1:239
	ds_read2_b32 v[176:177], v14 offset0:48 offset1:113
	ds_read2_b32 v[178:179], v14 offset0:178 offset1:243
	ds_read2_b32 v[180:181], v192 offset0:52 offset1:117
	ds_read2_b32 v[182:183], v192 offset0:182 offset1:247
	ds_read2_b32 v[184:185], v14 offset0:56 offset1:121
	ds_read2_b32 v[186:187], v14 offset0:186 offset1:251
	ds_read2_b32 v[188:189], v192 offset0:60 offset1:125
	ds_read2_b32 v[190:191], v192 offset0:190 offset1:255
	s_waitcnt lgkmcnt(0)
	v_add_u32_e32 v24, s59, v13
	v_mul_lo_u32 v22, s57, v24
	s_ashr_i32 s59, s58, 31
	v_readlane_b32 s76, v254, 31
	s_waitcnt lgkmcnt(0)
	v_mul_f32_e32 v8, v4, v128
	v_mul_f32_e32 v15, v5, v129
	v_cvt_pk_bf16_f32 v16, v8, v15
	s_add_i32 s3, s3, s33
	s_add_i32 s66, s66, s67
	s_add_i32 s68, s68, s69
	s_add_i32 s70, s70, s71
	s_waitcnt lgkmcnt(0)
	v_mul_f32_e32 v15, v7, v131
	v_mul_f32_e32 v8, v6, v130
	v_cvt_pk_bf16_f32 v17, v8, v15
	v_add_u32_e32 v15, 0x400, v14
	s_add_i32 s72, s72, s73
	s_add_i32 s74, s74, s75
	v_readlane_b32 s78, v254, 33
	v_readlane_b32 s79, v254, 34
	s_waitcnt lgkmcnt(0)
	v_mul_f32_e32 v8, v0, v132
	v_mul_f32_e32 v18, v1, v133
	v_cvt_pk_bf16_f32 v18, v8, v18
	v_readlane_b32 s80, v255, 21
	v_readlane_b32 s77, v254, 32
	s_movk_i32 s78, 0x1580
	v_readlane_b32 s82, v255, 23
	s_waitcnt lgkmcnt(0)
	v_mul_f32_e32 v8, v2, v134
	v_mul_f32_e32 v19, v3, v135
	v_cvt_pk_bf16_f32 v19, v8, v19
	v_ashrrev_i32_e32 v8, 31, v24
	v_mul_lo_u32 v8, s56, v8
	v_mad_u64_u32 v[20:21], s[4:5], s56, v24, 0
	v_add3_u32 v21, v21, v8, v22
	v_lshl_add_u64 v[20:21], v[20:21], 1, s[60:61]
	s_lshl_b64 s[4:5], s[58:59], 1
	v_lshl_add_u64 v[20:21], v[20:21], 0, s[4:5]
	v_lshlrev_b32_e32 v8, 1, v10
	v_lshl_add_u64 v[20:21], v[20:21], 0, v[8:9]
	global_store_dwordx4 v[20:21], v[16:19], off
	s_cmpk_lt_i32 s3, 25216
	v_readlane_b32 s83, v255, 24
	s_waitcnt lgkmcnt(0)
	v_mul_f32_e32 v16, v4, v136
	v_mul_f32_e32 v17, v5, v137
	v_cvt_pk_bf16_f32 v16, v16, v17
	s_mov_b32 s79, 0x3f22f983
	s_mov_b32 s85, 0xbfc90fda
	s_brev_b32 s86, 1
	s_movk_i32 s87, 0x1f8
	s_waitcnt lgkmcnt(0)
	v_mul_f32_e32 v17, v6, v138
	v_mul_f32_e32 v18, v7, v139
	v_cvt_pk_bf16_f32 v17, v17, v18
	s_mov_b64 s[88:89], 0x80
	s_mov_b64 s[92:93], 0x4000
	s_mov_b64 s[94:95], 0x4800
	v_readlane_b32 s81, v255, 22
	s_waitcnt lgkmcnt(0)
	v_mul_f32_e32 v18, v0, v140
	v_mul_f32_e32 v19, v1, v141
	v_cvt_pk_bf16_f32 v18, v18, v19
	s_waitcnt lgkmcnt(0)
	v_mul_f32_e32 v19, v2, v142
	v_mul_f32_e32 v20, v3, v143
	v_cvt_pk_bf16_f32 v19, v19, v20
	v_add_u32_e32 v20, 8, v24
	v_ashrrev_i32_e32 v21, 31, v20
	v_mul_lo_u32 v22, s56, v21
	v_mul_lo_u32 v23, s57, v20
	v_mad_u64_u32 v[20:21], s[6:7], s56, v20, 0
	v_add3_u32 v21, v21, v22, v23
	v_lshl_add_u64 v[20:21], v[20:21], 1, s[60:61]
	v_lshl_add_u64 v[20:21], v[20:21], 0, s[4:5]
	v_lshl_add_u64 v[20:21], v[20:21], 0, v[8:9]
	global_store_dwordx4 v[20:21], v[16:19], off
	s_waitcnt lgkmcnt(0)
	s_nop 0
	v_mul_f32_e32 v16, v4, v144
	v_mul_f32_e32 v17, v5, v145
	v_cvt_pk_bf16_f32 v16, v16, v17
	s_waitcnt lgkmcnt(0)
	v_mul_f32_e32 v17, v6, v146
	v_mul_f32_e32 v18, v7, v147
	v_cvt_pk_bf16_f32 v17, v17, v18
	s_waitcnt lgkmcnt(0)
	v_mul_f32_e32 v18, v0, v148
	v_mul_f32_e32 v19, v1, v149
	v_cvt_pk_bf16_f32 v18, v18, v19
	s_waitcnt lgkmcnt(0)
; __device__ __forceinline__ unsigned cvt_pk_bf16(float lo, float hi) { unsigned r; asm volatile("v_cvt_pk_bf16_f32 %0, %1, %2" : "=v"(r) : "v"(lo), "v"(hi)); return r; }
; #define LAS __attribute__((address_space(3)))
; #define LDS_WAIT() asm volatile("s_waitcnt lgkmcnt(0)" ::: "memory")
; __device__ __forceinline__ void conv_store(const ConvItem& ci, LAS float* scr, int lane, const float (&v)[64]) {
;     ...
;     for (int j = 0; j < 8; ++j) { const int n = (lane >> 3) + 8 * j; const LAS float* s = scr + (8 * c) * 65 + n;
;         v4u o; o.x = cvt_pk_bf16(s[0 * 65] * s0[0], s[1 * 65] * s0[1]); o.y = cvt_pk_bf16(s[2 * 65] * s0[2], s[3 * 65] * s0[3]); o.z = cvt_pk_bf16(s[4 * 65] * s1[0], s[5 * 65] * s1[1]); o.w = cvt_pk_bf16(s[6 * 65] * s1[2], s[7 * 65] * s1[3]);
;         *(v4u*)(ci.dst + (size_t)(ci.drow0 + n) * ci.ldd + ci.k0 + 8 * c) = o; }
;     LDS_WAIT(); asm volatile("" ::: "memory");
	v_mul_f32_e32 v19, v2, v150
	v_mul_f32_e32 v20, v3, v151
	v_cvt_pk_bf16_f32 v19, v19, v20
	v_add_u32_e32 v20, 16, v24
	v_ashrrev_i32_e32 v21, 31, v20
	v_mul_lo_u32 v22, s56, v21
	v_mul_lo_u32 v23, s57, v20
	v_mad_u64_u32 v[20:21], s[6:7], s56, v20, 0
	v_add3_u32 v21, v21, v22, v23
	v_lshl_add_u64 v[20:21], v[20:21], 1, s[60:61]
	v_lshl_add_u64 v[20:21], v[20:21], 0, s[4:5]
	v_lshl_add_u64 v[20:21], v[20:21], 0, v[8:9]
	global_store_dwordx4 v[20:21], v[16:19], off
	s_waitcnt lgkmcnt(0)
	s_nop 0
	v_mul_f32_e32 v16, v4, v152
	v_mul_f32_e32 v17, v5, v153
	v_cvt_pk_bf16_f32 v16, v16, v17
	s_waitcnt lgkmcnt(0)
	v_mul_f32_e32 v17, v6, v154
	v_mul_f32_e32 v18, v7, v155
	v_cvt_pk_bf16_f32 v17, v17, v18
	s_waitcnt lgkmcnt(0)
	v_mul_f32_e32 v18, v0, v156
	v_mul_f32_e32 v19, v1, v157
	v_cvt_pk_bf16_f32 v18, v18, v19
	s_waitcnt lgkmcnt(0)
	v_mul_f32_e32 v19, v2, v158
	v_mul_f32_e32 v20, v3, v159
	v_cvt_pk_bf16_f32 v19, v19, v20
	v_add_u32_e32 v20, 24, v24
	v_ashrrev_i32_e32 v21, 31, v20
	v_mul_lo_u32 v22, s56, v21
	v_mul_lo_u32 v23, s57, v20
	v_mad_u64_u32 v[20:21], s[6:7], s56, v20, 0
	v_add3_u32 v21, v21, v22, v23
	v_lshl_add_u64 v[20:21], v[20:21], 1, s[60:61]
	v_lshl_add_u64 v[20:21], v[20:21], 0, s[4:5]
	v_lshl_add_u64 v[20:21], v[20:21], 0, v[8:9]
	global_store_dwordx4 v[20:21], v[16:19], off
	s_waitcnt lgkmcnt(0)
	s_nop 0
	v_mul_f32_e32 v16, v4, v160
	v_mul_f32_e32 v17, v5, v161
	v_cvt_pk_bf16_f32 v16, v16, v17
	s_waitcnt lgkmcnt(0)
	v_mul_f32_e32 v17, v6, v162
	v_mul_f32_e32 v18, v7, v163
	v_cvt_pk_bf16_f32 v17, v17, v18
	s_waitcnt lgkmcnt(0)
	v_mul_f32_e32 v18, v0, v164
	v_mul_f32_e32 v19, v1, v165
	v_cvt_pk_bf16_f32 v18, v18, v19
	s_waitcnt lgkmcnt(0)
	v_mul_f32_e32 v19, v2, v166
	v_mul_f32_e32 v20, v3, v167
	v_cvt_pk_bf16_f32 v19, v19, v20
	v_add_u32_e32 v20, 32, v24
	v_ashrrev_i32_e32 v21, 31, v20
	v_mul_lo_u32 v22, s56, v21
	v_mul_lo_u32 v23, s57, v20
	v_mad_u64_u32 v[20:21], s[6:7], s56, v20, 0
	v_add3_u32 v21, v21, v22, v23
	v_lshl_add_u64 v[20:21], v[20:21], 1, s[60:61]
	v_lshl_add_u64 v[20:21], v[20:21], 0, s[4:5]
	v_lshl_add_u64 v[20:21], v[20:21], 0, v[8:9]
	global_store_dwordx4 v[20:21], v[16:19], off
	s_waitcnt lgkmcnt(0)
	s_nop 0
	v_mul_f32_e32 v16, v4, v168
	v_mul_f32_e32 v17, v5, v169
	v_cvt_pk_bf16_f32 v16, v16, v17
	s_waitcnt lgkmcnt(0)
	v_mul_f32_e32 v17, v6, v170
	v_mul_f32_e32 v18, v7, v171
	v_cvt_pk_bf16_f32 v17, v17, v18
	s_waitcnt lgkmcnt(0)
	v_mul_f32_e32 v18, v0, v172
	v_mul_f32_e32 v19, v1, v173
	v_cvt_pk_bf16_f32 v18, v18, v19
	s_waitcnt lgkmcnt(0)
	v_mul_f32_e32 v19, v2, v174
	v_mul_f32_e32 v20, v3, v175
	v_cvt_pk_bf16_f32 v19, v19, v20
	v_add_u32_e32 v20, 40, v24
	v_ashrrev_i32_e32 v21, 31, v20
	v_mul_lo_u32 v22, s56, v21
	v_mul_lo_u32 v23, s57, v20
	v_mad_u64_u32 v[20:21], s[6:7], s56, v20, 0
	v_add3_u32 v21, v21, v22, v23
	v_lshl_add_u64 v[20:21], v[20:21], 1, s[60:61]
	v_lshl_add_u64 v[20:21], v[20:21], 0, s[4:5]
	v_lshl_add_u64 v[20:21], v[20:21], 0, v[8:9]
	global_store_dwordx4 v[20:21], v[16:19], off
	s_waitcnt lgkmcnt(0)
	s_nop 0
	v_mul_f32_e32 v16, v4, v176
	v_mul_f32_e32 v17, v5, v177
	v_cvt_pk_bf16_f32 v16, v16, v17
	s_waitcnt lgkmcnt(0)
	v_mul_f32_e32 v17, v6, v178
	v_mul_f32_e32 v18, v7, v179
	v_cvt_pk_bf16_f32 v17, v17, v18
	s_waitcnt lgkmcnt(0)
	v_mul_f32_e32 v18, v0, v180
	v_mul_f32_e32 v19, v1, v181
	v_cvt_pk_bf16_f32 v18, v18, v19
	s_waitcnt lgkmcnt(0)
	v_mul_f32_e32 v19, v2, v182
	v_mul_f32_e32 v20, v3, v183
	v_cvt_pk_bf16_f32 v19, v19, v20
	v_add_u32_e32 v20, 48, v24
	v_ashrrev_i32_e32 v21, 31, v20
	v_mul_lo_u32 v22, s56, v21
	v_mul_lo_u32 v23, s57, v20
	v_mad_u64_u32 v[20:21], s[6:7], s56, v20, 0
	v_add3_u32 v21, v21, v22, v23
	v_lshl_add_u64 v[20:21], v[20:21], 1, s[60:61]
	v_lshl_add_u64 v[20:21], v[20:21], 0, s[4:5]
	v_lshl_add_u64 v[20:21], v[20:21], 0, v[8:9]
	global_store_dwordx4 v[20:21], v[16:19], off
	s_waitcnt lgkmcnt(0)
	v_mul_f32_e32 v4, v4, v184
	v_mul_f32_e32 v5, v5, v185
	v_cvt_pk_bf16_f32 v4, v4, v5
	s_waitcnt lgkmcnt(0)
	v_mul_f32_e32 v5, v6, v186
	v_mul_f32_e32 v6, v7, v187
	v_cvt_pk_bf16_f32 v5, v5, v6
	s_waitcnt lgkmcnt(0)
	v_mul_f32_e32 v0, v0, v188
	v_mul_f32_e32 v1, v1, v189
	v_cvt_pk_bf16_f32 v6, v0, v1
	s_waitcnt lgkmcnt(0)
	v_mul_f32_e32 v0, v2, v190
	v_mul_f32_e32 v1, v3, v191
	v_cvt_pk_bf16_f32 v7, v0, v1
	v_add_u32_e32 v0, 56, v24
	v_ashrrev_i32_e32 v1, 31, v0
	v_mul_lo_u32 v2, s56, v1
	v_mul_lo_u32 v3, s57, v0
	v_mad_u64_u32 v[0:1], s[6:7], s56, v0, 0
	v_add3_u32 v1, v1, v2, v3
	v_lshl_add_u64 v[0:1], v[0:1], 1, s[60:61]
	v_lshl_add_u64 v[0:1], v[0:1], 0, s[4:5]
	v_lshl_add_u64 v[0:1], v[0:1], 0, v[8:9]
	global_store_dwordx4 v[0:1], v[4:7], off
	s_waitcnt lgkmcnt(0)
	s_cbranch_scc0 .Lcvp11_ret

; __device__ __forceinline__ void conv_load(const ConvItem& ci, int lane, float (&v)[64]) {
;     ...
;     for (int i = 0; i < 64; ++i) { const int k = ci.k0 + i, kk = k < kmax ? k : kmax; v[i] = __builtin_nontemporal_load(base + (size_t)kk * ci.ldw); }
; #pragma unroll
;     for (int i = 0; i < 64; ++i) v[i] = (okc && (ci.k0 + i) < ci.Ksrc) ? v[i] : 0.f;
.Lcvp30_30:
	s_cmp_lt_i32 s58, s76
	s_cselect_b64 s[4:5], -1, 0
	s_and_b64 s[4:5], vcc, s[4:5]
	s_cmp_lt_i32 s64, s76
	s_waitcnt vmcnt(62)
	v_cndmask_b32_e64 v21, 0, v21, s[4:5]
	s_cselect_b64 s[4:5], -1, 0
	s_and_b64 s[4:5], vcc, s[4:5]
	s_cmp_lt_i32 s65, s76
	v_cndmask_b32_e64 v20, 0, v20, s[4:5]
	s_cselect_b64 s[4:5], -1, 0
	s_and_b64 s[4:5], vcc, s[4:5]
	s_cmp_lt_i32 s78, s76
	s_waitcnt vmcnt(61)
	v_cndmask_b32_e64 v19, 0, v19, s[4:5]
	s_cselect_b64 s[4:5], -1, 0
	s_and_b64 s[4:5], vcc, s[4:5]
	s_cmp_lt_i32 s79, s76
	s_waitcnt vmcnt(60)
	v_cndmask_b32_e64 v18, 0, v18, s[4:5]
	s_cselect_b64 s[4:5], -1, 0
	s_and_b64 s[4:5], vcc, s[4:5]
	s_cmp_lt_i32 s80, s76
	s_waitcnt vmcnt(59)
	v_cndmask_b32_e64 v17, 0, v17, s[4:5]
	s_cselect_b64 s[4:5], -1, 0
	s_and_b64 s[4:5], vcc, s[4:5]
	s_cmp_lt_i32 s81, s76
	s_waitcnt vmcnt(58)
	v_cndmask_b32_e64 v16, 0, v16, s[4:5]
	s_cselect_b64 s[4:5], -1, 0
	s_and_b64 s[4:5], vcc, s[4:5]
	s_cmp_lt_i32 s82, s76
	s_waitcnt vmcnt(57)
	v_cndmask_b32_e64 v15, 0, v15, s[4:5]
	s_cselect_b64 s[4:5], -1, 0
	s_and_b64 s[4:5], vcc, s[4:5]
	s_cmp_lt_i32 s83, s76
	s_waitcnt vmcnt(56)
	v_cndmask_b32_e64 v8, 0, v8, s[4:5]
	s_cselect_b64 s[4:5], -1, 0
	s_and_b64 s[4:5], vcc, s[4:5]
	s_cmp_lt_i32 s85, s76
	s_waitcnt vmcnt(55)
	v_cndmask_b32_e64 v29, 0, v29, s[4:5]
	s_cselect_b64 s[4:5], -1, 0
	s_and_b64 s[4:5], vcc, s[4:5]
	s_cmp_lt_i32 s86, s76
	s_waitcnt vmcnt(54)
	v_cndmask_b32_e64 v28, 0, v28, s[4:5]
	s_cselect_b64 s[4:5], -1, 0
	s_and_b64 s[4:5], vcc, s[4:5]
	s_cmp_lt_i32 s87, s76
	s_waitcnt vmcnt(53)
	v_cndmask_b32_e64 v27, 0, v27, s[4:5]
	s_cselect_b64 s[4:5], -1, 0
	s_and_b64 s[4:5], vcc, s[4:5]
	s_cmp_lt_i32 s88, s76
	s_waitcnt vmcnt(52)
	v_cndmask_b32_e64 v26, 0, v26, s[4:5]
	s_cselect_b64 s[4:5], -1, 0
	s_and_b64 s[4:5], vcc, s[4:5]
	s_cmp_lt_i32 s89, s76
	s_waitcnt vmcnt(51)
	v_cndmask_b32_e64 v25, 0, v25, s[4:5]
	s_cselect_b64 s[4:5], -1, 0
	s_and_b64 s[4:5], vcc, s[4:5]
	s_cmp_lt_i32 s90, s76
	s_waitcnt vmcnt(50)
	v_cndmask_b32_e64 v24, 0, v24, s[4:5]
	s_cselect_b64 s[4:5], -1, 0
	s_and_b64 s[4:5], vcc, s[4:5]
	s_cmp_lt_i32 s92, s76
	s_waitcnt vmcnt(49)
	v_cndmask_b32_e64 v23, 0, v23, s[4:5]
	s_cselect_b64 s[4:5], -1, 0
	s_and_b64 s[4:5], vcc, s[4:5]
	s_cmp_lt_i32 s93, s76
	s_waitcnt vmcnt(48)
	v_cndmask_b32_e64 v22, 0, v22, s[4:5]
	s_cselect_b64 s[4:5], -1, 0
	s_and_b64 s[4:5], vcc, s[4:5]
	s_cmp_lt_i32 s94, s76
	s_waitcnt vmcnt(47)
	v_cndmask_b32_e64 v37, 0, v37, s[4:5]
	s_cselect_b64 s[4:5], -1, 0
	s_and_b64 s[4:5], vcc, s[4:5]
	s_cmp_lt_i32 s95, s76
	s_waitcnt vmcnt(46)
	v_cndmask_b32_e64 v36, 0, v36, s[4:5]
	s_cselect_b64 s[4:5], -1, 0
	s_and_b64 s[4:5], vcc, s[4:5]
	s_cmp_lt_i32 s50, s76
	s_waitcnt vmcnt(45)
	v_cndmask_b32_e64 v35, 0, v35, s[4:5]
	s_cselect_b64 s[4:5], -1, 0
	s_and_b64 s[4:5], vcc, s[4:5]
	s_cmp_lt_i32 s51, s76
	s_waitcnt vmcnt(44)
	v_cndmask_b32_e64 v34, 0, v34, s[4:5]
	s_cselect_b64 s[4:5], -1, 0
	s_and_b64 s[4:5], vcc, s[4:5]
	s_cmp_lt_i32 s52, s76
	s_waitcnt vmcnt(43)
	v_cndmask_b32_e64 v33, 0, v33, s[4:5]
	s_cselect_b64 s[4:5], -1, 0
	s_and_b64 s[4:5], vcc, s[4:5]
	s_cmp_lt_i32 s53, s76
	s_waitcnt vmcnt(42)
	v_cndmask_b32_e64 v32, 0, v32, s[4:5]
	s_cselect_b64 s[4:5], -1, 0
	s_and_b64 s[4:5], vcc, s[4:5]
	s_cmp_lt_i32 s6, s76
	s_waitcnt vmcnt(41)
	v_cndmask_b32_e64 v31, 0, v31, s[4:5]
	s_cselect_b64 s[4:5], -1, 0
	s_and_b64 s[4:5], vcc, s[4:5]
	s_cmp_lt_i32 s7, s76
	s_waitcnt vmcnt(40)
	v_cndmask_b32_e64 v30, 0, v30, s[4:5]
	s_cselect_b64 s[4:5], -1, 0
	s_and_b64 s[4:5], vcc, s[4:5]
	s_cmp_lt_i32 s8, s76
	s_waitcnt vmcnt(39)
	v_cndmask_b32_e64 v45, 0, v45, s[4:5]
	s_cselect_b64 s[4:5], -1, 0
	s_and_b64 s[4:5], vcc, s[4:5]
	s_cmp_lt_i32 s9, s76
	s_waitcnt vmcnt(38)
	v_cndmask_b32_e64 v44, 0, v44, s[4:5]
	s_cselect_b64 s[4:5], -1, 0
	s_and_b64 s[4:5], vcc, s[4:5]
	s_cmp_lt_i32 s10, s76
	s_waitcnt vmcnt(37)
	v_cndmask_b32_e64 v43, 0, v43, s[4:5]
	s_cselect_b64 s[4:5], -1, 0
	s_and_b64 s[4:5], vcc, s[4:5]
	s_cmp_lt_i32 s11, s76
	s_waitcnt vmcnt(36)
	v_cndmask_b32_e64 v42, 0, v42, s[4:5]
	s_cselect_b64 s[4:5], -1, 0
	s_and_b64 s[4:5], vcc, s[4:5]
	s_cmp_lt_i32 s14, s76
	s_waitcnt vmcnt(35)
	v_cndmask_b32_e64 v41, 0, v41, s[4:5]
	s_cselect_b64 s[4:5], -1, 0
	s_and_b64 s[4:5], vcc, s[4:5]
	s_cmp_lt_i32 s15, s76
	s_waitcnt vmcnt(34)
	v_cndmask_b32_e64 v40, 0, v40, s[4:5]
	s_cselect_b64 s[4:5], -1, 0
	s_and_b64 s[4:5], vcc, s[4:5]
	s_cmp_lt_i32 s16, s76
	s_waitcnt vmcnt(33)
	v_cndmask_b32_e64 v39, 0, v39, s[4:5]
	s_cselect_b64 s[4:5], -1, 0
	s_and_b64 s[4:5], vcc, s[4:5]
	s_cmp_lt_i32 s17, s76
	s_waitcnt vmcnt(32)
	v_cndmask_b32_e64 v38, 0, v38, s[4:5]
	s_cselect_b64 s[4:5], -1, 0
	s_and_b64 s[4:5], vcc, s[4:5]
	s_cmp_lt_i32 s12, s76
	s_waitcnt vmcnt(31)
	v_cndmask_b32_e64 v53, 0, v53, s[4:5]
	s_cselect_b64 s[4:5], -1, 0
	s_and_b64 s[4:5], vcc, s[4:5]
	s_cmp_lt_i32 s13, s76
	s_waitcnt vmcnt(30)
	v_cndmask_b32_e64 v52, 0, v52, s[4:5]
	s_cselect_b64 s[4:5], -1, 0
	s_and_b64 s[4:5], vcc, s[4:5]
	s_cmp_lt_i32 s20, s76
	s_waitcnt vmcnt(29)
	v_cndmask_b32_e64 v51, 0, v51, s[4:5]
	s_cselect_b64 s[4:5], -1, 0
	s_and_b64 s[4:5], vcc, s[4:5]
	s_cmp_lt_i32 s21, s76
	s_waitcnt vmcnt(28)
	v_cndmask_b32_e64 v50, 0, v50, s[4:5]
	s_cselect_b64 s[4:5], -1, 0
	s_and_b64 s[4:5], vcc, s[4:5]
	s_cmp_lt_i32 s24, s76
	s_waitcnt vmcnt(27)
	v_cndmask_b32_e64 v49, 0, v49, s[4:5]
	s_cselect_b64 s[4:5], -1, 0
	s_and_b64 s[4:5], vcc, s[4:5]
	s_cmp_lt_i32 s25, s76
	s_waitcnt vmcnt(26)
	v_cndmask_b32_e64 v48, 0, v48, s[4:5]
	s_cselect_b64 s[4:5], -1, 0
	s_and_b64 s[4:5], vcc, s[4:5]
	s_cmp_lt_i32 s26, s76
	s_waitcnt vmcnt(25)
	v_cndmask_b32_e64 v47, 0, v47, s[4:5]
	s_cselect_b64 s[4:5], -1, 0
	s_and_b64 s[4:5], vcc, s[4:5]
	s_cmp_lt_i32 s27, s76
	s_waitcnt vmcnt(24)
; #define LAS __attribute__((address_space(3)))
; #define LDS_WAIT() asm volatile("s_waitcnt lgkmcnt(0)" ::: "memory")
; __device__ __forceinline__ void conv_load(const ConvItem& ci, int lane, float (&v)[64]) {
;     ...
;     for (int i = 0; i < 64; ++i) v[i] = (okc && (ci.k0 + i) < ci.Ksrc) ? v[i] : 0.f;
; }
; __device__ __forceinline__ void conv_store(const ConvItem& ci, LAS float* scr, int lane, const float (&v)[64]) {
;     const int c = lane & 7;
;     f32x4 s0 = {1.f, 1.f, 1.f, 1.f}, s1 = s0;
;     if (ci.ks) { const int kb = ci.k0 + 8 * c < ci.Ksrc - 8 ? ci.k0 + 8 * c : ci.Ksrc - 8; s0 = *(const f32x4*)(ci.ks + kb); s1 = *(const f32x4*)(ci.ks + kb + 4); }
; #pragma unroll
;     for (int i = 0; i < 64; ++i) scr[i * 65 + lane] = v[i];
;     LDS_WAIT(); asm volatile("" ::: "memory");
	v_cndmask_b32_e64 v46, 0, v46, s[4:5]
	s_cselect_b64 s[4:5], -1, 0
	s_and_b64 s[4:5], vcc, s[4:5]
	s_cmp_lt_i32 s18, s76
	s_waitcnt vmcnt(23)
	v_cndmask_b32_e64 v61, 0, v61, s[4:5]
	s_cselect_b64 s[4:5], -1, 0
	s_and_b64 s[4:5], vcc, s[4:5]
	s_cmp_lt_i32 s19, s76
	s_waitcnt vmcnt(22)
	v_cndmask_b32_e64 v60, 0, v60, s[4:5]
	s_cselect_b64 s[4:5], -1, 0
	s_and_b64 s[4:5], vcc, s[4:5]
	s_cmp_lt_i32 s28, s76
	s_waitcnt vmcnt(21)
	v_cndmask_b32_e64 v59, 0, v59, s[4:5]
	s_cselect_b64 s[4:5], -1, 0
	s_and_b64 s[4:5], vcc, s[4:5]
	s_cmp_lt_i32 s29, s76
	s_waitcnt vmcnt(20)
	v_cndmask_b32_e64 v58, 0, v58, s[4:5]
	s_cselect_b64 s[4:5], -1, 0
	s_and_b64 s[4:5], vcc, s[4:5]
	s_cmp_lt_i32 s22, s76
	s_waitcnt vmcnt(19)
	v_cndmask_b32_e64 v57, 0, v57, s[4:5]
	s_cselect_b64 s[4:5], -1, 0
	s_and_b64 s[4:5], vcc, s[4:5]
	s_cmp_lt_i32 s23, s76
	s_waitcnt vmcnt(18)
	v_cndmask_b32_e64 v56, 0, v56, s[4:5]
	s_cselect_b64 s[4:5], -1, 0
	s_and_b64 s[4:5], vcc, s[4:5]
	s_cmp_lt_i32 s30, s76
	s_waitcnt vmcnt(17)
	v_cndmask_b32_e64 v55, 0, v55, s[4:5]
	s_cselect_b64 s[4:5], -1, 0
	s_and_b64 s[4:5], vcc, s[4:5]
	s_cmp_lt_i32 s31, s76
	s_waitcnt vmcnt(16)
	v_cndmask_b32_e64 v54, 0, v54, s[4:5]
	s_cselect_b64 s[4:5], -1, 0
	s_and_b64 s[4:5], vcc, s[4:5]
	s_cmp_lt_i32 s36, s76
	s_waitcnt vmcnt(15)
	v_cndmask_b32_e64 v70, 0, v70, s[4:5]
	s_cselect_b64 s[4:5], -1, 0
	s_and_b64 s[4:5], vcc, s[4:5]
	s_cmp_lt_i32 s37, s76
	s_waitcnt vmcnt(14)
	v_cndmask_b32_e64 v69, 0, v69, s[4:5]
	s_cselect_b64 s[4:5], -1, 0
	s_and_b64 s[4:5], vcc, s[4:5]
	s_cmp_lt_i32 s38, s76
	s_waitcnt vmcnt(13)
	v_cndmask_b32_e64 v68, 0, v68, s[4:5]
	s_cselect_b64 s[4:5], -1, 0
	s_and_b64 s[4:5], vcc, s[4:5]
	s_cmp_lt_i32 s39, s76
	s_waitcnt vmcnt(12)
	v_cndmask_b32_e64 v67, 0, v67, s[4:5]
	s_cselect_b64 s[4:5], -1, 0
	s_and_b64 s[4:5], vcc, s[4:5]
	s_cmp_lt_i32 s34, s76
	s_waitcnt vmcnt(11)
	v_cndmask_b32_e64 v66, 0, v66, s[4:5]
	s_cselect_b64 s[4:5], -1, 0
	s_and_b64 s[4:5], vcc, s[4:5]
	s_cmp_lt_i32 s35, s76
	s_waitcnt vmcnt(10)
	v_cndmask_b32_e64 v64, 0, v64, s[4:5]
	s_cselect_b64 s[4:5], -1, 0
	s_and_b64 s[4:5], vcc, s[4:5]
	s_cmp_lt_i32 s42, s76
	s_waitcnt vmcnt(9)
	v_cndmask_b32_e64 v63, 0, v63, s[4:5]
	s_cselect_b64 s[4:5], -1, 0
	s_and_b64 s[4:5], vcc, s[4:5]
	s_cmp_lt_i32 s43, s76
	s_waitcnt vmcnt(8)
	v_cndmask_b32_e64 v62, 0, v62, s[4:5]
	s_cselect_b64 s[4:5], -1, 0
	s_and_b64 s[4:5], vcc, s[4:5]
	s_cmp_lt_i32 s54, s76
	s_waitcnt vmcnt(7)
	v_cndmask_b32_e64 v65, 0, v65, s[4:5]
	s_cselect_b64 s[4:5], -1, 0
	s_and_b64 s[4:5], vcc, s[4:5]
	s_cmp_lt_i32 s55, s76
	s_waitcnt vmcnt(6)
	v_cndmask_b32_e64 v74, 0, v74, s[4:5]
	s_cselect_b64 s[4:5], -1, 0
	s_and_b64 s[4:5], vcc, s[4:5]
	s_cmp_lt_i32 s46, s76
	ds_write2_b32 v12, v21, v20 offset1:65
	ds_write2_b32 v12, v19, v18 offset0:130 offset1:195
	v_add_u32_e32 v18, 0x400, v12
	s_waitcnt vmcnt(5)
	v_cndmask_b32_e64 v73, 0, v73, s[4:5]
	s_cselect_b64 s[4:5], -1, 0
	ds_write2_b32 v18, v17, v16 offset0:4 offset1:69
	ds_write2_b32 v18, v15, v8 offset0:134 offset1:199
	v_add_u32_e32 v8, 0x800, v12
	s_and_b64 s[4:5], vcc, s[4:5]
	ds_write2_b32 v8, v29, v28 offset0:8 offset1:73
	ds_write2_b32 v8, v27, v26 offset0:138 offset1:203
	v_add_u32_e32 v8, 0xc00, v12
	s_cmp_lt_i32 s47, s76
	ds_write2_b32 v8, v25, v24 offset0:12 offset1:77
	ds_write2_b32 v8, v23, v22 offset0:142 offset1:207
	v_add_u32_e32 v8, 0x1000, v12
	s_waitcnt vmcnt(4)
	v_cndmask_b32_e64 v72, 0, v72, s[4:5]
	s_cselect_b64 s[4:5], -1, 0
	ds_write2_b32 v8, v37, v36 offset0:16 offset1:81
	ds_write2_b32 v8, v35, v34 offset0:146 offset1:211
	v_add_u32_e32 v8, 0x1400, v12
	s_and_b64 s[4:5], vcc, s[4:5]
	ds_write2_b32 v8, v33, v32 offset0:20 offset1:85
	ds_write2_b32 v8, v31, v30 offset0:150 offset1:215
	v_add_u32_e32 v8, 0x1800, v12
	s_cmp_lt_i32 s48, s76
	ds_write2_b32 v8, v45, v44 offset0:24 offset1:89
	ds_write2_b32 v8, v43, v42 offset0:154 offset1:219
	v_add_u32_e32 v8, 0x1c00, v12
	s_waitcnt vmcnt(3)
	v_cndmask_b32_e64 v71, 0, v71, s[4:5]
	s_cselect_b64 s[4:5], -1, 0
	ds_write2_b32 v8, v41, v40 offset0:28 offset1:93
	ds_write2_b32 v8, v39, v38 offset0:158 offset1:223
	v_add_u32_e32 v8, 0x2000, v12
	s_and_b64 s[4:5], vcc, s[4:5]
	ds_write2_b32 v8, v53, v52 offset0:32 offset1:97
	ds_write2_b32 v8, v51, v50 offset0:162 offset1:227
	v_add_u32_e32 v8, 0x2400, v12
	s_cmp_lt_i32 s49, s76
	ds_write2_b32 v8, v49, v48 offset0:36 offset1:101
	ds_write2_b32 v8, v47, v46 offset0:166 offset1:231
	v_add_u32_e32 v8, 0x2800, v12
	s_waitcnt vmcnt(2)
	v_cndmask_b32_e64 v77, 0, v77, s[4:5]
	s_cselect_b64 s[4:5], -1, 0
	ds_write2_b32 v8, v61, v60 offset0:40 offset1:105
	ds_write2_b32 v8, v59, v58 offset0:170 offset1:235
	v_add_u32_e32 v8, 0x2c00, v12
	s_and_b64 s[4:5], vcc, s[4:5]
	ds_write2_b32 v8, v57, v56 offset0:44 offset1:109
	ds_write2_b32 v8, v55, v54 offset0:174 offset1:239
	v_add_u32_e32 v8, 0x3000, v12
	s_cmp_lt_i32 s44, s76
	ds_write2_b32 v8, v70, v69 offset0:48 offset1:113
	ds_write2_b32 v8, v68, v67 offset0:178 offset1:243
	v_add_u32_e32 v8, 0x3400, v12
	s_waitcnt vmcnt(1)
	v_cndmask_b32_e64 v76, 0, v76, s[4:5]
	s_cselect_b64 s[4:5], -1, 0
	ds_write2_b32 v8, v66, v64 offset0:52 offset1:117
	ds_write2_b32 v8, v63, v62 offset0:182 offset1:247
	v_add_u32_e32 v8, 0x3800, v12
	s_and_b64 vcc, vcc, s[4:5]
	ds_write2_b32 v8, v65, v74 offset0:56 offset1:121
	ds_write2_b32 v8, v73, v72 offset0:186 offset1:251
	v_add_u32_e32 v8, 0x3c00, v12
	s_waitcnt vmcnt(0)
	v_cndmask_b32_e32 v75, 0, v75, vcc
	ds_write2_b32 v8, v71, v77 offset0:60 offset1:125
	ds_write2_b32 v8, v76, v75 offset0:190 offset1:255
	s_waitcnt lgkmcnt(0)
; __device__ __forceinline__ unsigned cvt_pk_bf16(float lo, float hi) { unsigned r; asm volatile("v_cvt_pk_bf16_f32 %0, %1, %2" : "=v"(r) : "v"(lo), "v"(hi)); return r; }
; #define LAS __attribute__((address_space(3)))
; __device__ __forceinline__ void conv_store(const ConvItem& ci, LAS float* scr, int lane, const float (&v)[64]) {
;     ...
;     for (int j = 0; j < 8; ++j) { const int n = (lane >> 3) + 8 * j; const LAS float* s = scr + (8 * c) * 65 + n;
;         v4u o; o.x = cvt_pk_bf16(s[0 * 65] * s0[0], s[1 * 65] * s0[1]); o.y = cvt_pk_bf16(s[2 * 65] * s0[2], s[3 * 65] * s0[3]); o.z = cvt_pk_bf16(s[4 * 65] * s1[0], s[5 * 65] * s1[1]); o.w = cvt_pk_bf16(s[6 * 65] * s1[2], s[7 * 65] * s1[3]);
;         *(v4u*)(ci.dst + (size_t)(ci.drow0 + n) * ci.ldd + ci.k0 + 8 * c) = o; }
	v_add_u32_e32 v192, 0x400, v14
	ds_read2_b32 v[128:129], v14 offset1:65
	ds_read2_b32 v[130:131], v14 offset0:130 offset1:195
	ds_read2_b32 v[132:133], v192 offset0:4 offset1:69
	ds_read2_b32 v[134:135], v192 offset0:134 offset1:199
	ds_read2_b32 v[136:137], v14 offset0:8 offset1:73
	ds_read2_b32 v[138:139], v14 offset0:138 offset1:203
	ds_read2_b32 v[140:141], v192 offset0:12 offset1:77
	ds_read2_b32 v[142:143], v192 offset0:142 offset1:207
	ds_read2_b32 v[144:145], v14 offset0:16 offset1:81
	ds_read2_b32 v[146:147], v14 offset0:146 offset1:211
	ds_read2_b32 v[148:149], v192 offset0:20 offset1:85
	ds_read2_b32 v[150:151], v192 offset0:150 offset1:215
	ds_read2_b32 v[152:153], v14 offset0:24 offset1:89
	ds_read2_b32 v[154:155], v14 offset0:154 offset1:219
	ds_read2_b32 v[156:157], v192 offset0:28 offset1:93
	ds_read2_b32 v[158:159], v192 offset0:158 offset1:223
	ds_read2_b32 v[160:161], v14 offset0:32 offset1:97
	ds_read2_b32 v[162:163], v14 offset0:162 offset1:227
	ds_read2_b32 v[164:165], v192 offset0:36 offset1:101
	ds_read2_b32 v[166:167], v192 offset0:166 offset1:231
	ds_read2_b32 v[168:169], v14 offset0:40 offset1:105
	ds_read2_b32 v[170:171], v14 offset0:170 offset1:235
	ds_read2_b32 v[172:173], v192 offset0:44 offset1:109
	ds_read2_b32 v[174:175], v192 offset0:174 offset1:239
	ds_read2_b32 v[176:177], v14 offset0:48 offset1:113
	ds_read2_b32 v[178:179], v14 offset0:178 offset1:243
	ds_read2_b32 v[180:181], v192 offset0:52 offset1:117
	ds_read2_b32 v[182:183], v192 offset0:182 offset1:247
	ds_read2_b32 v[184:185], v14 offset0:56 offset1:121
	ds_read2_b32 v[186:187], v14 offset0:186 offset1:251
	ds_read2_b32 v[188:189], v192 offset0:60 offset1:125
	ds_read2_b32 v[190:191], v192 offset0:190 offset1:255
	s_waitcnt lgkmcnt(0)
	v_add_u32_e32 v24, s59, v13
	v_mul_lo_u32 v22, s57, v24
	s_ashr_i32 s59, s58, 31
	v_readlane_b32 s76, v254, 31
	s_waitcnt lgkmcnt(0)
	v_mul_f32_e32 v8, v4, v128
	v_mul_f32_e32 v15, v5, v129
	v_cvt_pk_bf16_f32 v16, v8, v15
	s_add_i32 s3, s3, s33
	s_add_i32 s66, s66, s67
	s_add_i32 s68, s68, s69
	s_add_i32 s70, s70, s71
	s_waitcnt lgkmcnt(0)
	v_mul_f32_e32 v15, v7, v131
	v_mul_f32_e32 v8, v6, v130
	v_cvt_pk_bf16_f32 v17, v8, v15
	v_add_u32_e32 v15, 0x400, v14
	s_add_i32 s72, s72, s73
	s_add_i32 s74, s74, s75
	v_readlane_b32 s78, v254, 33
	v_readlane_b32 s79, v254, 34
	s_waitcnt lgkmcnt(0)
	v_mul_f32_e32 v8, v0, v132
	v_mul_f32_e32 v18, v1, v133
	v_cvt_pk_bf16_f32 v18, v8, v18
	v_readlane_b32 s80, v255, 21
	v_readlane_b32 s77, v254, 32
	s_movk_i32 s78, 0x1580
	v_readlane_b32 s82, v255, 23
	s_waitcnt lgkmcnt(0)
	v_mul_f32_e32 v8, v2, v134
	v_mul_f32_e32 v19, v3, v135
	v_cvt_pk_bf16_f32 v19, v8, v19
	v_ashrrev_i32_e32 v8, 31, v24
	v_mul_lo_u32 v8, s56, v8
	v_mad_u64_u32 v[20:21], s[4:5], s56, v24, 0
	v_add3_u32 v21, v21, v8, v22
	v_lshl_add_u64 v[20:21], v[20:21], 1, s[60:61]
	s_lshl_b64 s[4:5], s[58:59], 1
	v_lshl_add_u64 v[20:21], v[20:21], 0, s[4:5]
	v_lshlrev_b32_e32 v8, 1, v10
	v_lshl_add_u64 v[20:21], v[20:21], 0, v[8:9]
	global_store_dwordx4 v[20:21], v[16:19], off
	s_cmpk_lt_i32 s3, 5504
	v_readlane_b32 s83, v255, 24
	s_waitcnt lgkmcnt(0)
	v_mul_f32_e32 v16, v4, v136
	v_mul_f32_e32 v17, v5, v137
	v_cvt_pk_bf16_f32 v16, v16, v17
	s_mov_b32 s79, 0x3f22f983
	s_mov_b32 s85, 0xbfc90fda
	s_brev_b32 s86, 1
	s_movk_i32 s87, 0x1f8
	s_waitcnt lgkmcnt(0)
	v_mul_f32_e32 v17, v6, v138
	v_mul_f32_e32 v18, v7, v139
	v_cvt_pk_bf16_f32 v17, v17, v18
	s_mov_b64 s[88:89], 0x80
	s_mov_b64 s[92:93], 0x4000
	s_mov_b64 s[94:95], 0x4800
	v_readlane_b32 s81, v255, 22
	s_waitcnt lgkmcnt(0)
	v_mul_f32_e32 v18, v0, v140
	v_mul_f32_e32 v19, v1, v141
	v_cvt_pk_bf16_f32 v18, v18, v19
	s_waitcnt lgkmcnt(0)
	v_mul_f32_e32 v19, v2, v142
	v_mul_f32_e32 v20, v3, v143
	v_cvt_pk_bf16_f32 v19, v19, v20
	v_add_u32_e32 v20, 8, v24
	v_ashrrev_i32_e32 v21, 31, v20
	v_mul_lo_u32 v22, s56, v21
	v_mul_lo_u32 v23, s57, v20
	v_mad_u64_u32 v[20:21], s[6:7], s56, v20, 0
	v_add3_u32 v21, v21, v22, v23
	v_lshl_add_u64 v[20:21], v[20:21], 1, s[60:61]
	v_lshl_add_u64 v[20:21], v[20:21], 0, s[4:5]
	v_lshl_add_u64 v[20:21], v[20:21], 0, v[8:9]
	global_store_dwordx4 v[20:21], v[16:19], off
	s_waitcnt lgkmcnt(0)
	s_nop 0
	v_mul_f32_e32 v16, v4, v144
	v_mul_f32_e32 v17, v5, v145
	v_cvt_pk_bf16_f32 v16, v16, v17
	s_waitcnt lgkmcnt(0)
	v_mul_f32_e32 v17, v6, v146
	v_mul_f32_e32 v18, v7, v147
	v_cvt_pk_bf16_f32 v17, v17, v18
	s_waitcnt lgkmcnt(0)
	v_mul_f32_e32 v18, v0, v148
	v_mul_f32_e32 v19, v1, v149
	v_cvt_pk_bf16_f32 v18, v18, v19
	s_waitcnt lgkmcnt(0)
; __device__ __forceinline__ unsigned cvt_pk_bf16(float lo, float hi) { unsigned r; asm volatile("v_cvt_pk_bf16_f32 %0, %1, %2" : "=v"(r) : "v"(lo), "v"(hi)); return r; }
; #define LAS __attribute__((address_space(3)))
; #define LDS_WAIT() asm volatile("s_waitcnt lgkmcnt(0)" ::: "memory")
; __device__ __forceinline__ void conv_store(const ConvItem& ci, LAS float* scr, int lane, const float (&v)[64]) {
;     ...
;     for (int j = 0; j < 8; ++j) { const int n = (lane >> 3) + 8 * j; const LAS float* s = scr + (8 * c) * 65 + n;
;         v4u o; o.x = cvt_pk_bf16(s[0 * 65] * s0[0], s[1 * 65] * s0[1]); o.y = cvt_pk_bf16(s[2 * 65] * s0[2], s[3 * 65] * s0[3]); o.z = cvt_pk_bf16(s[4 * 65] * s1[0], s[5 * 65] * s1[1]); o.w = cvt_pk_bf16(s[6 * 65] * s1[2], s[7 * 65] * s1[3]);
;         *(v4u*)(ci.dst + (size_t)(ci.drow0 + n) * ci.ldd + ci.k0 + 8 * c) = o; }
;     LDS_WAIT(); asm volatile("" ::: "memory");
	v_mul_f32_e32 v19, v2, v150
	v_mul_f32_e32 v20, v3, v151
	v_cvt_pk_bf16_f32 v19, v19, v20
	v_add_u32_e32 v20, 16, v24
	v_ashrrev_i32_e32 v21, 31, v20
	v_mul_lo_u32 v22, s56, v21
	v_mul_lo_u32 v23, s57, v20
	v_mad_u64_u32 v[20:21], s[6:7], s56, v20, 0
	v_add3_u32 v21, v21, v22, v23
	v_lshl_add_u64 v[20:21], v[20:21], 1, s[60:61]
	v_lshl_add_u64 v[20:21], v[20:21], 0, s[4:5]
	v_lshl_add_u64 v[20:21], v[20:21], 0, v[8:9]
	global_store_dwordx4 v[20:21], v[16:19], off
	s_waitcnt lgkmcnt(0)
	s_nop 0
	v_mul_f32_e32 v16, v4, v152
	v_mul_f32_e32 v17, v5, v153
	v_cvt_pk_bf16_f32 v16, v16, v17
	s_waitcnt lgkmcnt(0)
	v_mul_f32_e32 v17, v6, v154
	v_mul_f32_e32 v18, v7, v155
	v_cvt_pk_bf16_f32 v17, v17, v18
	s_waitcnt lgkmcnt(0)
	v_mul_f32_e32 v18, v0, v156
	v_mul_f32_e32 v19, v1, v157
	v_cvt_pk_bf16_f32 v18, v18, v19
	s_waitcnt lgkmcnt(0)
	v_mul_f32_e32 v19, v2, v158
	v_mul_f32_e32 v20, v3, v159
	v_cvt_pk_bf16_f32 v19, v19, v20
	v_add_u32_e32 v20, 24, v24
	v_ashrrev_i32_e32 v21, 31, v20
	v_mul_lo_u32 v22, s56, v21
	v_mul_lo_u32 v23, s57, v20
	v_mad_u64_u32 v[20:21], s[6:7], s56, v20, 0
	v_add3_u32 v21, v21, v22, v23
	v_lshl_add_u64 v[20:21], v[20:21], 1, s[60:61]
	v_lshl_add_u64 v[20:21], v[20:21], 0, s[4:5]
	v_lshl_add_u64 v[20:21], v[20:21], 0, v[8:9]
	global_store_dwordx4 v[20:21], v[16:19], off
	s_waitcnt lgkmcnt(0)
	s_nop 0
	v_mul_f32_e32 v16, v4, v160
	v_mul_f32_e32 v17, v5, v161
	v_cvt_pk_bf16_f32 v16, v16, v17
	s_waitcnt lgkmcnt(0)
	v_mul_f32_e32 v17, v6, v162
	v_mul_f32_e32 v18, v7, v163
	v_cvt_pk_bf16_f32 v17, v17, v18
	s_waitcnt lgkmcnt(0)
	v_mul_f32_e32 v18, v0, v164
	v_mul_f32_e32 v19, v1, v165
	v_cvt_pk_bf16_f32 v18, v18, v19
	s_waitcnt lgkmcnt(0)
	v_mul_f32_e32 v19, v2, v166
	v_mul_f32_e32 v20, v3, v167
	v_cvt_pk_bf16_f32 v19, v19, v20
	v_add_u32_e32 v20, 32, v24
	v_ashrrev_i32_e32 v21, 31, v20
	v_mul_lo_u32 v22, s56, v21
	v_mul_lo_u32 v23, s57, v20
	v_mad_u64_u32 v[20:21], s[6:7], s56, v20, 0
	v_add3_u32 v21, v21, v22, v23
	v_lshl_add_u64 v[20:21], v[20:21], 1, s[60:61]
	v_lshl_add_u64 v[20:21], v[20:21], 0, s[4:5]
	v_lshl_add_u64 v[20:21], v[20:21], 0, v[8:9]
	global_store_dwordx4 v[20:21], v[16:19], off
	s_waitcnt lgkmcnt(0)
	s_nop 0
	v_mul_f32_e32 v16, v4, v168
	v_mul_f32_e32 v17, v5, v169
	v_cvt_pk_bf16_f32 v16, v16, v17
	s_waitcnt lgkmcnt(0)
	v_mul_f32_e32 v17, v6, v170
	v_mul_f32_e32 v18, v7, v171
	v_cvt_pk_bf16_f32 v17, v17, v18
	s_waitcnt lgkmcnt(0)
	v_mul_f32_e32 v18, v0, v172
	v_mul_f32_e32 v19, v1, v173
	v_cvt_pk_bf16_f32 v18, v18, v19
	s_waitcnt lgkmcnt(0)
	v_mul_f32_e32 v19, v2, v174
	v_mul_f32_e32 v20, v3, v175
	v_cvt_pk_bf16_f32 v19, v19, v20
	v_add_u32_e32 v20, 40, v24
	v_ashrrev_i32_e32 v21, 31, v20
	v_mul_lo_u32 v22, s56, v21
	v_mul_lo_u32 v23, s57, v20
	v_mad_u64_u32 v[20:21], s[6:7], s56, v20, 0
	v_add3_u32 v21, v21, v22, v23
	v_lshl_add_u64 v[20:21], v[20:21], 1, s[60:61]
	v_lshl_add_u64 v[20:21], v[20:21], 0, s[4:5]
	v_lshl_add_u64 v[20:21], v[20:21], 0, v[8:9]
	global_store_dwordx4 v[20:21], v[16:19], off
	s_waitcnt lgkmcnt(0)
	s_nop 0
	v_mul_f32_e32 v16, v4, v176
	v_mul_f32_e32 v17, v5, v177
	v_cvt_pk_bf16_f32 v16, v16, v17
	s_waitcnt lgkmcnt(0)
	v_mul_f32_e32 v17, v6, v178
	v_mul_f32_e32 v18, v7, v179
	v_cvt_pk_bf16_f32 v17, v17, v18
	s_waitcnt lgkmcnt(0)
	v_mul_f32_e32 v18, v0, v180
	v_mul_f32_e32 v19, v1, v181
	v_cvt_pk_bf16_f32 v18, v18, v19
	s_waitcnt lgkmcnt(0)
	v_mul_f32_e32 v19, v2, v182
	v_mul_f32_e32 v20, v3, v183
	v_cvt_pk_bf16_f32 v19, v19, v20
	v_add_u32_e32 v20, 48, v24
	v_ashrrev_i32_e32 v21, 31, v20
	v_mul_lo_u32 v22, s56, v21
	v_mul_lo_u32 v23, s57, v20
	v_mad_u64_u32 v[20:21], s[6:7], s56, v20, 0
	v_add3_u32 v21, v21, v22, v23
	v_lshl_add_u64 v[20:21], v[20:21], 1, s[60:61]
	v_lshl_add_u64 v[20:21], v[20:21], 0, s[4:5]
	v_lshl_add_u64 v[20:21], v[20:21], 0, v[8:9]
	global_store_dwordx4 v[20:21], v[16:19], off
	s_waitcnt lgkmcnt(0)
	v_mul_f32_e32 v4, v4, v184
	v_mul_f32_e32 v5, v5, v185
	v_cvt_pk_bf16_f32 v4, v4, v5
	s_waitcnt lgkmcnt(0)
	v_mul_f32_e32 v5, v6, v186
	v_mul_f32_e32 v6, v7, v187
	v_cvt_pk_bf16_f32 v5, v5, v6
	s_waitcnt lgkmcnt(0)
	v_mul_f32_e32 v0, v0, v188
	v_mul_f32_e32 v1, v1, v189
	v_cvt_pk_bf16_f32 v6, v0, v1
	s_waitcnt lgkmcnt(0)
	v_mul_f32_e32 v0, v2, v190
	v_mul_f32_e32 v1, v3, v191
	v_cvt_pk_bf16_f32 v7, v0, v1
	v_add_u32_e32 v0, 56, v24
	v_ashrrev_i32_e32 v1, 31, v0
	v_mul_lo_u32 v2, s56, v1
	v_mul_lo_u32 v3, s57, v0
	v_mad_u64_u32 v[0:1], s[6:7], s56, v0, 0
	v_add3_u32 v1, v1, v2, v3
	v_lshl_add_u64 v[0:1], v[0:1], 1, s[60:61]
	v_lshl_add_u64 v[0:1], v[0:1], 0, s[4:5]
	v_lshl_add_u64 v[0:1], v[0:1], 0, v[8:9]
	global_store_dwordx4 v[0:1], v[4:7], off
	s_waitcnt lgkmcnt(0)
	s_cbranch_scc0 .Lcvp30_ret

; __global__ void __launch_bounds__(NWAVES * 64, 2) mk_fwd(Args args) {
;     ...
;             constexpr int I_UP = (D / 64) * (NUP / 64), I_DN = (DFF / 64) * (D / 64), I_IN = (D / 64) * (DINP / 64), I_GLU = 16 * 16, I_L = 4 * 16, I_V1 = 16 * 4, I_V2 = 4 * 16,
;                           I_BS5 = 16 * 32, I_BAT = 8 * 32, I_BRW = 16 * 32, I_OUT = 32 * 32;
;             constexpr int NITEMS = 2 * I_UP + 2 * I_DN + I_IN + I_GLU + 3 * I_L + I_V1 + I_V2 + I_BS5 + I_BAT + I_BRW + I_OUT;
;             const int lv = l > 0 ? l - 1 : 0;
;     ...
;             for (int it = gw; it < NITEMS; it += NGW) {
.Lcvp30_ret:
.Lcvrs_p30:
	v_readlane_b32 s0, v254, 8
	v_readlane_b32 s4, v254, 10
	v_readlane_b32 s1, v254, 9
	v_mbcnt_lo_u32_b32 v11, -1, 0
	v_mbcnt_hi_u32_b32 v11, -1, v11
	s_load_dword s6, s[0:1], 0x0
	s_mov_b32 s3, s84
	s_waitcnt lgkmcnt(0)
	s_movk_i32 s6, 128
	s_lshl_b32 s3, s3, 3
	v_readlane_b32 s0, v254, 0
	s_add_i32 s3, s3, s4
	s_add_i32 s3, s3, 0x4500
	v_readlane_b32 s1, v254, 1
	s_cmpk_gt_i32 s3, 21439
	s_cbranch_scc1 .Lcvp31_ret
	s_load_dwordx2 s[8:9], s[0:1], 0x138
	v_readlane_b32 s14, v254, 38
	s_nop 0
	s_add_i32 s14, s14, 1
	s_mulk_i32 s4, 0x4100
	s_add_i32 s7, s4, 0
	v_sub_u32_e64 v0, s14, 1 clamp
	s_lshl_b32 s33, s6, 3
	v_readfirstlane_b32 s4, v0
	s_lshl_b32 s96, s4, 16
	s_waitcnt lgkmcnt(0)
	s_add_u32 s4, s8, 0x22800000
	s_addc_u32 s5, s9, 0
	v_writelane_b32 v254, s4, 39
	s_mov_b32 s15, s97
	v_and_b32_e32 v0, 7, v11
	v_writelane_b32 v254, s5, 40
	s_add_u32 s4, s8, 0x22780000
	s_addc_u32 s5, s9, 0
	v_writelane_b32 v254, s4, 41
	v_ashrrev_i32_e32 v13, 3, v11
	v_lshlrev_b32_e32 v10, 3, v0
	v_writelane_b32 v254, s5, 42
	s_lshl_b32 s4, s14, 18
	s_add_u32 s10, s8, 0x22700000
	s_addc_u32 s11, s9, 0
	v_writelane_b32 v254, s10, 43
	s_mov_b32 s5, s97
	v_mul_u32_u24_e32 v0, 0x820, v0
	v_writelane_b32 v254, s11, 44
	s_mul_i32 s10, s14, 0x18000
	s_mov_b32 s11, s97
	v_writelane_b32 v254, s10, 45
	v_lshlrev_b32_e32 v1, 2, v13
	v_lshl_add_u32 v12, v11, 2, s7
	v_writelane_b32 v254, s11, 46
	s_add_u32 s10, s8, 0x22680000
	s_addc_u32 s11, s9, 0
	v_writelane_b32 v254, s10, 47
	v_add3_u32 v14, s7, v0, v1
	s_mov_b32 s41, s97
	v_writelane_b32 v254, s11, 48
	s_add_u32 s10, s8, 0x22600000
	s_addc_u32 s11, s9, 0
	v_writelane_b32 v254, s10, 49
	s_nop 1
	v_writelane_b32 v254, s11, 50
	s_lshl_b32 s10, s14, 20
	s_mov_b32 s11, s97
	v_writelane_b32 v254, s10, 51
	s_nop 1
	v_writelane_b32 v254, s11, 52
	s_add_u32 s10, s8, 0x22400000
	s_addc_u32 s11, s9, 0
	v_writelane_b32 v254, s10, 53
	s_nop 1
	v_writelane_b32 v254, s11, 54
	s_lshl_b32 s10, s14, 21
	s_mov_b32 s11, s97
	v_writelane_b32 v254, s10, 55
	s_nop 1
	v_writelane_b32 v254, s11, 56
	s_add_u32 s10, s8, 0x22e80000
	s_addc_u32 s11, s9, 0
	v_writelane_b32 v254, s10, 57
	s_nop 1
	v_writelane_b32 v254, s11, 58
	s_add_u32 s10, s8, 0x27b80000
	s_addc_u32 s11, s9, 0
	v_writelane_b32 v254, s10, 59
	s_nop 1
	v_writelane_b32 v254, s11, 60
	s_add_u32 s10, s8, 0x22880000
	s_addc_u32 s11, s9, 0
	v_writelane_b32 v254, s10, 61
	s_nop 1
	v_writelane_b32 v254, s11, 62
	s_lshl_b32 s10, s14, 22
	s_add_u32 s12, s8, 0x23280000
	s_addc_u32 s13, s9, 0
	v_writelane_b32 v254, s12, 63
	s_mov_b32 s11, s97
	s_nop 0
	v_writelane_b32 v255, s13, 0
	s_mul_i32 s12, s14, 0xac0000
	s_mov_b32 s13, s97
	v_writelane_b32 v255, s12, 1
	s_nop 1
	v_writelane_b32 v255, s13, 2
	s_add_u32 s12, s8, 0x26580000
	s_addc_u32 s13, s9, 0
	v_writelane_b32 v255, s12, 3
	s_nop 1
	v_writelane_b32 v255, s13, 4
	s_add_u32 s12, s8, 0x1d200000
	s_addc_u32 s13, s9, 0
	s_lshl_b32 s40, s14, 11
	v_writelane_b32 v255, s12, 5
	s_add_u32 s16, s8, 0x1e800000
	s_addc_u32 s17, s9, 0
	v_writelane_b32 v255, s13, 6
	v_writelane_b32 v255, s16, 7
	s_mul_i32 s12, s14, 0x1de0000
	s_mul_i32 s14, s14, 0x1580000
	v_writelane_b32 v255, s17, 8
	v_writelane_b32 v255, s14, 9
	s_mov_b32 s13, s97
	s_nop 0
	v_writelane_b32 v255, s15, 10
	s_add_u32 s14, s8, 0x23a80000
	s_addc_u32 s15, s9, 0
	v_writelane_b32 v255, s14, 11
	s_add_u32 s8, s8, 0x1a700000
	s_addc_u32 s9, s9, 0
	v_writelane_b32 v255, s15, 12
	v_writelane_b32 v255, s8, 13
	s_lshl_b64 s[4:5], s[4:5], 2
	s_lshl_b32 s7, s3, 4
	v_writelane_b32 v255, s9, 14
	v_writelane_b32 v255, s4, 15
	s_add_i32 s72, s7, 0xc00
	s_lshl_b32 s7, s3, 1
	v_writelane_b32 v255, s5, 16
	s_lshl_b64 s[4:5], s[10:11], 2
	v_writelane_b32 v255, s4, 17
	s_lshl_b32 s66, s3, 6
	s_lshl_b32 s67, s6, 9
	v_writelane_b32 v255, s5, 18
	s_lshl_b64 s[4:5], s[12:13], 2
	v_writelane_b32 v255, s4, 19
	s_lshl_b32 s68, s3, 5
	s_lshl_b32 s69, s6, 8
	v_writelane_b32 v255, s5, 20
	v_writelane_b32 v255, s80, 21
	s_lshl_b32 s70, s3, 2
	s_lshl_b32 s71, s6, 5
	v_writelane_b32 v255, s81, 22
	v_writelane_b32 v255, s82, 23
	s_lshl_b32 s73, s6, 7
	s_add_i32 s74, s7, 0x13500
	s_lshl_b32 s75, s6, 4
	v_writelane_b32 v255, s83, 24
	s_branch .Lcvp31_31

; __device__ __forceinline__ void conv_load(const ConvItem& ci, int lane, float (&v)[64]) {
;     ...
;     for (int i = 0; i < 64; ++i) { const int k = ci.k0 + i, kk = k < kmax ? k : kmax; v[i] = __builtin_nontemporal_load(base + (size_t)kk * ci.ldw); }
; #pragma unroll
;     for (int i = 0; i < 64; ++i) v[i] = (okc && (ci.k0 + i) < ci.Ksrc) ? v[i] : 0.f;
.Lcvp130_30:
	s_cmp_lt_i32 s58, s76
	s_cselect_b64 s[4:5], -1, 0
	s_and_b64 s[4:5], vcc, s[4:5]
	s_cmp_lt_i32 s64, s76
	s_waitcnt vmcnt(62)
	v_cndmask_b32_e64 v21, 0, v21, s[4:5]
	s_cselect_b64 s[4:5], -1, 0
	s_and_b64 s[4:5], vcc, s[4:5]
	s_cmp_lt_i32 s65, s76
	v_cndmask_b32_e64 v20, 0, v20, s[4:5]
	s_cselect_b64 s[4:5], -1, 0
	s_and_b64 s[4:5], vcc, s[4:5]
	s_cmp_lt_i32 s78, s76
	s_waitcnt vmcnt(61)
	v_cndmask_b32_e64 v19, 0, v19, s[4:5]
	s_cselect_b64 s[4:5], -1, 0
	s_and_b64 s[4:5], vcc, s[4:5]
	s_cmp_lt_i32 s79, s76
	s_waitcnt vmcnt(60)
	v_cndmask_b32_e64 v18, 0, v18, s[4:5]
	s_cselect_b64 s[4:5], -1, 0
	s_and_b64 s[4:5], vcc, s[4:5]
	s_cmp_lt_i32 s80, s76
	s_waitcnt vmcnt(59)
	v_cndmask_b32_e64 v17, 0, v17, s[4:5]
	s_cselect_b64 s[4:5], -1, 0
	s_and_b64 s[4:5], vcc, s[4:5]
	s_cmp_lt_i32 s81, s76
	s_waitcnt vmcnt(58)
	v_cndmask_b32_e64 v16, 0, v16, s[4:5]
	s_cselect_b64 s[4:5], -1, 0
	s_and_b64 s[4:5], vcc, s[4:5]
	s_cmp_lt_i32 s82, s76
	s_waitcnt vmcnt(57)
	v_cndmask_b32_e64 v15, 0, v15, s[4:5]
	s_cselect_b64 s[4:5], -1, 0
	s_and_b64 s[4:5], vcc, s[4:5]
	s_cmp_lt_i32 s83, s76
	s_waitcnt vmcnt(56)
	v_cndmask_b32_e64 v8, 0, v8, s[4:5]
	s_cselect_b64 s[4:5], -1, 0
	s_and_b64 s[4:5], vcc, s[4:5]
	s_cmp_lt_i32 s85, s76
	s_waitcnt vmcnt(55)
	v_cndmask_b32_e64 v29, 0, v29, s[4:5]
	s_cselect_b64 s[4:5], -1, 0
	s_and_b64 s[4:5], vcc, s[4:5]
	s_cmp_lt_i32 s86, s76
	s_waitcnt vmcnt(54)
	v_cndmask_b32_e64 v28, 0, v28, s[4:5]
	s_cselect_b64 s[4:5], -1, 0
	s_and_b64 s[4:5], vcc, s[4:5]
	s_cmp_lt_i32 s87, s76
	s_waitcnt vmcnt(53)
	v_cndmask_b32_e64 v27, 0, v27, s[4:5]
	s_cselect_b64 s[4:5], -1, 0
	s_and_b64 s[4:5], vcc, s[4:5]
	s_cmp_lt_i32 s88, s76
	s_waitcnt vmcnt(52)
	v_cndmask_b32_e64 v26, 0, v26, s[4:5]
	s_cselect_b64 s[4:5], -1, 0
	s_and_b64 s[4:5], vcc, s[4:5]
	s_cmp_lt_i32 s89, s76
	s_waitcnt vmcnt(51)
	v_cndmask_b32_e64 v25, 0, v25, s[4:5]
	s_cselect_b64 s[4:5], -1, 0
	s_and_b64 s[4:5], vcc, s[4:5]
	s_cmp_lt_i32 s90, s76
	s_waitcnt vmcnt(50)
	v_cndmask_b32_e64 v24, 0, v24, s[4:5]
	s_cselect_b64 s[4:5], -1, 0
	s_and_b64 s[4:5], vcc, s[4:5]
	s_cmp_lt_i32 s92, s76
	s_waitcnt vmcnt(49)
	v_cndmask_b32_e64 v23, 0, v23, s[4:5]
	s_cselect_b64 s[4:5], -1, 0
	s_and_b64 s[4:5], vcc, s[4:5]
	s_cmp_lt_i32 s93, s76
	s_waitcnt vmcnt(48)
	v_cndmask_b32_e64 v22, 0, v22, s[4:5]
	s_cselect_b64 s[4:5], -1, 0
	s_and_b64 s[4:5], vcc, s[4:5]
	s_cmp_lt_i32 s94, s76
	s_waitcnt vmcnt(47)
	v_cndmask_b32_e64 v37, 0, v37, s[4:5]
	s_cselect_b64 s[4:5], -1, 0
	s_and_b64 s[4:5], vcc, s[4:5]
	s_cmp_lt_i32 s95, s76
	s_waitcnt vmcnt(46)
	v_cndmask_b32_e64 v36, 0, v36, s[4:5]
	s_cselect_b64 s[4:5], -1, 0
	s_and_b64 s[4:5], vcc, s[4:5]
	s_cmp_lt_i32 s50, s76
	s_waitcnt vmcnt(45)
	v_cndmask_b32_e64 v35, 0, v35, s[4:5]
	s_cselect_b64 s[4:5], -1, 0
	s_and_b64 s[4:5], vcc, s[4:5]
	s_cmp_lt_i32 s51, s76
	s_waitcnt vmcnt(44)
	v_cndmask_b32_e64 v34, 0, v34, s[4:5]
	s_cselect_b64 s[4:5], -1, 0
	s_and_b64 s[4:5], vcc, s[4:5]
	s_cmp_lt_i32 s52, s76
	s_waitcnt vmcnt(43)
	v_cndmask_b32_e64 v33, 0, v33, s[4:5]
	s_cselect_b64 s[4:5], -1, 0
	s_and_b64 s[4:5], vcc, s[4:5]
	s_cmp_lt_i32 s53, s76
	s_waitcnt vmcnt(42)
	v_cndmask_b32_e64 v32, 0, v32, s[4:5]
	s_cselect_b64 s[4:5], -1, 0
	s_and_b64 s[4:5], vcc, s[4:5]
	s_cmp_lt_i32 s6, s76
	s_waitcnt vmcnt(41)
	v_cndmask_b32_e64 v31, 0, v31, s[4:5]
	s_cselect_b64 s[4:5], -1, 0
	s_and_b64 s[4:5], vcc, s[4:5]
	s_cmp_lt_i32 s7, s76
	s_waitcnt vmcnt(40)
	v_cndmask_b32_e64 v30, 0, v30, s[4:5]
	s_cselect_b64 s[4:5], -1, 0
	s_and_b64 s[4:5], vcc, s[4:5]
	s_cmp_lt_i32 s8, s76
	s_waitcnt vmcnt(39)
	v_cndmask_b32_e64 v45, 0, v45, s[4:5]
	s_cselect_b64 s[4:5], -1, 0
	s_and_b64 s[4:5], vcc, s[4:5]
	s_cmp_lt_i32 s9, s76
	s_waitcnt vmcnt(38)
	v_cndmask_b32_e64 v44, 0, v44, s[4:5]
	s_cselect_b64 s[4:5], -1, 0
	s_and_b64 s[4:5], vcc, s[4:5]
	s_cmp_lt_i32 s10, s76
	s_waitcnt vmcnt(37)
	v_cndmask_b32_e64 v43, 0, v43, s[4:5]
	s_cselect_b64 s[4:5], -1, 0
	s_and_b64 s[4:5], vcc, s[4:5]
	s_cmp_lt_i32 s11, s76
	s_waitcnt vmcnt(36)
	v_cndmask_b32_e64 v42, 0, v42, s[4:5]
	s_cselect_b64 s[4:5], -1, 0
	s_and_b64 s[4:5], vcc, s[4:5]
	s_cmp_lt_i32 s14, s76
	s_waitcnt vmcnt(35)
	v_cndmask_b32_e64 v41, 0, v41, s[4:5]
	s_cselect_b64 s[4:5], -1, 0
	s_and_b64 s[4:5], vcc, s[4:5]
	s_cmp_lt_i32 s15, s76
	s_waitcnt vmcnt(34)
	v_cndmask_b32_e64 v40, 0, v40, s[4:5]
	s_cselect_b64 s[4:5], -1, 0
	s_and_b64 s[4:5], vcc, s[4:5]
	s_cmp_lt_i32 s16, s76
	s_waitcnt vmcnt(33)
	v_cndmask_b32_e64 v39, 0, v39, s[4:5]
	s_cselect_b64 s[4:5], -1, 0
	s_and_b64 s[4:5], vcc, s[4:5]
	s_cmp_lt_i32 s17, s76
	s_waitcnt vmcnt(32)
	v_cndmask_b32_e64 v38, 0, v38, s[4:5]
	s_cselect_b64 s[4:5], -1, 0
	s_and_b64 s[4:5], vcc, s[4:5]
	s_cmp_lt_i32 s12, s76
	s_waitcnt vmcnt(31)
	v_cndmask_b32_e64 v53, 0, v53, s[4:5]
	s_cselect_b64 s[4:5], -1, 0
	s_and_b64 s[4:5], vcc, s[4:5]
	s_cmp_lt_i32 s13, s76
	s_waitcnt vmcnt(30)
	v_cndmask_b32_e64 v52, 0, v52, s[4:5]
	s_cselect_b64 s[4:5], -1, 0
	s_and_b64 s[4:5], vcc, s[4:5]
	s_cmp_lt_i32 s20, s76
	s_waitcnt vmcnt(29)
	v_cndmask_b32_e64 v51, 0, v51, s[4:5]
	s_cselect_b64 s[4:5], -1, 0
	s_and_b64 s[4:5], vcc, s[4:5]
	s_cmp_lt_i32 s21, s76
	s_waitcnt vmcnt(28)
	v_cndmask_b32_e64 v50, 0, v50, s[4:5]
	s_cselect_b64 s[4:5], -1, 0
	s_and_b64 s[4:5], vcc, s[4:5]
	s_cmp_lt_i32 s24, s76
	s_waitcnt vmcnt(27)
	v_cndmask_b32_e64 v49, 0, v49, s[4:5]
	s_cselect_b64 s[4:5], -1, 0
	s_and_b64 s[4:5], vcc, s[4:5]
	s_cmp_lt_i32 s25, s76
	s_waitcnt vmcnt(26)
	v_cndmask_b32_e64 v48, 0, v48, s[4:5]
	s_cselect_b64 s[4:5], -1, 0
	s_and_b64 s[4:5], vcc, s[4:5]
	s_cmp_lt_i32 s26, s76
	s_waitcnt vmcnt(25)
	v_cndmask_b32_e64 v47, 0, v47, s[4:5]
	s_cselect_b64 s[4:5], -1, 0
	s_and_b64 s[4:5], vcc, s[4:5]
	s_cmp_lt_i32 s27, s76
	s_waitcnt vmcnt(24)
; #define LAS __attribute__((address_space(3)))
; #define LDS_WAIT() asm volatile("s_waitcnt lgkmcnt(0)" ::: "memory")
; __device__ __forceinline__ void conv_load(const ConvItem& ci, int lane, float (&v)[64]) {
;     const bool okc = ci.srcc >= 0 && (ci.srcc + lane) < ci.ncols;
;     const float* base = ci.W + (okc ? ci.srcc + lane : 0);
;     const int kmax = ci.Ksrc - 1;
; #pragma unroll
;     for (int i = 0; i < 64; ++i) { const int k = ci.k0 + i, kk = k < kmax ? k : kmax; v[i] = __builtin_nontemporal_load(base + (size_t)kk * ci.ldw); }
; #pragma unroll
;     for (int i = 0; i < 64; ++i) v[i] = (okc && (ci.k0 + i) < ci.Ksrc) ? v[i] : 0.f;
; }
; __device__ __forceinline__ void conv_store(const ConvItem& ci, LAS float* scr, int lane, const float (&v)[64]) {
;     const int c = lane & 7;
;     f32x4 s0 = {1.f, 1.f, 1.f, 1.f}, s1 = s0;
;     if (ci.ks) { const int kb = ci.k0 + 8 * c < ci.Ksrc - 8 ? ci.k0 + 8 * c : ci.Ksrc - 8; s0 = *(const f32x4*)(ci.ks + kb); s1 = *(const f32x4*)(ci.ks + kb + 4); }
; #pragma unroll
;     for (int i = 0; i < 64; ++i) scr[i * 65 + lane] = v[i];
;     LDS_WAIT(); asm volatile("" ::: "memory");
	v_cndmask_b32_e64 v46, 0, v46, s[4:5]
	s_cselect_b64 s[4:5], -1, 0
	s_and_b64 s[4:5], vcc, s[4:5]
	s_cmp_lt_i32 s18, s76
	s_waitcnt vmcnt(23)
	v_cndmask_b32_e64 v61, 0, v61, s[4:5]
	s_cselect_b64 s[4:5], -1, 0
	s_and_b64 s[4:5], vcc, s[4:5]
	s_cmp_lt_i32 s19, s76
	s_waitcnt vmcnt(22)
	v_cndmask_b32_e64 v60, 0, v60, s[4:5]
	s_cselect_b64 s[4:5], -1, 0
	s_and_b64 s[4:5], vcc, s[4:5]
	s_cmp_lt_i32 s28, s76
	s_waitcnt vmcnt(21)
	v_cndmask_b32_e64 v59, 0, v59, s[4:5]
	s_cselect_b64 s[4:5], -1, 0
	s_and_b64 s[4:5], vcc, s[4:5]
	s_cmp_lt_i32 s29, s76
	s_waitcnt vmcnt(20)
	v_cndmask_b32_e64 v58, 0, v58, s[4:5]
	s_cselect_b64 s[4:5], -1, 0
	s_and_b64 s[4:5], vcc, s[4:5]
	s_cmp_lt_i32 s22, s76
	s_waitcnt vmcnt(19)
	v_cndmask_b32_e64 v57, 0, v57, s[4:5]
	s_cselect_b64 s[4:5], -1, 0
	s_and_b64 s[4:5], vcc, s[4:5]
	s_cmp_lt_i32 s23, s76
	s_waitcnt vmcnt(18)
	v_cndmask_b32_e64 v56, 0, v56, s[4:5]
	s_cselect_b64 s[4:5], -1, 0
	s_and_b64 s[4:5], vcc, s[4:5]
	s_cmp_lt_i32 s30, s76
	s_waitcnt vmcnt(17)
	v_cndmask_b32_e64 v55, 0, v55, s[4:5]
	s_cselect_b64 s[4:5], -1, 0
	s_and_b64 s[4:5], vcc, s[4:5]
	s_cmp_lt_i32 s31, s76
	s_waitcnt vmcnt(16)
	v_cndmask_b32_e64 v54, 0, v54, s[4:5]
	s_cselect_b64 s[4:5], -1, 0
	s_and_b64 s[4:5], vcc, s[4:5]
	s_cmp_lt_i32 s36, s76
	s_waitcnt vmcnt(15)
	v_cndmask_b32_e64 v70, 0, v70, s[4:5]
	s_cselect_b64 s[4:5], -1, 0
	s_and_b64 s[4:5], vcc, s[4:5]
	s_cmp_lt_i32 s37, s76
	s_waitcnt vmcnt(14)
	v_cndmask_b32_e64 v69, 0, v69, s[4:5]
	s_cselect_b64 s[4:5], -1, 0
	s_and_b64 s[4:5], vcc, s[4:5]
	s_cmp_lt_i32 s38, s76
	s_waitcnt vmcnt(13)
	v_cndmask_b32_e64 v68, 0, v68, s[4:5]
	s_cselect_b64 s[4:5], -1, 0
	s_and_b64 s[4:5], vcc, s[4:5]
	s_cmp_lt_i32 s39, s76
	s_waitcnt vmcnt(12)
	v_cndmask_b32_e64 v67, 0, v67, s[4:5]
	s_cselect_b64 s[4:5], -1, 0
	s_and_b64 s[4:5], vcc, s[4:5]
	s_cmp_lt_i32 s34, s76
	s_waitcnt vmcnt(11)
	v_cndmask_b32_e64 v66, 0, v66, s[4:5]
	s_cselect_b64 s[4:5], -1, 0
	s_and_b64 s[4:5], vcc, s[4:5]
	s_cmp_lt_i32 s35, s76
	s_waitcnt vmcnt(10)
	v_cndmask_b32_e64 v64, 0, v64, s[4:5]
	s_cselect_b64 s[4:5], -1, 0
	s_and_b64 s[4:5], vcc, s[4:5]
	s_cmp_lt_i32 s42, s76
	s_waitcnt vmcnt(9)
	v_cndmask_b32_e64 v63, 0, v63, s[4:5]
	s_cselect_b64 s[4:5], -1, 0
	s_and_b64 s[4:5], vcc, s[4:5]
	s_cmp_lt_i32 s43, s76
	s_waitcnt vmcnt(8)
	v_cndmask_b32_e64 v62, 0, v62, s[4:5]
	s_cselect_b64 s[4:5], -1, 0
	s_and_b64 s[4:5], vcc, s[4:5]
	s_cmp_lt_i32 s54, s76
	s_waitcnt vmcnt(7)
	v_cndmask_b32_e64 v65, 0, v65, s[4:5]
	s_cselect_b64 s[4:5], -1, 0
	s_and_b64 s[4:5], vcc, s[4:5]
	s_cmp_lt_i32 s55, s76
	s_waitcnt vmcnt(6)
	v_cndmask_b32_e64 v74, 0, v74, s[4:5]
	s_cselect_b64 s[4:5], -1, 0
	s_and_b64 s[4:5], vcc, s[4:5]
	s_cmp_lt_i32 s46, s76
	ds_write2_b32 v12, v21, v20 offset1:65
	ds_write2_b32 v12, v19, v18 offset0:130 offset1:195
	v_add_u32_e32 v18, 0x400, v12
	s_waitcnt vmcnt(5)
	v_cndmask_b32_e64 v73, 0, v73, s[4:5]
	s_cselect_b64 s[4:5], -1, 0
	ds_write2_b32 v18, v17, v16 offset0:4 offset1:69
	ds_write2_b32 v18, v15, v8 offset0:134 offset1:199
	v_add_u32_e32 v8, 0x800, v12
	s_and_b64 s[4:5], vcc, s[4:5]
	ds_write2_b32 v8, v29, v28 offset0:8 offset1:73
	ds_write2_b32 v8, v27, v26 offset0:138 offset1:203
	v_add_u32_e32 v8, 0xc00, v12
	s_cmp_lt_i32 s47, s76
	ds_write2_b32 v8, v25, v24 offset0:12 offset1:77
	ds_write2_b32 v8, v23, v22 offset0:142 offset1:207
	v_add_u32_e32 v8, 0x1000, v12
	s_waitcnt vmcnt(4)
	v_cndmask_b32_e64 v72, 0, v72, s[4:5]
	s_cselect_b64 s[4:5], -1, 0
	ds_write2_b32 v8, v37, v36 offset0:16 offset1:81
	ds_write2_b32 v8, v35, v34 offset0:146 offset1:211
	v_add_u32_e32 v8, 0x1400, v12
	s_and_b64 s[4:5], vcc, s[4:5]
	ds_write2_b32 v8, v33, v32 offset0:20 offset1:85
	ds_write2_b32 v8, v31, v30 offset0:150 offset1:215
	v_add_u32_e32 v8, 0x1800, v12
	s_cmp_lt_i32 s48, s76
	ds_write2_b32 v8, v45, v44 offset0:24 offset1:89
	ds_write2_b32 v8, v43, v42 offset0:154 offset1:219
	v_add_u32_e32 v8, 0x1c00, v12
	s_waitcnt vmcnt(3)
	v_cndmask_b32_e64 v71, 0, v71, s[4:5]
	s_cselect_b64 s[4:5], -1, 0
	ds_write2_b32 v8, v41, v40 offset0:28 offset1:93
	ds_write2_b32 v8, v39, v38 offset0:158 offset1:223
	v_add_u32_e32 v8, 0x2000, v12
	s_and_b64 s[4:5], vcc, s[4:5]
	ds_write2_b32 v8, v53, v52 offset0:32 offset1:97
	ds_write2_b32 v8, v51, v50 offset0:162 offset1:227
	v_add_u32_e32 v8, 0x2400, v12
	s_cmp_lt_i32 s49, s76
	ds_write2_b32 v8, v49, v48 offset0:36 offset1:101
	ds_write2_b32 v8, v47, v46 offset0:166 offset1:231
	v_add_u32_e32 v8, 0x2800, v12
	s_waitcnt vmcnt(2)
	v_cndmask_b32_e64 v77, 0, v77, s[4:5]
	s_cselect_b64 s[4:5], -1, 0
	ds_write2_b32 v8, v61, v60 offset0:40 offset1:105
	ds_write2_b32 v8, v59, v58 offset0:170 offset1:235
	v_add_u32_e32 v8, 0x2c00, v12
	s_and_b64 s[4:5], vcc, s[4:5]
	ds_write2_b32 v8, v57, v56 offset0:44 offset1:109
	ds_write2_b32 v8, v55, v54 offset0:174 offset1:239
	v_add_u32_e32 v8, 0x3000, v12
	s_cmp_lt_i32 s44, s76
	ds_write2_b32 v8, v70, v69 offset0:48 offset1:113
	ds_write2_b32 v8, v68, v67 offset0:178 offset1:243
	v_add_u32_e32 v8, 0x3400, v12
	s_waitcnt vmcnt(1)
	v_cndmask_b32_e64 v76, 0, v76, s[4:5]
	s_cselect_b64 s[4:5], -1, 0
	ds_write2_b32 v8, v66, v64 offset0:52 offset1:117
	ds_write2_b32 v8, v63, v62 offset0:182 offset1:247
	v_add_u32_e32 v8, 0x3800, v12
	s_and_b64 vcc, vcc, s[4:5]
	ds_write2_b32 v8, v65, v74 offset0:56 offset1:121
	ds_write2_b32 v8, v73, v72 offset0:186 offset1:251
	v_add_u32_e32 v8, 0x3c00, v12
	s_waitcnt vmcnt(0)
	v_cndmask_b32_e32 v75, 0, v75, vcc
	ds_write2_b32 v8, v71, v77 offset0:60 offset1:125
	ds_write2_b32 v8, v76, v75 offset0:190 offset1:255
	s_waitcnt lgkmcnt(0)
; __device__ __forceinline__ unsigned cvt_pk_bf16(float lo, float hi) { unsigned r; asm volatile("v_cvt_pk_bf16_f32 %0, %1, %2" : "=v"(r) : "v"(lo), "v"(hi)); return r; }
; #define LAS __attribute__((address_space(3)))
; #define LDS_WAIT() asm volatile("s_waitcnt lgkmcnt(0)" ::: "memory")
; __device__ __forceinline__ void conv_store(const ConvItem& ci, LAS float* scr, int lane, const float (&v)[64]) {
;     ...
;     for (int j = 0; j < 8; ++j) { const int n = (lane >> 3) + 8 * j; const LAS float* s = scr + (8 * c) * 65 + n;
;         v4u o; o.x = cvt_pk_bf16(s[0 * 65] * s0[0], s[1 * 65] * s0[1]); o.y = cvt_pk_bf16(s[2 * 65] * s0[2], s[3 * 65] * s0[3]); o.z = cvt_pk_bf16(s[4 * 65] * s1[0], s[5 * 65] * s1[1]); o.w = cvt_pk_bf16(s[6 * 65] * s1[2], s[7 * 65] * s1[3]);
;         *(v4u*)(ci.dst + (size_t)(ci.drow0 + n) * ci.ldd + ci.k0 + 8 * c) = o; }
;     LDS_WAIT(); asm volatile("" ::: "memory");
; }
	v_add_u32_e32 v192, 0x400, v14
	ds_read2_b32 v[128:129], v14 offset1:65
	ds_read2_b32 v[130:131], v14 offset0:130 offset1:195
	ds_read2_b32 v[132:133], v192 offset0:4 offset1:69
	ds_read2_b32 v[134:135], v192 offset0:134 offset1:199
	ds_read2_b32 v[136:137], v14 offset0:8 offset1:73
	ds_read2_b32 v[138:139], v14 offset0:138 offset1:203
	ds_read2_b32 v[140:141], v192 offset0:12 offset1:77
	ds_read2_b32 v[142:143], v192 offset0:142 offset1:207
	ds_read2_b32 v[144:145], v14 offset0:16 offset1:81
	ds_read2_b32 v[146:147], v14 offset0:146 offset1:211
	ds_read2_b32 v[148:149], v192 offset0:20 offset1:85
	ds_read2_b32 v[150:151], v192 offset0:150 offset1:215
	ds_read2_b32 v[152:153], v14 offset0:24 offset1:89
	ds_read2_b32 v[154:155], v14 offset0:154 offset1:219
	ds_read2_b32 v[156:157], v192 offset0:28 offset1:93
	ds_read2_b32 v[158:159], v192 offset0:158 offset1:223
	ds_read2_b32 v[160:161], v14 offset0:32 offset1:97
	ds_read2_b32 v[162:163], v14 offset0:162 offset1:227
	ds_read2_b32 v[164:165], v192 offset0:36 offset1:101
	ds_read2_b32 v[166:167], v192 offset0:166 offset1:231
	ds_read2_b32 v[168:169], v14 offset0:40 offset1:105
	ds_read2_b32 v[170:171], v14 offset0:170 offset1:235
	ds_read2_b32 v[172:173], v192 offset0:44 offset1:109
	ds_read2_b32 v[174:175], v192 offset0:174 offset1:239
	ds_read2_b32 v[176:177], v14 offset0:48 offset1:113
	ds_read2_b32 v[178:179], v14 offset0:178 offset1:243
	ds_read2_b32 v[180:181], v192 offset0:52 offset1:117
	ds_read2_b32 v[182:183], v192 offset0:182 offset1:247
	ds_read2_b32 v[184:185], v14 offset0:56 offset1:121
	ds_read2_b32 v[186:187], v14 offset0:186 offset1:251
	ds_read2_b32 v[188:189], v192 offset0:60 offset1:125
	ds_read2_b32 v[190:191], v192 offset0:190 offset1:255
	s_waitcnt lgkmcnt(0)
	v_add_u32_e32 v24, s59, v13
	v_mul_lo_u32 v22, s57, v24
	s_ashr_i32 s59, s58, 31
	v_readlane_b32 s76, v254, 31
	s_waitcnt lgkmcnt(0)
	v_mul_f32_e32 v8, v4, v128
	v_mul_f32_e32 v15, v5, v129
	v_cvt_pk_bf16_f32 v16, v8, v15
	s_add_i32 s3, s3, s33
	s_add_i32 s66, s66, s67
	s_add_i32 s68, s68, s69
	s_add_i32 s70, s70, s71
	s_waitcnt lgkmcnt(0)
	v_mul_f32_e32 v15, v7, v131
	v_mul_f32_e32 v8, v6, v130
	v_cvt_pk_bf16_f32 v17, v8, v15
	v_add_u32_e32 v15, 0x400, v14
	s_add_i32 s72, s72, s73
	s_add_i32 s74, s74, s75
	v_readlane_b32 s78, v254, 33
	v_readlane_b32 s79, v254, 34
	s_waitcnt lgkmcnt(0)
	v_mul_f32_e32 v8, v0, v132
	v_mul_f32_e32 v18, v1, v133
	v_cvt_pk_bf16_f32 v18, v8, v18
	v_readlane_b32 s80, v255, 21
	v_readlane_b32 s77, v254, 32
	s_movk_i32 s78, 0x1580
	v_readlane_b32 s82, v255, 23
	s_waitcnt lgkmcnt(0)
	v_mul_f32_e32 v8, v2, v134
	v_mul_f32_e32 v19, v3, v135
	v_cvt_pk_bf16_f32 v19, v8, v19
	v_ashrrev_i32_e32 v8, 31, v24
	v_mul_lo_u32 v8, s56, v8
	v_mad_u64_u32 v[20:21], s[4:5], s56, v24, 0
	v_add3_u32 v21, v21, v8, v22
	v_lshl_add_u64 v[20:21], v[20:21], 1, s[60:61]
	s_lshl_b64 s[4:5], s[58:59], 1
	v_lshl_add_u64 v[20:21], v[20:21], 0, s[4:5]
	v_lshlrev_b32_e32 v8, 1, v10
	v_lshl_add_u64 v[20:21], v[20:21], 0, v[8:9]
	global_store_dwordx4 v[20:21], v[16:19], off
	s_cmpk_lt_i32 s3, 18688
	v_readlane_b32 s83, v255, 24
	s_waitcnt lgkmcnt(0)
	v_mul_f32_e32 v16, v4, v136
	v_mul_f32_e32 v17, v5, v137
	v_cvt_pk_bf16_f32 v16, v16, v17
	s_mov_b32 s79, 0x3f22f983
	s_mov_b32 s85, 0xbfc90fda
	s_brev_b32 s86, 1
	s_movk_i32 s87, 0x1f8
	s_waitcnt lgkmcnt(0)
	v_mul_f32_e32 v17, v6, v138
	v_mul_f32_e32 v18, v7, v139
	v_cvt_pk_bf16_f32 v17, v17, v18
	s_mov_b64 s[88:89], 0x80
	s_mov_b64 s[92:93], 0x4000
	s_mov_b64 s[94:95], 0x4800
	v_readlane_b32 s81, v255, 22
	s_waitcnt lgkmcnt(0)
	v_mul_f32_e32 v18, v0, v140
	v_mul_f32_e32 v19, v1, v141
	v_cvt_pk_bf16_f32 v18, v18, v19
	s_waitcnt lgkmcnt(0)
	v_mul_f32_e32 v19, v2, v142
	v_mul_f32_e32 v20, v3, v143
	v_cvt_pk_bf16_f32 v19, v19, v20
	v_add_u32_e32 v20, 8, v24
	v_ashrrev_i32_e32 v21, 31, v20
	v_mul_lo_u32 v22, s56, v21
	v_mul_lo_u32 v23, s57, v20
	v_mad_u64_u32 v[20:21], s[6:7], s56, v20, 0
	v_add3_u32 v21, v21, v22, v23
	v_lshl_add_u64 v[20:21], v[20:21], 1, s[60:61]
	v_lshl_add_u64 v[20:21], v[20:21], 0, s[4:5]
	v_lshl_add_u64 v[20:21], v[20:21], 0, v[8:9]
	global_store_dwordx4 v[20:21], v[16:19], off
	s_waitcnt lgkmcnt(0)
	s_nop 0
	v_mul_f32_e32 v16, v4, v144
	v_mul_f32_e32 v17, v5, v145
	v_cvt_pk_bf16_f32 v16, v16, v17
	s_waitcnt lgkmcnt(0)
	v_mul_f32_e32 v17, v6, v146
	v_mul_f32_e32 v18, v7, v147
	v_cvt_pk_bf16_f32 v17, v17, v18
	s_waitcnt lgkmcnt(0)
	v_mul_f32_e32 v18, v0, v148
	v_mul_f32_e32 v19, v1, v149
	v_cvt_pk_bf16_f32 v18, v18, v19
	s_waitcnt lgkmcnt(0)
; __device__ __forceinline__ unsigned cvt_pk_bf16(float lo, float hi) { unsigned r; asm volatile("v_cvt_pk_bf16_f32 %0, %1, %2" : "=v"(r) : "v"(lo), "v"(hi)); return r; }
; #define LAS __attribute__((address_space(3)))
; #define LDS_WAIT() asm volatile("s_waitcnt lgkmcnt(0)" ::: "memory")
; __device__ __forceinline__ void conv_store(const ConvItem& ci, LAS float* scr, int lane, const float (&v)[64]) {
;     ...
;     for (int j = 0; j < 8; ++j) { const int n = (lane >> 3) + 8 * j; const LAS float* s = scr + (8 * c) * 65 + n;
;         v4u o; o.x = cvt_pk_bf16(s[0 * 65] * s0[0], s[1 * 65] * s0[1]); o.y = cvt_pk_bf16(s[2 * 65] * s0[2], s[3 * 65] * s0[3]); o.z = cvt_pk_bf16(s[4 * 65] * s1[0], s[5 * 65] * s1[1]); o.w = cvt_pk_bf16(s[6 * 65] * s1[2], s[7 * 65] * s1[3]);
;         *(v4u*)(ci.dst + (size_t)(ci.drow0 + n) * ci.ldd + ci.k0 + 8 * c) = o; }
;     LDS_WAIT(); asm volatile("" ::: "memory");
; }
; __global__ void __launch_bounds__(NWAVES * 64, 2) mk_fwd(Args args) {
;     ...
;             for (int it = gw; it < NITEMS; it += NGW) {
	v_mul_f32_e32 v19, v2, v150
	v_mul_f32_e32 v20, v3, v151
	v_cvt_pk_bf16_f32 v19, v19, v20
	v_add_u32_e32 v20, 16, v24
	v_ashrrev_i32_e32 v21, 31, v20
	v_mul_lo_u32 v22, s56, v21
	v_mul_lo_u32 v23, s57, v20
	v_mad_u64_u32 v[20:21], s[6:7], s56, v20, 0
	v_add3_u32 v21, v21, v22, v23
	v_lshl_add_u64 v[20:21], v[20:21], 1, s[60:61]
	v_lshl_add_u64 v[20:21], v[20:21], 0, s[4:5]
	v_lshl_add_u64 v[20:21], v[20:21], 0, v[8:9]
	global_store_dwordx4 v[20:21], v[16:19], off
	s_waitcnt lgkmcnt(0)
	s_nop 0
	v_mul_f32_e32 v16, v4, v152
	v_mul_f32_e32 v17, v5, v153
	v_cvt_pk_bf16_f32 v16, v16, v17
	s_waitcnt lgkmcnt(0)
	v_mul_f32_e32 v17, v6, v154
	v_mul_f32_e32 v18, v7, v155
	v_cvt_pk_bf16_f32 v17, v17, v18
	s_waitcnt lgkmcnt(0)
	v_mul_f32_e32 v18, v0, v156
	v_mul_f32_e32 v19, v1, v157
	v_cvt_pk_bf16_f32 v18, v18, v19
	s_waitcnt lgkmcnt(0)
	v_mul_f32_e32 v19, v2, v158
	v_mul_f32_e32 v20, v3, v159
	v_cvt_pk_bf16_f32 v19, v19, v20
	v_add_u32_e32 v20, 24, v24
	v_ashrrev_i32_e32 v21, 31, v20
	v_mul_lo_u32 v22, s56, v21
	v_mul_lo_u32 v23, s57, v20
	v_mad_u64_u32 v[20:21], s[6:7], s56, v20, 0
	v_add3_u32 v21, v21, v22, v23
	v_lshl_add_u64 v[20:21], v[20:21], 1, s[60:61]
	v_lshl_add_u64 v[20:21], v[20:21], 0, s[4:5]
	v_lshl_add_u64 v[20:21], v[20:21], 0, v[8:9]
	global_store_dwordx4 v[20:21], v[16:19], off
	s_waitcnt lgkmcnt(0)
	s_nop 0
	v_mul_f32_e32 v16, v4, v160
	v_mul_f32_e32 v17, v5, v161
	v_cvt_pk_bf16_f32 v16, v16, v17
	s_waitcnt lgkmcnt(0)
	v_mul_f32_e32 v17, v6, v162
	v_mul_f32_e32 v18, v7, v163
	v_cvt_pk_bf16_f32 v17, v17, v18
	s_waitcnt lgkmcnt(0)
	v_mul_f32_e32 v18, v0, v164
	v_mul_f32_e32 v19, v1, v165
	v_cvt_pk_bf16_f32 v18, v18, v19
	s_waitcnt lgkmcnt(0)
	v_mul_f32_e32 v19, v2, v166
	v_mul_f32_e32 v20, v3, v167
	v_cvt_pk_bf16_f32 v19, v19, v20
	v_add_u32_e32 v20, 32, v24
	v_ashrrev_i32_e32 v21, 31, v20
	v_mul_lo_u32 v22, s56, v21
	v_mul_lo_u32 v23, s57, v20
	v_mad_u64_u32 v[20:21], s[6:7], s56, v20, 0
	v_add3_u32 v21, v21, v22, v23
	v_lshl_add_u64 v[20:21], v[20:21], 1, s[60:61]
	v_lshl_add_u64 v[20:21], v[20:21], 0, s[4:5]
	v_lshl_add_u64 v[20:21], v[20:21], 0, v[8:9]
	global_store_dwordx4 v[20:21], v[16:19], off
	s_waitcnt lgkmcnt(0)
	s_nop 0
	v_mul_f32_e32 v16, v4, v168
	v_mul_f32_e32 v17, v5, v169
	v_cvt_pk_bf16_f32 v16, v16, v17
	s_waitcnt lgkmcnt(0)
	v_mul_f32_e32 v17, v6, v170
	v_mul_f32_e32 v18, v7, v171
	v_cvt_pk_bf16_f32 v17, v17, v18
	s_waitcnt lgkmcnt(0)
	v_mul_f32_e32 v18, v0, v172
	v_mul_f32_e32 v19, v1, v173
	v_cvt_pk_bf16_f32 v18, v18, v19
	s_waitcnt lgkmcnt(0)
	v_mul_f32_e32 v19, v2, v174
	v_mul_f32_e32 v20, v3, v175
	v_cvt_pk_bf16_f32 v19, v19, v20
	v_add_u32_e32 v20, 40, v24
	v_ashrrev_i32_e32 v21, 31, v20
	v_mul_lo_u32 v22, s56, v21
	v_mul_lo_u32 v23, s57, v20
	v_mad_u64_u32 v[20:21], s[6:7], s56, v20, 0
	v_add3_u32 v21, v21, v22, v23
	v_lshl_add_u64 v[20:21], v[20:21], 1, s[60:61]
	v_lshl_add_u64 v[20:21], v[20:21], 0, s[4:5]
	v_lshl_add_u64 v[20:21], v[20:21], 0, v[8:9]
	global_store_dwordx4 v[20:21], v[16:19], off
	s_waitcnt lgkmcnt(0)
	s_nop 0
	v_mul_f32_e32 v16, v4, v176
	v_mul_f32_e32 v17, v5, v177
	v_cvt_pk_bf16_f32 v16, v16, v17
	s_waitcnt lgkmcnt(0)
	v_mul_f32_e32 v17, v6, v178
	v_mul_f32_e32 v18, v7, v179
	v_cvt_pk_bf16_f32 v17, v17, v18
	s_waitcnt lgkmcnt(0)
	v_mul_f32_e32 v18, v0, v180
	v_mul_f32_e32 v19, v1, v181
	v_cvt_pk_bf16_f32 v18, v18, v19
	s_waitcnt lgkmcnt(0)
	v_mul_f32_e32 v19, v2, v182
	v_mul_f32_e32 v20, v3, v183
	v_cvt_pk_bf16_f32 v19, v19, v20
	v_add_u32_e32 v20, 48, v24
	v_ashrrev_i32_e32 v21, 31, v20
	v_mul_lo_u32 v22, s56, v21
	v_mul_lo_u32 v23, s57, v20
	v_mad_u64_u32 v[20:21], s[6:7], s56, v20, 0
	v_add3_u32 v21, v21, v22, v23
	v_lshl_add_u64 v[20:21], v[20:21], 1, s[60:61]
	v_lshl_add_u64 v[20:21], v[20:21], 0, s[4:5]
	v_lshl_add_u64 v[20:21], v[20:21], 0, v[8:9]
	global_store_dwordx4 v[20:21], v[16:19], off
	s_waitcnt lgkmcnt(0)
	v_mul_f32_e32 v4, v4, v184
	v_mul_f32_e32 v5, v5, v185
	v_cvt_pk_bf16_f32 v4, v4, v5
	s_waitcnt lgkmcnt(0)
	v_mul_f32_e32 v5, v6, v186
	v_mul_f32_e32 v6, v7, v187
	v_cvt_pk_bf16_f32 v5, v5, v6
	s_waitcnt lgkmcnt(0)
	v_mul_f32_e32 v0, v0, v188
	v_mul_f32_e32 v1, v1, v189
	v_cvt_pk_bf16_f32 v6, v0, v1
	s_waitcnt lgkmcnt(0)
	v_mul_f32_e32 v0, v2, v190
	v_mul_f32_e32 v1, v3, v191
	v_cvt_pk_bf16_f32 v7, v0, v1
	v_add_u32_e32 v0, 56, v24
	v_ashrrev_i32_e32 v1, 31, v0
	v_mul_lo_u32 v2, s56, v1
	v_mul_lo_u32 v3, s57, v0
	v_mad_u64_u32 v[0:1], s[6:7], s56, v0, 0
	v_add3_u32 v1, v1, v2, v3
	v_lshl_add_u64 v[0:1], v[0:1], 1, s[60:61]
	v_lshl_add_u64 v[0:1], v[0:1], 0, s[4:5]
	v_lshl_add_u64 v[0:1], v[0:1], 0, v[8:9]
	global_store_dwordx4 v[0:1], v[4:7], off
	s_waitcnt lgkmcnt(0)
	s_cbranch_scc0 .Lcvp130_ret

; #define LAS __attribute__((address_space(3)))
; __global__ void __launch_bounds__(NWAVES * 64, 2) mk_fwd(Args args) {
;     ...
;             PH_LOCALS
;             LAS float* scr = (LAS float*)(lds + RING_OFF + wave * 16640);   static_assert(8 * 16640 <= LDSCTL_OFF, "converter scratch below the LDS control words");
;             constexpr int I_UP = (D / 64) * (NUP / 64), I_DN = (DFF / 64) * (D / 64), I_IN = (D / 64) * (DINP / 64), I_GLU = 16 * 16, I_L = 4 * 16, I_V1 = 16 * 4, I_V2 = 4 * 16,
;                           I_BS5 = 16 * 32, I_BAT = 8 * 32, I_BRW = 16 * 32, I_OUT = 32 * 32;
;             constexpr int NITEMS = 2 * I_UP + 2 * I_DN + I_IN + I_GLU + 3 * I_L + I_V1 + I_V2 + I_BS5 + I_BAT + I_BRW + I_OUT;
;             const int lv = l > 0 ? l - 1 : 0;
;     ...
;             for (int it = gw; it < NITEMS; it += NGW) {
;                 ConvItem ca; CONV_DESC(ca, it);
;                 float va[64];
;                 conv_load(ca, lane, va);
;                 conv_store(ca, scr, lane, va);
.Lcvp130_ret:
.Lcvrs_p130:
	v_readlane_b32 s0, v254, 8
	v_readlane_b32 s4, v254, 10
	v_readlane_b32 s1, v254, 9
	v_mbcnt_lo_u32_b32 v11, -1, 0
	v_mbcnt_hi_u32_b32 v11, -1, v11
	s_load_dword s6, s[0:1], 0x0
	s_mov_b32 s3, s84
	s_waitcnt lgkmcnt(0)
	s_movk_i32 s6, 160
	s_lshl_b32 s3, s3, 3
	v_readlane_b32 s0, v254, 0
	s_add_i32 s3, s3, s4
	s_add_i32 s3, s3, 0x5f80
	v_readlane_b32 s1, v254, 1
	s_cmpk_gt_i32 s3, 27071
	s_cbranch_scc1 .Lcvp131_ret
	s_load_dwordx2 s[8:9], s[0:1], 0x138
	v_readlane_b32 s14, v254, 38
	s_nop 0
	s_add_i32 s14, s14, 1
	s_mulk_i32 s4, 0x4100
	s_add_i32 s7, s4, 0
	v_sub_u32_e64 v0, s14, 1 clamp
	s_lshl_b32 s33, s6, 3
	v_readfirstlane_b32 s4, v0
	s_lshl_b32 s96, s4, 16
	s_waitcnt lgkmcnt(0)
	s_add_u32 s4, s8, 0x22800000
	s_addc_u32 s5, s9, 0
	v_writelane_b32 v254, s4, 39
	s_mov_b32 s15, s97
	v_and_b32_e32 v0, 7, v11
	v_writelane_b32 v254, s5, 40
	s_add_u32 s4, s8, 0x22780000
	s_addc_u32 s5, s9, 0
	v_writelane_b32 v254, s4, 41
	v_ashrrev_i32_e32 v13, 3, v11
	v_lshlrev_b32_e32 v10, 3, v0
	v_writelane_b32 v254, s5, 42
	s_lshl_b32 s4, s14, 18
	s_add_u32 s10, s8, 0x22700000
	s_addc_u32 s11, s9, 0
	v_writelane_b32 v254, s10, 43
	s_mov_b32 s5, s97
	v_mul_u32_u24_e32 v0, 0x820, v0
	v_writelane_b32 v254, s11, 44
	s_mul_i32 s10, s14, 0x18000
	s_mov_b32 s11, s97
	v_writelane_b32 v254, s10, 45
	v_lshlrev_b32_e32 v1, 2, v13
	v_lshl_add_u32 v12, v11, 2, s7
	v_writelane_b32 v254, s11, 46
	s_add_u32 s10, s8, 0x22680000
	s_addc_u32 s11, s9, 0
	v_writelane_b32 v254, s10, 47
	v_add3_u32 v14, s7, v0, v1
	s_mov_b32 s41, s97
	v_writelane_b32 v254, s11, 48
	s_add_u32 s10, s8, 0x22600000
	s_addc_u32 s11, s9, 0
	v_writelane_b32 v254, s10, 49
	s_nop 1
	v_writelane_b32 v254, s11, 50
	s_lshl_b32 s10, s14, 20
	s_mov_b32 s11, s97
	v_writelane_b32 v254, s10, 51
	s_nop 1
	v_writelane_b32 v254, s11, 52
	s_add_u32 s10, s8, 0x22400000
	s_addc_u32 s11, s9, 0
	v_writelane_b32 v254, s10, 53
	s_nop 1
	v_writelane_b32 v254, s11, 54
	s_lshl_b32 s10, s14, 21
	s_mov_b32 s11, s97
	v_writelane_b32 v254, s10, 55
	s_nop 1
	v_writelane_b32 v254, s11, 56
	s_add_u32 s10, s8, 0x22e80000
	s_addc_u32 s11, s9, 0
	v_writelane_b32 v254, s10, 57
	s_nop 1
	v_writelane_b32 v254, s11, 58
	s_add_u32 s10, s8, 0x27b80000
	s_addc_u32 s11, s9, 0
	v_writelane_b32 v254, s10, 59
	s_nop 1
	v_writelane_b32 v254, s11, 60
	s_add_u32 s10, s8, 0x22880000
	s_addc_u32 s11, s9, 0
	v_writelane_b32 v254, s10, 61
	s_nop 1
	v_writelane_b32 v254, s11, 62
	s_lshl_b32 s10, s14, 22
	s_add_u32 s12, s8, 0x23280000
	s_addc_u32 s13, s9, 0
	v_writelane_b32 v254, s12, 63
	s_mov_b32 s11, s97
	s_nop 0
	v_writelane_b32 v255, s13, 0
	s_mul_i32 s12, s14, 0xac0000
	s_mov_b32 s13, s97
	v_writelane_b32 v255, s12, 1
	s_nop 1
	v_writelane_b32 v255, s13, 2
	s_add_u32 s12, s8, 0x26580000
	s_addc_u32 s13, s9, 0
	v_writelane_b32 v255, s12, 3
	s_nop 1
	v_writelane_b32 v255, s13, 4
	s_add_u32 s12, s8, 0x1d200000
	s_addc_u32 s13, s9, 0
	s_lshl_b32 s40, s14, 11
	v_writelane_b32 v255, s12, 5
	s_add_u32 s16, s8, 0x1e800000
	s_addc_u32 s17, s9, 0
	v_writelane_b32 v255, s13, 6
	v_writelane_b32 v255, s16, 7
	s_mul_i32 s12, s14, 0x1de0000
	s_mul_i32 s14, s14, 0x1580000
	v_writelane_b32 v255, s17, 8
	v_writelane_b32 v255, s14, 9
	s_mov_b32 s13, s97
	s_nop 0
	v_writelane_b32 v255, s15, 10
	s_add_u32 s14, s8, 0x23a80000
	s_addc_u32 s15, s9, 0
	v_writelane_b32 v255, s14, 11
	s_add_u32 s8, s8, 0x1a700000
	s_addc_u32 s9, s9, 0
	v_writelane_b32 v255, s15, 12
	v_writelane_b32 v255, s8, 13
	s_lshl_b64 s[4:5], s[4:5], 2
	s_lshl_b32 s7, s3, 4
	v_writelane_b32 v255, s9, 14
	v_writelane_b32 v255, s4, 15
	s_add_i32 s72, s7, 0xc00
	s_lshl_b32 s7, s3, 1
	v_writelane_b32 v255, s5, 16
	s_lshl_b64 s[4:5], s[10:11], 2
	v_writelane_b32 v255, s4, 17
	s_lshl_b32 s66, s3, 6
	s_lshl_b32 s67, s6, 9
	v_writelane_b32 v255, s5, 18
	s_lshl_b64 s[4:5], s[12:13], 2
	v_writelane_b32 v255, s4, 19
	s_lshl_b32 s68, s3, 5
	s_lshl_b32 s69, s6, 8
	v_writelane_b32 v255, s5, 20
	v_writelane_b32 v255, s80, 21
	s_lshl_b32 s70, s3, 2
	s_lshl_b32 s71, s6, 5
	v_writelane_b32 v255, s81, 22
	v_writelane_b32 v255, s82, 23
	s_lshl_b32 s73, s6, 7
	s_add_i32 s74, s7, 0x13500
	s_lshl_b32 s75, s6, 4
	v_writelane_b32 v255, s83, 24
	s_branch .Lcvp131_31
